# v13 + GEMM epilogues: xor-16/xor-32 steps of the sum-of-squares reductions by v_permlane16/32_swap instead of ds_bpermute (167 sites, bit-identical)
# speedup vs baseline: 1.0081x; 1.0081x over previous
.LBB0_251:
	s_and_b64 s[0:1], s[22:23], exec
	s_movk_i32 s0, 0x400
	s_cselect_b32 s11, 0x100, s0
	s_lshl_b64 s[0:1], s[2:3], 6
	v_readlane_b32 s2, v250, 7
	v_lshlrev_b32_e32 v99, 4, v99
	v_readlane_b32 s3, v250, 8
	s_add_u32 s0, s2, s0
	v_lshl_add_u32 v202, v98, 6, v99
	s_addc_u32 s1, s3, s1
	global_load_dwordx4 v[188:191], v202, s[0:1]
	global_load_dwordx4 v[170:173], v202, s[0:1] offset:1024
	global_load_dwordx4 v[166:169], v202, s[0:1] offset:2048
	global_load_dwordx4 v[146:149], v202, s[0:1] offset:3072
	v_lshlrev_b32_e32 v98, 1, v98
	v_lshl_add_u32 v192, v98, s9, v99
	v_lshl_add_u64 v[98:99], s[0:1], 0, v[202:203]
	s_movk_i32 s0, 0x2000
	v_add_co_u32_e32 v98, vcc, s0, v98
	v_and_b32_e32 v175, 64, v248
	s_nop 0
	v_addc_co_u32_e32 v99, vcc, 0, v99, vcc
	v_xor_b32_e32 v174, 16, v248
	v_add_u32_e32 v175, 64, v175
	v_cmp_lt_i32_e32 vcc, v174, v175
	s_mov_b32 s16, 0xf800000
	s_lshl_b32 s2, s64, 1
	v_cndmask_b32_e32 v174, v248, v174, vcc
	v_lshlrev_b32_e32 v185, 2, v174
	v_xor_b32_e32 v174, 32, v248
	v_cmp_lt_i32_e32 vcc, v174, v175
	s_add_u32 s22, s40, s2
	s_addc_u32 s23, s41, 0
	v_cndmask_b32_e32 v174, v248, v174, vcc
	v_lshlrev_b32_e32 v186, 2, v174
	v_mov_b32_e32 v193, v203
	v_lshl_add_u64 v[174:175], s[22:23], 0, v[192:193]
	global_load_dwordx4 v[142:145], v[98:99], off
	global_load_dwordx4 v[138:141], v[98:99], off offset:1024
	global_load_dwordx4 v[118:121], v[98:99], off offset:2048
	s_nop 0
	global_load_dwordx4 v[98:101], v[98:99], off offset:3072
	s_lshl_b32 s24, s11, 5
	s_mov_b32 s15, 0xf800000
	s_waitcnt vmcnt(7)
	v_mov_b32_e32 v194, v189
	v_mov_b32_e32 v195, v190
	v_mov_b32_e32 v189, v191
	v_pk_add_f32 v[188:189], v[194:195], v[188:189]
	s_nop 0
	v_add_f32_e32 v187, v188, v189
	v_mov_b32_e32 v188, v187
	s_nop 1
	v_permlane16_swap_b32_e32 v187, v188
	s_waitcnt lgkmcnt(0)
	v_add_f32_e32 v187, v187, v188
	v_mov_b32_e32 v188, v187
	s_nop 1
	v_permlane32_swap_b32_e32 v187, v188
	s_waitcnt lgkmcnt(0)
	v_add_f32_e32 v187, v187, v188
	v_fmamk_f32 v187, v187, 0x3a800000, v204
	v_cmp_gt_f32_e32 vcc, s16, v187
	v_mul_f32_e32 v188, 0x4f800000, v187
	s_nop 0
	v_cndmask_b32_e32 v187, v187, v188, vcc
	v_sqrt_f32_e32 v188, v187
	s_nop 0
	v_add_u32_e32 v189, -1, v188
	v_fma_f32 v190, -v189, v188, v187
	v_cmp_ge_f32_e64 s[2:3], 0, v190
	v_add_u32_e32 v190, 1, v188
	s_nop 0
	v_cndmask_b32_e64 v189, v188, v189, s[2:3]
	v_fma_f32 v188, -v190, v188, v187
	v_cmp_lt_f32_e64 s[2:3], 0, v188
	s_nop 1
	v_cndmask_b32_e64 v188, v189, v190, s[2:3]
	v_mul_f32_e32 v189, 0x37800000, v188
	v_cndmask_b32_e32 v188, v188, v189, vcc
	v_cmp_class_f32_e32 vcc, v187, v205
	s_nop 1
	v_cndmask_b32_e32 v187, v188, v187, vcc
	v_div_scale_f32 v188, s[0:1], v187, v187, 1.0
	v_rcp_f32_e32 v189, v188
	s_nop 0
	v_fma_f32 v190, -v188, v189, 1.0
	v_fmac_f32_e32 v189, v190, v189
	v_div_scale_f32 v190, vcc, 1.0, v187, 1.0
	v_mul_f32_e32 v191, v190, v189
	v_fma_f32 v193, -v188, v191, v190
	v_fmac_f32_e32 v191, v193, v189
	v_fma_f32 v188, -v188, v191, v190
	v_div_fmas_f32 v188, v188, v189, v191
	v_div_fixup_f32 v188, v188, v187, 1.0
	v_pk_fma_f32 v[164:165], v[164:165], v[188:189], v[80:81] op_sel_hi:[1,0,1]
	v_pk_fma_f32 v[162:163], v[162:163], v[188:189], v[78:79] op_sel_hi:[1,0,1]
	v_pk_fma_f32 v[190:191], v[160:161], v[188:189], v[76:77] op_sel_hi:[1,0,1]
	v_pk_fma_f32 v[160:161], v[158:159], v[188:189], v[74:75] op_sel_hi:[1,0,1]
	v_cvt_pk_bf16_f32 v158, v162, v163
	v_cvt_pk_bf16_f32 v159, v164, v165
	v_pk_fma_f32 v[156:157], v[156:157], v[188:189], v[72:73] op_sel_hi:[1,0,1]
	v_cvt_pk_bf16_f32 v160, v160, v161
	v_cvt_pk_bf16_f32 v161, v190, v191
	global_store_dwordx4 v192, v[158:161], s[22:23]
	v_pk_fma_f32 v[154:155], v[154:155], v[188:189], v[70:71] op_sel_hi:[1,0,1]
	s_nop 0
	v_pk_fma_f32 v[158:159], v[152:153], v[188:189], v[68:69] op_sel_hi:[1,0,1]
	v_pk_fma_f32 v[152:153], v[150:151], v[188:189], v[66:67] op_sel_hi:[1,0,1]
	v_cvt_pk_bf16_f32 v150, v154, v155
	v_cvt_pk_bf16_f32 v151, v156, v157
	s_nop 0
	v_cvt_pk_bf16_f32 v152, v152, v153
	v_cvt_pk_bf16_f32 v153, v158, v159
	global_store_dwordx4 v192, v[150:153], s[22:23] offset:256
	s_waitcnt vmcnt(8)
	s_nop 0
	v_mov_b32_e32 v150, v171
	v_mov_b32_e32 v151, v172
	v_mov_b32_e32 v171, v173
	v_pk_add_f32 v[150:151], v[150:151], v[170:171]
	s_nop 0
	v_add_f32_e32 v150, v150, v151
	v_mov_b32_e32 v151, v150
	s_nop 1
	v_permlane16_swap_b32_e32 v150, v151
	s_waitcnt lgkmcnt(0)
	v_add_f32_e32 v150, v150, v151
	v_mov_b32_e32 v151, v150
	s_nop 1
	v_permlane32_swap_b32_e32 v150, v151
	s_waitcnt lgkmcnt(0)
	v_add_f32_e32 v150, v150, v151
	v_fmamk_f32 v150, v150, 0x3a800000, v204
	v_cmp_gt_f32_e32 vcc, s16, v150
	v_mul_f32_e32 v151, 0x4f800000, v150
	s_nop 0
	v_cndmask_b32_e32 v150, v150, v151, vcc
	v_sqrt_f32_e32 v151, v150
	s_nop 0
	v_add_u32_e32 v152, -1, v151
	v_fma_f32 v153, -v152, v151, v150
	v_cmp_ge_f32_e64 s[2:3], 0, v153
	v_add_u32_e32 v153, 1, v151
	s_nop 0
	v_cndmask_b32_e64 v152, v151, v152, s[2:3]
	v_fma_f32 v151, -v153, v151, v150
	v_cmp_lt_f32_e64 s[2:3], 0, v151
	s_nop 1
	v_cndmask_b32_e64 v151, v152, v153, s[2:3]
	v_mul_f32_e32 v152, 0x37800000, v151
	v_cndmask_b32_e32 v151, v151, v152, vcc
	v_cmp_class_f32_e32 vcc, v150, v205
	s_nop 1
	v_cndmask_b32_e32 v150, v151, v150, vcc
	v_div_scale_f32 v151, s[0:1], v150, v150, 1.0
	v_rcp_f32_e32 v152, v151
	s_nop 0
	v_fma_f32 v153, -v151, v152, 1.0
	v_fmac_f32_e32 v152, v153, v152
	v_div_scale_f32 v153, vcc, 1.0, v150, 1.0
	v_mul_f32_e32 v154, v153, v152
	v_fma_f32 v155, -v151, v154, v153
	v_fmac_f32_e32 v154, v155, v152
	v_fma_f32 v151, -v151, v154, v153
	v_div_fmas_f32 v151, v151, v152, v154
	v_div_fixup_f32 v150, v151, v150, 1.0
	v_lshl_add_u64 v[152:153], v[174:175], 0, s[24:25]
	v_pk_fma_f32 v[136:137], v[136:137], v[150:151], v[80:81] op_sel_hi:[1,0,1]
	v_pk_fma_f32 v[134:135], v[134:135], v[150:151], v[78:79] op_sel_hi:[1,0,1]
	v_pk_fma_f32 v[154:155], v[132:133], v[150:151], v[76:77] op_sel_hi:[1,0,1]
	v_pk_fma_f32 v[132:133], v[130:131], v[150:151], v[74:75] op_sel_hi:[1,0,1]
	v_cvt_pk_bf16_f32 v130, v134, v135
	v_cvt_pk_bf16_f32 v131, v136, v137
	v_pk_fma_f32 v[128:129], v[128:129], v[150:151], v[72:73] op_sel_hi:[1,0,1]
	v_cvt_pk_bf16_f32 v132, v132, v133
	v_cvt_pk_bf16_f32 v133, v154, v155
	global_store_dwordx4 v[152:153], v[130:133], off
	v_pk_fma_f32 v[126:127], v[126:127], v[150:151], v[70:71] op_sel_hi:[1,0,1]
	s_lshl_b32 s24, s11, 6
	v_pk_fma_f32 v[130:131], v[124:125], v[150:151], v[68:69] op_sel_hi:[1,0,1]
	v_pk_fma_f32 v[124:125], v[122:123], v[150:151], v[66:67] op_sel_hi:[1,0,1]
	v_cvt_pk_bf16_f32 v122, v126, v127
	v_cvt_pk_bf16_f32 v123, v128, v129
	s_nop 0
	v_cvt_pk_bf16_f32 v124, v124, v125
	v_cvt_pk_bf16_f32 v125, v130, v131
	global_store_dwordx4 v[152:153], v[122:125], off offset:256
	s_waitcnt vmcnt(9)
	s_nop 0
	v_mov_b32_e32 v122, v167
	v_mov_b32_e32 v123, v168
	v_mov_b32_e32 v167, v169
	v_pk_add_f32 v[122:123], v[122:123], v[166:167]
	s_nop 0
	v_add_f32_e32 v122, v122, v123
	v_mov_b32_e32 v123, v122
	s_nop 1
	v_permlane16_swap_b32_e32 v122, v123
	s_waitcnt lgkmcnt(0)
	v_add_f32_e32 v122, v122, v123
	v_mov_b32_e32 v123, v122
	s_nop 1
	v_permlane32_swap_b32_e32 v122, v123
	s_waitcnt lgkmcnt(0)
	v_add_f32_e32 v122, v122, v123
	v_fmamk_f32 v122, v122, 0x3a800000, v204
	v_cmp_gt_f32_e32 vcc, s16, v122
	v_mul_f32_e32 v123, 0x4f800000, v122
	s_nop 0
	v_cndmask_b32_e32 v122, v122, v123, vcc
	v_sqrt_f32_e32 v123, v122
	s_nop 0
	v_add_u32_e32 v124, -1, v123
	v_fma_f32 v125, -v124, v123, v122
	v_cmp_ge_f32_e64 s[2:3], 0, v125
	v_add_u32_e32 v125, 1, v123
	s_nop 0
	v_cndmask_b32_e64 v124, v123, v124, s[2:3]
	v_fma_f32 v123, -v125, v123, v122
	v_cmp_lt_f32_e64 s[2:3], 0, v123
	s_nop 1
	v_cndmask_b32_e64 v123, v124, v125, s[2:3]
	v_mul_f32_e32 v124, 0x37800000, v123
	v_cndmask_b32_e32 v123, v123, v124, vcc
	v_cmp_class_f32_e32 vcc, v122, v205
	s_nop 1
	v_cndmask_b32_e32 v122, v123, v122, vcc
	v_div_scale_f32 v123, s[0:1], v122, v122, 1.0
	v_rcp_f32_e32 v124, v123
	s_nop 0
	v_fma_f32 v125, -v123, v124, 1.0
	v_fmac_f32_e32 v124, v125, v124
	v_div_scale_f32 v125, vcc, 1.0, v122, 1.0
	v_mul_f32_e32 v126, v125, v124
	v_fma_f32 v127, -v123, v126, v125
	v_fmac_f32_e32 v126, v127, v124
	v_fma_f32 v123, -v123, v126, v125
	v_div_fmas_f32 v123, v123, v124, v126
	v_div_fixup_f32 v122, v123, v122, 1.0
	v_lshl_add_u64 v[124:125], v[174:175], 0, s[24:25]
	v_pk_fma_f32 v[116:117], v[116:117], v[122:123], v[80:81] op_sel_hi:[1,0,1]
	v_pk_fma_f32 v[114:115], v[114:115], v[122:123], v[78:79] op_sel_hi:[1,0,1]
	v_pk_fma_f32 v[126:127], v[112:113], v[122:123], v[76:77] op_sel_hi:[1,0,1]
	v_pk_fma_f32 v[112:113], v[110:111], v[122:123], v[74:75] op_sel_hi:[1,0,1]
	v_cvt_pk_bf16_f32 v110, v114, v115
	v_cvt_pk_bf16_f32 v111, v116, v117
	v_pk_fma_f32 v[108:109], v[108:109], v[122:123], v[72:73] op_sel_hi:[1,0,1]
	v_cvt_pk_bf16_f32 v112, v112, v113
	v_cvt_pk_bf16_f32 v113, v126, v127
	global_store_dwordx4 v[124:125], v[110:113], off
	v_pk_fma_f32 v[106:107], v[106:107], v[122:123], v[70:71] op_sel_hi:[1,0,1]
	s_lshl_b32 s24, 0x60, s9
	v_pk_fma_f32 v[110:111], v[104:105], v[122:123], v[68:69] op_sel_hi:[1,0,1]
	v_pk_fma_f32 v[104:105], v[102:103], v[122:123], v[66:67] op_sel_hi:[1,0,1]
	v_cvt_pk_bf16_f32 v102, v106, v107
	v_cvt_pk_bf16_f32 v103, v108, v109
	s_nop 0
	v_cvt_pk_bf16_f32 v104, v104, v105
	v_cvt_pk_bf16_f32 v105, v110, v111
	global_store_dwordx4 v[124:125], v[102:105], off offset:256
	s_waitcnt vmcnt(10)
	s_nop 0
	v_mov_b32_e32 v102, v147
	v_mov_b32_e32 v103, v148
	v_mov_b32_e32 v147, v149
	v_pk_add_f32 v[102:103], v[102:103], v[146:147]
	s_nop 0
	v_add_f32_e32 v102, v102, v103
	v_mov_b32_e32 v103, v102
	s_nop 1
	v_permlane16_swap_b32_e32 v102, v103
	s_waitcnt lgkmcnt(0)
	v_add_f32_e32 v102, v102, v103
	v_mov_b32_e32 v103, v102
	s_nop 1
	v_permlane32_swap_b32_e32 v102, v103
	s_waitcnt lgkmcnt(0)
	v_add_f32_e32 v102, v102, v103
	v_fmamk_f32 v102, v102, 0x3a800000, v204
	v_cmp_gt_f32_e32 vcc, s16, v102
	v_mul_f32_e32 v103, 0x4f800000, v102
	s_nop 0
	v_cndmask_b32_e32 v102, v102, v103, vcc
	v_sqrt_f32_e32 v103, v102
	s_nop 0
	v_add_u32_e32 v104, -1, v103
	v_fma_f32 v105, -v104, v103, v102
	v_cmp_ge_f32_e64 s[2:3], 0, v105
	v_add_u32_e32 v105, 1, v103
	s_nop 0
	v_cndmask_b32_e64 v104, v103, v104, s[2:3]
	v_fma_f32 v103, -v105, v103, v102
	v_cmp_lt_f32_e64 s[2:3], 0, v103
	s_nop 1
	v_cndmask_b32_e64 v103, v104, v105, s[2:3]
	v_mul_f32_e32 v104, 0x37800000, v103
	v_cndmask_b32_e32 v103, v103, v104, vcc
	v_cmp_class_f32_e32 vcc, v102, v205
	s_nop 1
	v_cndmask_b32_e32 v102, v103, v102, vcc
	v_div_scale_f32 v103, s[0:1], v102, v102, 1.0
	v_rcp_f32_e32 v104, v103
	s_nop 0
	v_fma_f32 v105, -v103, v104, 1.0
	v_fmac_f32_e32 v104, v105, v104
	v_div_scale_f32 v105, vcc, 1.0, v102, 1.0
	v_mul_f32_e32 v106, v105, v104
	v_fma_f32 v107, -v103, v106, v105
	v_fmac_f32_e32 v106, v107, v104
	v_fma_f32 v103, -v103, v106, v105
	v_div_fmas_f32 v103, v103, v104, v106
	v_div_fixup_f32 v102, v103, v102, 1.0
	v_lshl_add_u64 v[104:105], v[174:175], 0, s[24:25]
	v_pk_fma_f32 v[96:97], v[96:97], v[102:103], v[80:81] op_sel_hi:[1,0,1]
	v_pk_fma_f32 v[94:95], v[94:95], v[102:103], v[78:79] op_sel_hi:[1,0,1]
	v_pk_fma_f32 v[106:107], v[92:93], v[102:103], v[76:77] op_sel_hi:[1,0,1]
	v_pk_fma_f32 v[92:93], v[90:91], v[102:103], v[74:75] op_sel_hi:[1,0,1]
	v_cvt_pk_bf16_f32 v90, v94, v95
	v_cvt_pk_bf16_f32 v91, v96, v97
	v_pk_fma_f32 v[88:89], v[88:89], v[102:103], v[72:73] op_sel_hi:[1,0,1]
	v_cvt_pk_bf16_f32 v92, v92, v93
	v_cvt_pk_bf16_f32 v93, v106, v107
	global_store_dwordx4 v[104:105], v[90:93], off
	v_pk_fma_f32 v[86:87], v[86:87], v[102:103], v[70:71] op_sel_hi:[1,0,1]
	s_lshl_b32 s24, s11, 8
	v_pk_fma_f32 v[90:91], v[84:85], v[102:103], v[68:69] op_sel_hi:[1,0,1]
	v_pk_fma_f32 v[84:85], v[82:83], v[102:103], v[66:67] op_sel_hi:[1,0,1]
	v_cvt_pk_bf16_f32 v82, v86, v87
	v_cvt_pk_bf16_f32 v83, v88, v89
	s_nop 0
	v_cvt_pk_bf16_f32 v84, v84, v85
	v_cvt_pk_bf16_f32 v85, v90, v91
	global_store_dwordx4 v[104:105], v[82:85], off offset:256
	s_waitcnt vmcnt(11)
	s_nop 0
	v_mov_b32_e32 v82, v143
	v_mov_b32_e32 v83, v144
	v_mov_b32_e32 v143, v145
	v_pk_add_f32 v[82:83], v[82:83], v[142:143]
	s_nop 0
	v_add_f32_e32 v82, v82, v83
	v_mov_b32_e32 v83, v82
	s_nop 1
	v_permlane16_swap_b32_e32 v82, v83
	s_waitcnt lgkmcnt(0)
	v_add_f32_e32 v82, v82, v83
	v_mov_b32_e32 v83, v82
	s_nop 1
	v_permlane32_swap_b32_e32 v82, v83
	s_waitcnt lgkmcnt(0)
	v_add_f32_e32 v82, v82, v83
	v_fmamk_f32 v82, v82, 0x3a800000, v204
	v_cmp_gt_f32_e32 vcc, s16, v82
	v_mul_f32_e32 v83, 0x4f800000, v82
	s_nop 0
	v_cndmask_b32_e32 v82, v82, v83, vcc
	v_sqrt_f32_e32 v83, v82
	s_nop 0
	v_add_u32_e32 v84, -1, v83
	v_fma_f32 v85, -v84, v83, v82
	v_cmp_ge_f32_e64 s[2:3], 0, v85
	v_add_u32_e32 v85, 1, v83
	s_nop 0
	v_cndmask_b32_e64 v84, v83, v84, s[2:3]
	v_fma_f32 v83, -v85, v83, v82
	v_cmp_lt_f32_e64 s[2:3], 0, v83
	s_nop 1
	v_cndmask_b32_e64 v83, v84, v85, s[2:3]
	v_mul_f32_e32 v84, 0x37800000, v83
	v_cndmask_b32_e32 v83, v83, v84, vcc
	v_cmp_class_f32_e32 vcc, v82, v205
	s_nop 1
	v_cndmask_b32_e32 v82, v83, v82, vcc
	v_div_scale_f32 v83, s[0:1], v82, v82, 1.0
	v_rcp_f32_e32 v84, v83
	s_nop 0
	v_fma_f32 v85, -v83, v84, 1.0
	v_fmac_f32_e32 v84, v85, v84
	v_div_scale_f32 v85, vcc, 1.0, v82, 1.0
	v_mul_f32_e32 v86, v85, v84
	v_fma_f32 v87, -v83, v86, v85
	v_fmac_f32_e32 v86, v87, v84
	v_fma_f32 v83, -v83, v86, v85
	v_div_fmas_f32 v83, v83, v84, v86
	v_div_fixup_f32 v82, v83, v82, 1.0
	v_lshl_add_u64 v[84:85], v[174:175], 0, s[24:25]
	v_pk_fma_f32 v[56:57], v[56:57], v[82:83], v[80:81] op_sel_hi:[1,0,1]
	v_pk_fma_f32 v[54:55], v[54:55], v[82:83], v[78:79] op_sel_hi:[1,0,1]
	v_pk_fma_f32 v[86:87], v[52:53], v[82:83], v[76:77] op_sel_hi:[1,0,1]
	v_pk_fma_f32 v[52:53], v[50:51], v[82:83], v[74:75] op_sel_hi:[1,0,1]
	v_cvt_pk_bf16_f32 v50, v54, v55
	v_cvt_pk_bf16_f32 v51, v56, v57
	v_pk_fma_f32 v[54:55], v[64:65], v[82:83], v[68:69] op_sel_hi:[1,0,1]
	v_cvt_pk_bf16_f32 v52, v52, v53
	v_cvt_pk_bf16_f32 v53, v86, v87
	global_store_dwordx4 v[84:85], v[50:53], off
	v_pk_fma_f32 v[56:57], v[62:63], v[82:83], v[66:67] op_sel_hi:[1,0,1]
	s_lshl_b32 s24, 0x120, s9
	v_pk_fma_f32 v[50:51], v[58:59], v[82:83], v[70:71] op_sel_hi:[1,0,1]
	v_pk_fma_f32 v[52:53], v[60:61], v[82:83], v[72:73] op_sel_hi:[1,0,1]
	v_cvt_pk_bf16_f32 v50, v50, v51
	s_nop 0
	v_cvt_pk_bf16_f32 v51, v52, v53
	v_cvt_pk_bf16_f32 v52, v56, v57
	v_cvt_pk_bf16_f32 v53, v54, v55
	global_store_dwordx4 v[84:85], v[50:53], off offset:256
	s_waitcnt vmcnt(12)
	s_nop 0
	v_mov_b32_e32 v50, v139
	v_mov_b32_e32 v51, v140
	v_mov_b32_e32 v139, v141
	v_pk_add_f32 v[50:51], v[50:51], v[138:139]
	s_nop 0
	v_add_f32_e32 v50, v50, v51
	v_mov_b32_e32 v51, v50
	s_nop 1
	v_permlane16_swap_b32_e32 v50, v51
	s_waitcnt lgkmcnt(0)
	v_add_f32_e32 v50, v50, v51
	v_mov_b32_e32 v51, v50
	s_nop 1
	v_permlane32_swap_b32_e32 v50, v51
	s_waitcnt lgkmcnt(0)
	v_add_f32_e32 v50, v50, v51
	v_fmamk_f32 v50, v50, 0x3a800000, v204
	v_cmp_gt_f32_e32 vcc, s16, v50
	v_mul_f32_e32 v51, 0x4f800000, v50
	s_nop 0
	v_cndmask_b32_e32 v50, v50, v51, vcc
	v_sqrt_f32_e32 v51, v50
	s_nop 0
	v_add_u32_e32 v52, -1, v51
	v_fma_f32 v53, -v52, v51, v50
	v_cmp_ge_f32_e64 s[2:3], 0, v53
	v_add_u32_e32 v53, 1, v51
	s_nop 0
	v_cndmask_b32_e64 v52, v51, v52, s[2:3]
	v_fma_f32 v51, -v53, v51, v50
	v_cmp_lt_f32_e64 s[2:3], 0, v51
	s_nop 1
	v_cndmask_b32_e64 v51, v52, v53, s[2:3]
	v_mul_f32_e32 v52, 0x37800000, v51
	v_cndmask_b32_e32 v51, v51, v52, vcc
	v_cmp_class_f32_e32 vcc, v50, v205
	s_nop 1
	v_cndmask_b32_e32 v50, v51, v50, vcc
	v_div_scale_f32 v51, s[0:1], v50, v50, 1.0
	v_rcp_f32_e32 v52, v51
	s_nop 0
	v_fma_f32 v53, -v51, v52, 1.0
	v_fmac_f32_e32 v52, v53, v52
	v_div_scale_f32 v53, vcc, 1.0, v50, 1.0
	v_mul_f32_e32 v54, v53, v52
	v_fma_f32 v55, -v51, v54, v53
	v_fmac_f32_e32 v54, v55, v52
	v_fma_f32 v51, -v51, v54, v53
	v_div_fmas_f32 v51, v51, v52, v54
	v_div_fixup_f32 v50, v51, v50, 1.0
	v_lshl_add_u64 v[52:53], v[174:175], 0, s[24:25]
	v_pk_fma_f32 v[40:41], v[40:41], v[50:51], v[80:81] op_sel_hi:[1,0,1]
	v_pk_fma_f32 v[38:39], v[38:39], v[50:51], v[78:79] op_sel_hi:[1,0,1]
	v_pk_fma_f32 v[54:55], v[36:37], v[50:51], v[76:77] op_sel_hi:[1,0,1]
	v_pk_fma_f32 v[36:37], v[34:35], v[50:51], v[74:75] op_sel_hi:[1,0,1]
	v_cvt_pk_bf16_f32 v34, v38, v39
	v_cvt_pk_bf16_f32 v35, v40, v41
	v_pk_fma_f32 v[38:39], v[48:49], v[50:51], v[68:69] op_sel_hi:[1,0,1]
	v_cvt_pk_bf16_f32 v36, v36, v37
	v_cvt_pk_bf16_f32 v37, v54, v55
	global_store_dwordx4 v[52:53], v[34:37], off
	v_pk_fma_f32 v[40:41], v[46:47], v[50:51], v[66:67] op_sel_hi:[1,0,1]
	s_lshl_b32 s24, 0x140, s9
	v_pk_fma_f32 v[34:35], v[42:43], v[50:51], v[70:71] op_sel_hi:[1,0,1]
	v_pk_fma_f32 v[36:37], v[44:45], v[50:51], v[72:73] op_sel_hi:[1,0,1]
	v_cvt_pk_bf16_f32 v34, v34, v35
	s_nop 0
	v_cvt_pk_bf16_f32 v35, v36, v37
	v_cvt_pk_bf16_f32 v36, v40, v41
	v_cvt_pk_bf16_f32 v37, v38, v39
	global_store_dwordx4 v[52:53], v[34:37], off offset:256
	s_waitcnt vmcnt(13)
	s_nop 0
	v_mov_b32_e32 v34, v119
	v_mov_b32_e32 v35, v120
	v_mov_b32_e32 v119, v121
	v_pk_add_f32 v[34:35], v[34:35], v[118:119]
	s_nop 0
	v_add_f32_e32 v34, v34, v35
	v_mov_b32_e32 v35, v34
	s_nop 1
	v_permlane16_swap_b32_e32 v34, v35
	s_waitcnt lgkmcnt(0)
	v_add_f32_e32 v34, v34, v35
	v_mov_b32_e32 v35, v34
	s_nop 1
	v_permlane32_swap_b32_e32 v34, v35
	s_waitcnt lgkmcnt(0)
	v_add_f32_e32 v34, v34, v35
	v_fmamk_f32 v34, v34, 0x3a800000, v204
	v_cmp_gt_f32_e32 vcc, s16, v34
	v_mul_f32_e32 v35, 0x4f800000, v34
	s_nop 0
	v_cndmask_b32_e32 v34, v34, v35, vcc
	v_sqrt_f32_e32 v35, v34
	s_nop 0
	v_add_u32_e32 v36, -1, v35
	v_fma_f32 v37, -v36, v35, v34
	v_cmp_ge_f32_e64 s[2:3], 0, v37
	v_add_u32_e32 v37, 1, v35
	s_nop 0
	v_cndmask_b32_e64 v36, v35, v36, s[2:3]
	v_fma_f32 v35, -v37, v35, v34
	v_cmp_lt_f32_e64 s[2:3], 0, v35
	s_nop 1
	v_cndmask_b32_e64 v35, v36, v37, s[2:3]
	v_mul_f32_e32 v36, 0x37800000, v35
	v_cndmask_b32_e32 v35, v35, v36, vcc
	v_cmp_class_f32_e32 vcc, v34, v205
	s_nop 1
	v_cndmask_b32_e32 v34, v35, v34, vcc
	v_div_scale_f32 v35, s[0:1], v34, v34, 1.0
	v_rcp_f32_e32 v36, v35
	s_nop 0
	v_fma_f32 v37, -v35, v36, 1.0
	v_fmac_f32_e32 v36, v37, v36
	v_div_scale_f32 v37, vcc, 1.0, v34, 1.0
	v_mul_f32_e32 v38, v37, v36
	v_fma_f32 v39, -v35, v38, v37
	v_fmac_f32_e32 v38, v39, v36
	v_fma_f32 v35, -v35, v38, v37
	v_div_fmas_f32 v35, v35, v36, v38
	v_div_fixup_f32 v34, v35, v34, 1.0
	v_lshl_add_u64 v[36:37], v[174:175], 0, s[24:25]
	v_pk_fma_f32 v[24:25], v[24:25], v[34:35], v[80:81] op_sel_hi:[1,0,1]
	v_pk_fma_f32 v[22:23], v[22:23], v[34:35], v[78:79] op_sel_hi:[1,0,1]
	v_pk_fma_f32 v[38:39], v[20:21], v[34:35], v[76:77] op_sel_hi:[1,0,1]
	v_pk_fma_f32 v[20:21], v[18:19], v[34:35], v[74:75] op_sel_hi:[1,0,1]
	v_cvt_pk_bf16_f32 v18, v22, v23
	v_cvt_pk_bf16_f32 v19, v24, v25
	v_pk_fma_f32 v[22:23], v[32:33], v[34:35], v[68:69] op_sel_hi:[1,0,1]
	v_cvt_pk_bf16_f32 v20, v20, v21
	v_cvt_pk_bf16_f32 v21, v38, v39
	global_store_dwordx4 v[36:37], v[18:21], off
	v_pk_fma_f32 v[24:25], v[30:31], v[34:35], v[66:67] op_sel_hi:[1,0,1]
	s_lshl_b32 s24, 0x160, s9
	v_pk_fma_f32 v[18:19], v[26:27], v[34:35], v[70:71] op_sel_hi:[1,0,1]
	v_pk_fma_f32 v[20:21], v[28:29], v[34:35], v[72:73] op_sel_hi:[1,0,1]
	v_cvt_pk_bf16_f32 v18, v18, v19
	s_nop 0
	v_cvt_pk_bf16_f32 v19, v20, v21
	v_cvt_pk_bf16_f32 v20, v24, v25
	v_cvt_pk_bf16_f32 v21, v22, v23
	global_store_dwordx4 v[36:37], v[18:21], off offset:256
	s_waitcnt vmcnt(14)
	s_nop 0
	v_mov_b32_e32 v18, v99
	v_mov_b32_e32 v19, v100
	v_mov_b32_e32 v99, v101
	v_pk_add_f32 v[18:19], v[18:19], v[98:99]
	s_nop 0
	v_add_f32_e32 v18, v18, v19
	v_mov_b32_e32 v19, v18
	s_nop 1
	v_permlane16_swap_b32_e32 v18, v19
	s_waitcnt lgkmcnt(0)
	v_add_f32_e32 v18, v18, v19
	v_mov_b32_e32 v19, v18
	s_nop 1
	v_permlane32_swap_b32_e32 v18, v19
	s_waitcnt lgkmcnt(0)
	v_add_f32_e32 v18, v18, v19
	v_fmamk_f32 v18, v18, 0x3a800000, v204
	v_cmp_gt_f32_e32 vcc, s16, v18
	v_mul_f32_e32 v19, 0x4f800000, v18
	s_nop 0
	v_cndmask_b32_e32 v18, v18, v19, vcc
	v_sqrt_f32_e32 v19, v18
	s_nop 0
	v_add_u32_e32 v20, -1, v19
	v_fma_f32 v21, -v20, v19, v18
	v_cmp_ge_f32_e64 s[2:3], 0, v21
	v_add_u32_e32 v21, 1, v19
	s_nop 0
	v_cndmask_b32_e64 v20, v19, v20, s[2:3]
	v_fma_f32 v19, -v21, v19, v18
	v_cmp_lt_f32_e64 s[2:3], 0, v19
	s_nop 1
	v_cndmask_b32_e64 v19, v20, v21, s[2:3]
	v_mul_f32_e32 v20, 0x37800000, v19
	v_cndmask_b32_e32 v19, v19, v20, vcc
	v_cmp_class_f32_e32 vcc, v18, v205
	s_mov_b64 s[2:3], -1
	s_nop 0
	v_cndmask_b32_e32 v18, v19, v18, vcc
	v_div_scale_f32 v19, s[0:1], v18, v18, 1.0
	v_rcp_f32_e32 v20, v19
	s_nop 0
	v_fma_f32 v21, -v19, v20, 1.0
	v_fmac_f32_e32 v20, v21, v20
	v_div_scale_f32 v21, vcc, 1.0, v18, 1.0
	v_mul_f32_e32 v22, v21, v20
	v_fma_f32 v23, -v19, v22, v21
	v_fmac_f32_e32 v22, v23, v20
	v_fma_f32 v19, -v19, v22, v21
	v_div_fmas_f32 v19, v19, v20, v22
	v_div_fixup_f32 v18, v19, v18, 1.0
	v_pk_fma_f32 v[22:23], v[4:5], v[18:19], v[76:77] op_sel_hi:[1,0,1]
	v_pk_fma_f32 v[4:5], v[2:3], v[18:19], v[74:75] op_sel_hi:[1,0,1]
	v_lshl_add_u64 v[20:21], v[174:175], 0, s[24:25]
	v_pk_fma_f32 v[8:9], v[8:9], v[18:19], v[80:81] op_sel_hi:[1,0,1]
	v_pk_fma_f32 v[6:7], v[6:7], v[18:19], v[78:79] op_sel_hi:[1,0,1]
	s_and_b64 vcc, exec, s[38:39]
	v_cvt_pk_bf16_f32 v2, v6, v7
	v_cvt_pk_bf16_f32 v3, v8, v9
	v_cvt_pk_bf16_f32 v4, v4, v5
	v_cvt_pk_bf16_f32 v5, v22, v23
	global_store_dwordx4 v[20:21], v[2:5], off
	v_pk_fma_f32 v[6:7], v[16:17], v[18:19], v[68:69] op_sel_hi:[1,0,1]
	v_pk_fma_f32 v[8:9], v[14:15], v[18:19], v[66:67] op_sel_hi:[1,0,1]
	v_pk_fma_f32 v[4:5], v[12:13], v[18:19], v[72:73] op_sel_hi:[1,0,1]
	v_pk_fma_f32 v[2:3], v[10:11], v[18:19], v[70:71] op_sel_hi:[1,0,1]
	s_nop 0
	v_cvt_pk_bf16_f32 v2, v2, v3
	v_cvt_pk_bf16_f32 v3, v4, v5
	v_cvt_pk_bf16_f32 v4, v8, v9
	v_cvt_pk_bf16_f32 v5, v6, v7
	global_store_dwordx4 v[20:21], v[2:5], off offset:256
	s_cbranch_vccnz .LBB0_238
	s_andn2_b64 vcc, exec, s[4:5]
	s_cbranch_vccnz .LBB0_237
	s_barrier
	s_branch .LBB0_237

.LBB0_459:
	v_mul_f32_e32 v101, v101, v101
	v_mul_f32_e32 v99, v99, v99
	v_fmac_f32_e32 v101, v100, v100
	v_fmac_f32_e32 v99, v98, v98
	v_mul_f32_e32 v117, v117, v117
	v_mul_f32_e32 v115, v115, v115
	v_add_f32_e32 v98, v101, v99
	v_mul_f32_e32 v99, v105, v105
	v_mul_f32_e32 v100, v103, v103
	v_fmac_f32_e32 v117, v116, v116
	v_fmac_f32_e32 v115, v114, v114
	v_fmac_f32_e32 v99, v104, v104
	v_fmac_f32_e32 v100, v102, v102
	v_add_f32_e32 v114, v117, v115
	v_mul_f32_e32 v115, v121, v121
	v_mul_f32_e32 v116, v119, v119
	v_add_f32_e32 v99, v99, v100
	v_and_b32_e32 v100, 64, v248
	v_fmac_f32_e32 v115, v120, v120
	v_fmac_f32_e32 v116, v118, v118
	v_add_f32_e32 v98, v98, v99
	v_xor_b32_e32 v99, 16, v248
	v_add_u32_e32 v101, 64, v100
	v_add_f32_e32 v115, v115, v116
	v_cmp_lt_i32_e32 vcc, v99, v101
	v_add_f32_e32 v114, v114, v115
	v_add_f32_e32 v98, v114, v98
	v_cndmask_b32_e32 v99, v248, v99, vcc
	v_lshlrev_b32_e32 v118, 2, v99
	v_mov_b32_e32 v99, v98
	s_nop 1
	v_permlane16_swap_b32_e32 v98, v99
	s_lshl_b64 s[0:1], s[22:23], 6
	v_readlane_b32 s16, v250, 7
	v_readlane_b32 s17, v250, 8
	s_add_u32 s5, s16, s0
	s_waitcnt lgkmcnt(0)
	v_add_f32_e32 v100, v98, v99
	v_xor_b32_e32 v98, 32, v248
	s_addc_u32 s16, s17, s1
	s_lshl_b32 s0, s4, 2
	v_cmp_lt_i32_e32 vcc, v98, v101
	s_ashr_i32 s1, s0, 31
	s_lshl_b64 s[0:1], s[0:1], 2
	v_cndmask_b32_e32 v98, v248, v98, vcc
	v_lshlrev_b32_e32 v119, 2, v98
	s_add_u32 s0, s5, s0
	v_mov_b32_e32 v101, v100
	s_nop 1
	v_permlane32_swap_b32_e32 v100, v101
	s_addc_u32 s1, s16, s1
	s_add_u32 s0, s0, s78
	s_addc_u32 s1, s1, 0
	v_lshlrev_b32_e32 v202, 6, v232
	v_cmp_eq_u32_e64 s[4:5], 0, v233
	v_lshl_add_u64 v[98:99], s[0:1], 0, v[202:203]
	s_and_saveexec_b64 s[22:23], s[4:5]
	s_cbranch_execz .LBB0_461
	s_waitcnt lgkmcnt(0)
	v_add_f32_e32 v100, v100, v101
	global_store_dword v[98:99], v100, off

.LBB0_463:
	v_mul_f32_e32 v105, v105, v105
	v_mul_f32_e32 v101, v101, v101
	v_fmac_f32_e32 v105, v104, v104
	v_fmac_f32_e32 v101, v100, v100
	v_add_f32_e32 v100, v105, v101
	v_mul_f32_e32 v101, v115, v115
	v_mul_f32_e32 v103, v103, v103
	v_fmac_f32_e32 v101, v114, v114
	v_fmac_f32_e32 v103, v102, v102
	v_add_f32_e32 v101, v101, v103
	v_add_f32_e32 v100, v100, v101
	v_mul_f32_e32 v101, v117, v117
	v_mul_f32_e32 v102, v107, v107
	v_fmac_f32_e32 v101, v116, v116
	v_fmac_f32_e32 v102, v106, v106
	v_add_f32_e32 v101, v101, v102
	v_mul_f32_e32 v102, v111, v111
	v_mul_f32_e32 v103, v109, v109
	v_fmac_f32_e32 v102, v110, v110
	v_fmac_f32_e32 v103, v108, v108
	v_add_f32_e32 v102, v102, v103
	v_add_f32_e32 v101, v101, v102
	v_add_f32_e32 v100, v100, v101
	v_mov_b32_e32 v101, v100
	s_nop 1
	v_permlane16_swap_b32_e32 v100, v101
	s_waitcnt lgkmcnt(0)
	v_add_f32_e32 v100, v100, v101
	v_mov_b32_e32 v101, v100
	s_nop 1
	v_permlane32_swap_b32_e32 v100, v101
	s_and_saveexec_b64 s[22:23], s[4:5]
	s_cbranch_execz .LBB0_465
	s_waitcnt lgkmcnt(0)
	v_add_f32_e32 v100, v100, v101
	global_store_dword v[98:99], v100, off offset:1024

.LBB0_467:
	v_mul_f32_e32 v72, v101, v101
	v_mul_f32_e32 v73, v83, v83
	v_fmac_f32_e32 v72, v100, v100
	v_fmac_f32_e32 v73, v82, v82
	v_add_f32_e32 v72, v72, v73
	v_mul_f32_e32 v73, v87, v87
	v_mul_f32_e32 v82, v85, v85
	v_fmac_f32_e32 v73, v86, v86
	v_fmac_f32_e32 v82, v84, v84
	v_add_f32_e32 v73, v73, v82
	v_add_f32_e32 v72, v72, v73
	v_mul_f32_e32 v73, v89, v89
	v_mul_f32_e32 v67, v67, v67
	v_fmac_f32_e32 v73, v88, v88
	v_fmac_f32_e32 v67, v66, v66
	v_add_f32_e32 v66, v73, v67
	v_mul_f32_e32 v67, v71, v71
	v_mul_f32_e32 v69, v69, v69
	v_fmac_f32_e32 v67, v70, v70
	v_fmac_f32_e32 v69, v68, v68
	v_add_f32_e32 v67, v67, v69
	v_add_f32_e32 v66, v66, v67
	v_add_f32_e32 v66, v72, v66
	v_mov_b32_e32 v67, v66
	s_nop 1
	v_permlane16_swap_b32_e32 v66, v67
	s_waitcnt lgkmcnt(0)
	v_add_f32_e32 v66, v66, v67
	v_mov_b32_e32 v67, v66
	s_nop 1
	v_permlane32_swap_b32_e32 v66, v67
	s_and_saveexec_b64 s[22:23], s[4:5]
	s_cbranch_execz .LBB0_469
	s_waitcnt lgkmcnt(0)
	v_add_f32_e32 v66, v66, v67
	global_store_dword v[98:99], v66, off offset:2048

.LBB0_471:
	v_mul_f32_e32 v71, v71, v71
	v_mul_f32_e32 v67, v67, v67
	v_fmac_f32_e32 v71, v70, v70
	v_fmac_f32_e32 v67, v66, v66
	v_add_f32_e32 v66, v71, v67
	v_mul_f32_e32 v67, v83, v83
	v_mul_f32_e32 v69, v69, v69
	v_fmac_f32_e32 v67, v82, v82
	v_fmac_f32_e32 v69, v68, v68
	v_add_f32_e32 v67, v67, v69
	v_add_f32_e32 v66, v66, v67
	v_mul_f32_e32 v67, v77, v77
	v_mul_f32_e32 v68, v73, v73
	v_fmac_f32_e32 v67, v76, v76
	v_fmac_f32_e32 v68, v72, v72
	v_add_f32_e32 v67, v67, v68
	v_mul_f32_e32 v68, v79, v79
	v_mul_f32_e32 v69, v75, v75
	v_fmac_f32_e32 v68, v78, v78
	v_fmac_f32_e32 v69, v74, v74
	v_add_f32_e32 v68, v68, v69
	v_add_f32_e32 v67, v67, v68
	v_add_f32_e32 v66, v66, v67
	v_mov_b32_e32 v67, v66
	s_nop 1
	v_permlane16_swap_b32_e32 v66, v67
	s_waitcnt lgkmcnt(0)
	v_add_f32_e32 v66, v66, v67
	v_mov_b32_e32 v67, v66
	s_nop 1
	v_permlane32_swap_b32_e32 v66, v67
	s_and_saveexec_b64 s[22:23], s[4:5]
	s_cbranch_execz .LBB0_473
	s_waitcnt lgkmcnt(0)
	v_add_f32_e32 v66, v66, v67
	global_store_dword v[98:99], v66, off offset:3072

.LBB0_475:
	v_mul_f32_e32 v40, v67, v67
	v_mul_f32_e32 v41, v51, v51
	v_fmac_f32_e32 v40, v66, v66
	v_fmac_f32_e32 v41, v50, v50
	v_add_f32_e32 v40, v40, v41
	v_mul_f32_e32 v41, v55, v55
	v_mul_f32_e32 v50, v53, v53
	v_fmac_f32_e32 v41, v54, v54
	v_fmac_f32_e32 v50, v52, v52
	v_add_f32_e32 v41, v41, v50
	v_add_f32_e32 v40, v40, v41
	v_mul_f32_e32 v41, v57, v57
	v_mul_f32_e32 v35, v35, v35
	v_fmac_f32_e32 v41, v56, v56
	v_fmac_f32_e32 v35, v34, v34
	v_add_f32_e32 v34, v41, v35
	v_mul_f32_e32 v35, v39, v39
	v_mul_f32_e32 v37, v37, v37
	v_fmac_f32_e32 v35, v38, v38
	v_fmac_f32_e32 v37, v36, v36
	v_add_f32_e32 v35, v35, v37
	v_add_f32_e32 v34, v34, v35
	v_add_f32_e32 v34, v40, v34
	v_mov_b32_e32 v35, v34
	s_nop 1
	v_permlane16_swap_b32_e32 v34, v35
	s_waitcnt lgkmcnt(0)
	v_add_f32_e32 v34, v34, v35
	v_mov_b32_e32 v35, v34
	s_nop 1
	v_permlane32_swap_b32_e32 v34, v35
	s_and_saveexec_b64 s[22:23], s[4:5]
	s_cbranch_execz .LBB0_477
	s_waitcnt lgkmcnt(0)
	v_add_f32_e32 v36, v34, v35
	v_add_co_u32_e32 v34, vcc, 0x2000, v98
	s_nop 1
	v_addc_co_u32_e32 v35, vcc, 0, v99, vcc
	global_store_dword v[34:35], v36, off

.LBB0_479:
	v_mul_f32_e32 v39, v39, v39
	v_mul_f32_e32 v35, v35, v35
	v_fmac_f32_e32 v39, v38, v38
	v_fmac_f32_e32 v35, v34, v34
	v_add_f32_e32 v34, v39, v35
	v_mul_f32_e32 v35, v51, v51
	v_mul_f32_e32 v37, v37, v37
	v_fmac_f32_e32 v35, v50, v50
	v_fmac_f32_e32 v37, v36, v36
	v_add_f32_e32 v35, v35, v37
	v_add_f32_e32 v34, v34, v35
	v_mul_f32_e32 v35, v45, v45
	v_mul_f32_e32 v36, v41, v41
	v_fmac_f32_e32 v35, v44, v44
	v_fmac_f32_e32 v36, v40, v40
	v_add_f32_e32 v35, v35, v36
	v_mul_f32_e32 v36, v47, v47
	v_mul_f32_e32 v37, v43, v43
	v_fmac_f32_e32 v36, v46, v46
	v_fmac_f32_e32 v37, v42, v42
	v_add_f32_e32 v36, v36, v37
	v_add_f32_e32 v35, v35, v36
	v_add_f32_e32 v34, v34, v35
	v_mov_b32_e32 v35, v34
	s_nop 1
	v_permlane16_swap_b32_e32 v34, v35
	s_waitcnt lgkmcnt(0)
	v_add_f32_e32 v34, v34, v35
	v_mov_b32_e32 v35, v34
	s_nop 1
	v_permlane32_swap_b32_e32 v34, v35
	s_and_saveexec_b64 s[22:23], s[4:5]
	s_cbranch_execz .LBB0_481
	s_waitcnt lgkmcnt(0)
	v_add_f32_e32 v36, v34, v35
	v_add_co_u32_e32 v34, vcc, 0x2000, v98
	s_nop 1
	v_addc_co_u32_e32 v35, vcc, 0, v99, vcc
	global_store_dword v[34:35], v36, off offset:1024

.LBB0_483:
	v_mul_f32_e32 v8, v35, v35
	v_mul_f32_e32 v9, v19, v19
	v_fmac_f32_e32 v8, v34, v34
	v_fmac_f32_e32 v9, v18, v18
	v_add_f32_e32 v8, v8, v9
	v_mul_f32_e32 v9, v23, v23
	v_mul_f32_e32 v18, v21, v21
	v_fmac_f32_e32 v9, v22, v22
	v_fmac_f32_e32 v18, v20, v20
	v_add_f32_e32 v9, v9, v18
	v_add_f32_e32 v8, v8, v9
	v_mul_f32_e32 v9, v25, v25
	v_mul_f32_e32 v3, v3, v3
	v_fmac_f32_e32 v9, v24, v24
	v_fmac_f32_e32 v3, v2, v2
	v_add_f32_e32 v2, v9, v3
	v_mul_f32_e32 v3, v7, v7
	v_mul_f32_e32 v5, v5, v5
	v_fmac_f32_e32 v3, v6, v6
	v_fmac_f32_e32 v5, v4, v4
	v_add_f32_e32 v3, v3, v5
	v_add_f32_e32 v2, v2, v3
	v_add_f32_e32 v2, v8, v2
	v_mov_b32_e32 v3, v2
	s_nop 1
	v_permlane16_swap_b32_e32 v2, v3
	s_waitcnt lgkmcnt(0)
	v_add_f32_e32 v2, v2, v3
	v_mov_b32_e32 v3, v2
	s_nop 1
	v_permlane32_swap_b32_e32 v2, v3
	s_and_saveexec_b64 s[22:23], s[4:5]
	s_cbranch_execz .LBB0_485
	s_waitcnt lgkmcnt(0)
	v_add_f32_e32 v4, v2, v3
	v_add_co_u32_e32 v2, vcc, 0x2000, v98
	s_nop 1
	v_addc_co_u32_e32 v3, vcc, 0, v99, vcc
	global_store_dword v[2:3], v4, off offset:2048

.LBB0_487:
	v_mul_f32_e32 v7, v7, v7
	v_mul_f32_e32 v3, v3, v3
	v_fmac_f32_e32 v7, v6, v6
	v_fmac_f32_e32 v3, v2, v2
	v_add_f32_e32 v2, v7, v3
	v_mul_f32_e32 v3, v19, v19
	v_mul_f32_e32 v5, v5, v5
	v_fmac_f32_e32 v3, v18, v18
	v_fmac_f32_e32 v5, v4, v4
	v_add_f32_e32 v3, v3, v5
	v_add_f32_e32 v2, v2, v3
	v_mul_f32_e32 v3, v13, v13
	v_mul_f32_e32 v4, v9, v9
	v_fmac_f32_e32 v3, v12, v12
	v_fmac_f32_e32 v4, v8, v8
	v_add_f32_e32 v3, v3, v4
	v_mul_f32_e32 v4, v15, v15
	v_mul_f32_e32 v5, v11, v11
	v_fmac_f32_e32 v4, v14, v14
	v_fmac_f32_e32 v5, v10, v10
	v_add_f32_e32 v4, v4, v5
	v_add_f32_e32 v3, v3, v4
	v_add_f32_e32 v2, v2, v3
	v_mov_b32_e32 v3, v2
	s_nop 1
	v_permlane16_swap_b32_e32 v2, v3
	s_waitcnt lgkmcnt(0)
	v_add_f32_e32 v2, v2, v3
	v_mov_b32_e32 v3, v2
	s_nop 1
	v_permlane32_swap_b32_e32 v2, v3
	s_and_saveexec_b64 s[2:3], s[4:5]
	s_cbranch_execz .LBB0_489
	s_waitcnt lgkmcnt(0)
	v_add_f32_e32 v4, v2, v3
	v_add_co_u32_e32 v2, vcc, 0x2000, v98
	s_nop 1
	v_addc_co_u32_e32 v3, vcc, 0, v99, vcc
	global_store_dword v[2:3], v4, off offset:3072

.LBB0_567:
	s_ashr_i32 s13, s12, 31
	s_lshl_b64 s[0:1], s[12:13], 8
	s_add_u32 s22, s0, s72
	s_addc_u32 s23, s1, s81
	v_mov_b32_e32 v199, v179
	v_mov_b32_e32 v165, v180
	s_lshl_b64 s[12:13], s[22:23], 6
	v_readlane_b32 s0, v250, 7
	v_readlane_b32 s1, v250, 8
	s_add_u32 s0, s0, s12
	v_lshlrev_b32_e32 v164, 6, v199
	s_addc_u32 s1, s1, s13
	v_lshl_add_u32 v202, v165, 4, v164
	s_nop 0
	global_load_dwordx4 v[34:37], v202, s[0:1]
	global_load_dwordx4 v[38:41], v202, s[0:1] offset:1024
	global_load_dwordx4 v[42:45], v202, s[0:1] offset:2048
	global_load_dwordx4 v[46:49], v202, s[0:1] offset:3072
	v_lshl_add_u64 v[66:67], s[0:1], 0, v[202:203]
	s_movk_i32 s0, 0x2000
	v_add_co_u32_e32 v66, vcc, s0, v66
	v_and_b32_e32 v80, 64, v248
	s_nop 0
	v_addc_co_u32_e32 v67, vcc, 0, v67, vcc
	global_load_dwordx4 v[68:71], v[66:67], off
	global_load_dwordx4 v[72:75], v[66:67], off offset:1024
	global_load_dwordx4 v[76:79], v[66:67], off offset:2048
	global_load_dwordx4 v[166:169], v[66:67], off offset:3072
	v_xor_b32_e32 v67, 16, v248
	v_add_u32_e32 v80, 64, v80
	v_cmp_lt_i32_e32 vcc, v67, v80
	v_xor_b32_e32 v162, 32, v248
	s_lshl_b64 s[0:1], s[22:23], 8
	v_cndmask_b32_e32 v67, v248, v67, vcc
	v_lshlrev_b32_e32 v184, 2, v67
	v_cmp_lt_i32_e32 vcc, v162, v80
	v_readlane_b32 s2, v251, 44
	s_add_u32 s0, s2, s0
	v_cndmask_b32_e32 v80, v248, v162, vcc
	v_readlane_b32 s2, v251, 45
	v_lshlrev_b32_e32 v163, 8, v199
	v_lshlrev_b32_e32 v183, 2, v80
	s_addc_u32 s1, s2, s1
	v_mov_b32_e32 v81, v203
	v_lshl_add_u32 v80, v165, 6, v163
	s_cmp_eq_u32 s58, 1
	v_lshl_add_u64 v[162:163], s[0:1], 0, v[80:81]
	s_cselect_b64 s[0:1], -1, 0
	s_and_b64 s[0:1], s[10:11], s[0:1]
	v_mov_b32_e32 v66, 0
	v_cndmask_b32_e64 v67, 0, 1, s[0:1]
	v_cmp_ne_u32_e64 s[42:43], 1, v67
	s_andn2_b64 vcc, exec, s[0:1]
	v_mov_b32_e32 v67, v66
	v_mov_b32_e32 v80, v66
	v_mov_b32_e32 v81, v66
	s_waitcnt vmcnt(7)
	v_add_f32_e32 v34, v34, v35
	v_add_f32_e32 v35, v36, v37
	s_waitcnt vmcnt(6)
	v_add_f32_e32 v36, v38, v39
	v_add_f32_e32 v37, v40, v41
	s_waitcnt vmcnt(5)
	v_add_f32_e32 v38, v42, v43
	v_add_f32_e32 v39, v44, v45
	s_waitcnt vmcnt(4)
	v_add_f32_e32 v40, v46, v47
	v_add_f32_e32 v41, v48, v49
	s_waitcnt vmcnt(3)
	v_add_f32_e32 v42, v68, v69
	v_add_f32_e32 v43, v70, v71
	s_waitcnt vmcnt(2)
	v_add_f32_e32 v44, v72, v73
	v_add_f32_e32 v45, v74, v75
	s_waitcnt vmcnt(1)
	v_add_f32_e32 v46, v76, v77
	v_add_f32_e32 v47, v78, v79
	s_waitcnt vmcnt(0)
	v_add_f32_e32 v48, v166, v167
	v_add_f32_e32 v49, v168, v169
	v_add_f32_e32 v34, v34, v35
	v_add_f32_e32 v35, v36, v37
	v_add_f32_e32 v36, v38, v39
	v_add_f32_e32 v37, v40, v41
	v_add_f32_e32 v42, v42, v43
	v_add_f32_e32 v43, v44, v45
	v_add_f32_e32 v44, v46, v47
	v_add_f32_e32 v45, v48, v49
	v_mov_b32_e32 v38, v34
	s_nop 1
	v_permlane16_swap_b32_e32 v34, v38
	v_mov_b32_e32 v39, v35
	s_nop 1
	v_permlane16_swap_b32_e32 v35, v39
	v_mov_b32_e32 v40, v36
	s_nop 1
	v_permlane16_swap_b32_e32 v36, v40
	v_mov_b32_e32 v41, v37
	s_nop 1
	v_permlane16_swap_b32_e32 v37, v41
	v_mov_b32_e32 v46, v42
	s_nop 1
	v_permlane16_swap_b32_e32 v42, v46
	v_mov_b32_e32 v47, v43
	s_nop 1
	v_permlane16_swap_b32_e32 v43, v47
	v_mov_b32_e32 v48, v44
	s_nop 1
	v_permlane16_swap_b32_e32 v44, v48
	v_mov_b32_e32 v49, v45
	s_nop 1
	v_permlane16_swap_b32_e32 v45, v49
	s_waitcnt lgkmcnt(7)
	v_add_f32_e32 v166, v34, v38
	s_waitcnt lgkmcnt(6)
	v_add_f32_e32 v197, v35, v39
	s_waitcnt lgkmcnt(5)
	v_add_f32_e32 v195, v36, v40
	s_waitcnt lgkmcnt(4)
	v_add_f32_e32 v193, v37, v41
	s_waitcnt lgkmcnt(3)
	v_add_f32_e32 v191, v42, v46
	s_waitcnt lgkmcnt(2)
	v_add_f32_e32 v189, v43, v47
	s_waitcnt lgkmcnt(1)
	v_add_f32_e32 v187, v44, v48
	s_waitcnt lgkmcnt(0)
	v_add_f32_e32 v185, v45, v49
	ds_bpermute_b32 v167, v183, v166
	ds_bpermute_b32 v198, v183, v197
	ds_bpermute_b32 v196, v183, v195
	ds_bpermute_b32 v194, v183, v193
	ds_bpermute_b32 v192, v183, v191
	ds_bpermute_b32 v190, v183, v189
	ds_bpermute_b32 v188, v183, v187
	ds_bpermute_b32 v186, v183, v185
	v_mov_b32_e32 v68, v66
	v_mov_b32_e32 v69, v66
	v_mov_b32_e32 v78, v66
	v_mov_b32_e32 v79, v66
	v_mov_b32_e32 v74, v66
	v_mov_b32_e32 v75, v66
	v_mov_b32_e32 v76, v66
	v_mov_b32_e32 v77, v66
	v_mov_b32_e32 v70, v66
	v_mov_b32_e32 v71, v66
	v_mov_b32_e32 v72, v66
	v_mov_b32_e32 v73, v66
	v_mov_b32_e32 v46, v66
	v_mov_b32_e32 v47, v66
	v_mov_b32_e32 v48, v66
	v_mov_b32_e32 v49, v66
	v_mov_b32_e32 v42, v66
	v_mov_b32_e32 v43, v66
	v_mov_b32_e32 v44, v66
	v_mov_b32_e32 v45, v66
	v_mov_b32_e32 v38, v66
	v_mov_b32_e32 v39, v66
	v_mov_b32_e32 v40, v66
	v_mov_b32_e32 v41, v66
	v_mov_b32_e32 v34, v66
	v_mov_b32_e32 v35, v66
	v_mov_b32_e32 v36, v66
	v_mov_b32_e32 v37, v66
	s_cbranch_vccnz .LBB0_569
	s_mov_b64 s[0:1], 0x1000
	v_lshl_add_u64 v[34:35], v[162:163], 0, s[0:1]
	s_movk_i32 s0, 0x1000
	v_add_co_u32_e32 v36, vcc, s0, v162
	global_load_dwordx4 v[66:69], v[162:163], off
	global_load_dwordx4 v[78:81], v[162:163], off offset:16
	global_load_dwordx4 v[74:77], v[162:163], off offset:32
	global_load_dwordx4 v[70:73], v[162:163], off offset:48
	v_addc_co_u32_e32 v37, vcc, 0, v163, vcc
	global_load_dwordx4 v[42:45], v[34:35], off offset:16
	global_load_dwordx4 v[38:41], v[34:35], off offset:32
	global_load_dwordx4 v[46:49], v[36:37], off
	s_nop 0
	global_load_dwordx4 v[34:37], v[34:35], off offset:48

.LBB0_585:
	v_mov_b32_e32 v156, v199
	s_nop 1
	v_permlane16_swap_b32_e32 v199, v156
	s_lshl_b64 s[2:3], s[40:41], 2
	v_readlane_b32 s1, v251, 42
	s_add_u32 s2, s1, s2
	v_readlane_b32 s1, v251, 43
	s_waitcnt lgkmcnt(0)
	v_add_f32_e32 v156, v199, v156
	v_mov_b32_e32 v157, v156
	s_nop 1
	v_permlane32_swap_b32_e32 v156, v157
	s_addc_u32 s3, s1, s3
	v_cmp_eq_u32_e64 s[40:41], 0, v165
	v_mov_b32_e32 v165, v203
	v_lshl_add_u64 v[154:155], s[2:3], 0, v[164:165]
	s_and_saveexec_b64 s[2:3], s[40:41]
	s_cbranch_execz .LBB0_587
	s_lshl_b32 s24, s0, 2
	v_lshl_add_u64 v[158:159], v[154:155], 0, s[24:25]
	s_waitcnt lgkmcnt(0)
	v_add_f32_e32 v156, v156, v157
	global_store_dword v[158:159], v156, off

.LBB0_603:
	v_mov_b32_e32 v130, v157
	s_nop 1
	v_permlane16_swap_b32_e32 v157, v130
	s_waitcnt lgkmcnt(0)
	v_add_f32_e32 v130, v157, v130
	v_mov_b32_e32 v131, v130
	s_nop 1
	v_permlane32_swap_b32_e32 v130, v131
	s_and_saveexec_b64 s[2:3], s[40:41]
	s_cbranch_execz .LBB0_605
	s_lshl_b32 s24, s0, 2
	v_lshl_add_u64 v[132:133], v[154:155], 0, s[24:25]
	s_waitcnt lgkmcnt(0)
	v_add_f32_e32 v130, v130, v131
	global_store_dword v[132:133], v130, off offset:1024

.LBB0_623:
	v_mov_b32_e32 v114, v131
	s_nop 1
	v_permlane16_swap_b32_e32 v131, v114
	s_waitcnt lgkmcnt(0)
	v_add_f32_e32 v114, v131, v114
	v_mov_b32_e32 v115, v114
	s_nop 1
	v_permlane32_swap_b32_e32 v114, v115
	s_and_saveexec_b64 s[2:3], s[40:41]
	s_cbranch_execz .LBB0_625
	s_lshl_b32 s24, s0, 2
	v_lshl_add_u64 v[116:117], v[154:155], 0, s[24:25]
	s_waitcnt lgkmcnt(0)
	v_add_f32_e32 v114, v114, v115
	global_store_dword v[116:117], v114, off offset:2048

.LBB0_641:
	v_mov_b32_e32 v98, v115
	s_nop 1
	v_permlane16_swap_b32_e32 v115, v98
	s_waitcnt lgkmcnt(0)
	v_add_f32_e32 v98, v115, v98
	v_mov_b32_e32 v99, v98
	s_nop 1
	v_permlane32_swap_b32_e32 v98, v99
	s_and_saveexec_b64 s[2:3], s[40:41]
	s_cbranch_execz .LBB0_643
	s_lshl_b32 s24, s0, 2
	v_lshl_add_u64 v[100:101], v[154:155], 0, s[24:25]
	s_waitcnt lgkmcnt(0)
	v_add_f32_e32 v98, v98, v99
	global_store_dword v[100:101], v98, off offset:3072

.LBB0_661:
	ds_bpermute_b32 v82, v184, v91
	s_waitcnt lgkmcnt(0)
	v_add_f32_e32 v82, v91, v82
	v_mov_b32_e32 v83, v82
	s_nop 1
	v_permlane32_swap_b32_e32 v82, v83
	s_and_saveexec_b64 s[2:3], s[40:41]
	s_cbranch_execz .LBB0_663
	s_lshl_b32 s24, s0, 2
	v_lshl_add_u64 v[84:85], v[154:155], 0, s[24:25]
	s_waitcnt lgkmcnt(0)
	v_add_f32_e32 v86, v82, v83
	v_add_co_u32_e32 v82, vcc, 0x2000, v84
	s_nop 1
	v_addc_co_u32_e32 v83, vcc, 0, v85, vcc
	global_store_dword v[82:83], v86, off

.LBB0_679:
	ds_bpermute_b32 v50, v184, v59
	s_waitcnt lgkmcnt(0)
	v_add_f32_e32 v50, v59, v50
	v_mov_b32_e32 v51, v50
	s_nop 1
	v_permlane32_swap_b32_e32 v50, v51
	s_and_saveexec_b64 s[2:3], s[40:41]
	s_cbranch_execz .LBB0_681
	s_lshl_b32 s24, s0, 2
	v_lshl_add_u64 v[52:53], v[154:155], 0, s[24:25]
	s_waitcnt lgkmcnt(0)
	v_add_f32_e32 v54, v50, v51
	v_add_co_u32_e32 v50, vcc, 0x2000, v52
	s_nop 1
	v_addc_co_u32_e32 v51, vcc, 0, v53, vcc
	global_store_dword v[50:51], v54, off offset:1024

.LBB0_699:
	ds_bpermute_b32 v18, v184, v27
	s_waitcnt lgkmcnt(0)
	v_add_f32_e32 v18, v27, v18
	v_mov_b32_e32 v19, v18
	s_nop 1
	v_permlane32_swap_b32_e32 v18, v19
	s_and_saveexec_b64 s[2:3], s[40:41]
	s_cbranch_execz .LBB0_701
	s_lshl_b32 s24, s0, 2
	v_lshl_add_u64 v[20:21], v[154:155], 0, s[24:25]
	s_waitcnt lgkmcnt(0)
	v_add_f32_e32 v22, v18, v19
	v_add_co_u32_e32 v18, vcc, 0x2000, v20
	s_nop 1
	v_addc_co_u32_e32 v19, vcc, 0, v21, vcc
	global_store_dword v[18:19], v22, off offset:2048

.LBB0_717:
	v_mov_b32_e32 v2, v11
	s_nop 1
	v_permlane16_swap_b32_e32 v11, v2
	s_waitcnt lgkmcnt(0)
	v_add_f32_e32 v2, v11, v2
	v_mov_b32_e32 v3, v2
	s_nop 1
	v_permlane32_swap_b32_e32 v2, v3
	s_and_saveexec_b64 s[2:3], s[40:41]
	s_cbranch_execz .LBB0_719
	s_lshl_b32 s24, s0, 2
	v_lshl_add_u64 v[4:5], v[154:155], 0, s[24:25]
	s_waitcnt lgkmcnt(0)
	v_add_f32_e32 v6, v2, v3
	v_add_co_u32_e32 v2, vcc, 0x2000, v4
	s_nop 1
	v_addc_co_u32_e32 v3, vcc, 0, v5, vcc
	global_store_dword v[2:3], v6, off offset:3072

.LBB0_804:
	s_or_b64 exec, exec, s[22:23]
	v_lshlrev_b32_e32 v130, 8, v198
	v_lshl_add_u32 v130, v132, 6, v130
	v_and_b32_e32 v132, 64, v248
	v_xor_b32_e32 v131, 16, v248
	v_add_u32_e32 v132, 64, v132
	v_cmp_lt_i32_e32 vcc, v131, v132
	s_waitcnt vmcnt(0)
	v_add_f32_e32 v86, v86, v87
	v_add_f32_e32 v87, v88, v89
	v_cndmask_b32_e32 v131, v248, v131, vcc
	v_lshlrev_b32_e32 v131, 2, v131
	v_add_f32_e32 v86, v86, v87
	v_mov_b32_e32 v87, v86
	s_nop 1
	v_permlane16_swap_b32_e32 v86, v87
	v_add_f32_e32 v74, v74, v75
	v_add_f32_e32 v75, v76, v77
	v_add_f32_e32 v76, v110, v111
	v_add_f32_e32 v77, v112, v113
	s_waitcnt lgkmcnt(0)
	v_add_f32_e32 v236, v86, v87
	v_add_f32_e32 v86, v94, v95
	v_add_f32_e32 v87, v96, v97
	v_add_f32_e32 v86, v86, v87
	v_add_f32_e32 v74, v74, v75
	v_add_f32_e32 v76, v76, v77
	v_mov_b32_e32 v87, v86
	s_nop 1
	v_permlane16_swap_b32_e32 v86, v87
	v_mov_b32_e32 v75, v74
	s_nop 1
	v_permlane16_swap_b32_e32 v74, v75
	v_mov_b32_e32 v77, v76
	s_nop 1
	v_permlane16_swap_b32_e32 v76, v77
	v_add_f32_e32 v90, v90, v91
	v_add_f32_e32 v91, v92, v93
	s_waitcnt lgkmcnt(2)
	v_add_f32_e32 v234, v86, v87
	s_waitcnt lgkmcnt(1)
	v_add_f32_e32 v232, v74, v75
	s_waitcnt lgkmcnt(0)
	v_add_f32_e32 v230, v76, v77
	v_add_f32_e32 v74, v102, v103
	v_add_f32_e32 v75, v104, v105
	v_add_f32_e32 v76, v118, v119
	v_add_f32_e32 v77, v120, v121
	v_add_f32_e32 v86, v98, v99
	v_add_f32_e32 v87, v100, v101
	v_add_f32_e32 v90, v90, v91
	v_add_f32_e32 v74, v74, v75
	v_add_f32_e32 v76, v76, v77
	v_add_f32_e32 v86, v86, v87
	v_mov_b32_e32 v91, v90
	s_nop 1
	v_permlane16_swap_b32_e32 v90, v91
	v_mov_b32_e32 v75, v74
	s_nop 1
	v_permlane16_swap_b32_e32 v74, v75
	v_mov_b32_e32 v77, v76
	s_nop 1
	v_permlane16_swap_b32_e32 v76, v77
	v_mov_b32_e32 v87, v86
	s_nop 1
	v_permlane16_swap_b32_e32 v86, v87
	v_xor_b32_e32 v133, 32, v248
	v_cmp_lt_i32_e32 vcc, v133, v132
	s_lshl_b64 s[0:1], s[4:5], 8
	v_readlane_b32 s2, v251, 44
	v_cndmask_b32_e32 v88, v248, v133, vcc
	s_add_u32 s0, s2, s0
	v_readlane_b32 s2, v251, 45
	v_lshlrev_b32_e32 v88, 2, v88
	s_waitcnt lgkmcnt(3)
	v_add_f32_e32 v199, v90, v91
	s_waitcnt lgkmcnt(2)
	v_add_f32_e32 v228, v74, v75
	s_waitcnt lgkmcnt(1)
	v_add_f32_e32 v226, v76, v77
	s_waitcnt lgkmcnt(0)
	v_add_f32_e32 v224, v86, v87
	s_addc_u32 s1, s2, s1
	ds_bpermute_b32 v238, v88, v199
	ds_bpermute_b32 v237, v88, v236
	ds_bpermute_b32 v235, v88, v234
	ds_bpermute_b32 v233, v88, v232
	ds_bpermute_b32 v231, v88, v230
	ds_bpermute_b32 v229, v88, v228
	ds_bpermute_b32 v227, v88, v226
	ds_bpermute_b32 v225, v88, v224
	s_cmp_gt_i32 s16, 3
	s_cselect_b64 s[40:41], -1, 0
	s_cmp_lt_i32 s16, 4
	s_cselect_b64 s[22:23], -1, 0
	v_mov_b32_e32 v131, v203
	v_lshl_add_u64 v[200:201], s[0:1], 0, v[130:131]
	s_and_b64 vcc, exec, s[22:23]
	s_cbranch_vccnz .LBB0_806
	s_mov_b64 s[0:1], 0x1000
	v_add_co_u32_e32 v76, vcc, 0x1000, v200
	v_lshl_add_u64 v[74:75], v[200:201], 0, s[0:1]
	s_nop 0
	v_addc_co_u32_e32 v77, vcc, 0, v201, vcc
	s_mov_b64 s[0:1], 0x2000
	global_load_dwordx4 v[162:165], v[200:201], off offset:48
	global_load_dwordx4 v[166:169], v[200:201], off offset:32
	global_load_dwordx4 v[170:173], v[200:201], off offset:16
	global_load_dwordx4 v[174:177], v[200:201], off
	global_load_dwordx4 v[142:145], v[76:77], off
	global_load_dwordx4 v[134:137], v[74:75], off offset:48
	global_load_dwordx4 v[130:133], v[74:75], off offset:32
	global_load_dwordx4 v[138:141], v[74:75], off offset:16
	v_lshl_add_u64 v[74:75], v[200:201], 0, s[0:1]
	s_movk_i32 s0, 0x2000
	v_add_co_u32_e32 v76, vcc, s0, v200
	s_mov_b64 s[0:1], 0x3000
	s_nop 0
	v_addc_co_u32_e32 v77, vcc, 0, v201, vcc
	global_load_dwordx4 v[118:121], v[76:77], off
	global_load_dwordx4 v[98:101], v[74:75], off offset:48
	global_load_dwordx4 v[102:105], v[74:75], off offset:32
	global_load_dwordx4 v[110:113], v[74:75], off offset:16
	v_add_co_u32_e32 v74, vcc, 0x3000, v200
	v_lshl_add_u64 v[90:91], v[200:201], 0, s[0:1]
	s_nop 0
	v_addc_co_u32_e32 v75, vcc, 0, v201, vcc
	global_load_dwordx4 v[94:97], v[74:75], off
	s_nop 0
	global_load_dwordx4 v[74:77], v[90:91], off offset:48
	global_load_dwordx4 v[86:89], v[90:91], off offset:32
	s_nop 0
	global_load_dwordx4 v[90:93], v[90:91], off offset:16

.LBB0_868:
	s_or_b64 exec, exec, s[4:5]
	v_and_b32_e32 v35, 64, v248
	v_xor_b32_e32 v34, 16, v248
	v_add_u32_e32 v35, 64, v35
	v_cmp_lt_i32_e32 vcc, v34, v35
	v_mov_b32_e32 v40, v3
	v_mov_b32_e32 v41, v4
	v_mov_b32_e32 v3, v5
	v_cndmask_b32_e32 v34, v248, v34, vcc
	v_pk_add_f32 v[2:3], v[40:41], v[2:3]
	v_lshlrev_b32_e32 v37, 2, v34
	v_add_f32_e32 v2, v2, v3
	v_mov_b32_e32 v3, v2
	s_nop 1
	v_permlane16_swap_b32_e32 v2, v3
	v_xor_b32_e32 v34, 32, v248
	v_cmp_lt_i32_e32 vcc, v34, v35
	v_readlane_b32 s44, v249, 7
	s_mov_b32 s13, 0xf800000
	v_cndmask_b32_e32 v34, v248, v34, vcc
	v_lshlrev_b32_e32 v36, 2, v34
	s_waitcnt lgkmcnt(0)
	v_add_f32_e32 v2, v2, v3
	v_mov_b32_e32 v3, v2
	s_nop 1
	v_permlane32_swap_b32_e32 v2, v3
	s_movk_i32 s0, 0xfc0
	v_readlane_b32 s48, v249, 11
	v_readlane_b32 s49, v249, 12
	v_mad_u64_u32 v[38:39], s[0:1], v209, s0, v[202:203]
	s_waitcnt lgkmcnt(0)
	v_add_f32_e32 v2, v2, v3
	v_fmamk_f32 v2, v2, 0x3b800000, v204
	v_cmp_gt_f32_e32 vcc, s13, v2
	v_mul_f32_e32 v3, 0x4f800000, v2
	v_readlane_b32 s50, v249, 13
	v_readlane_b32 s51, v249, 14
	s_mov_b64 s[16:17], s[48:49]
	v_cndmask_b32_e32 v2, v2, v3, vcc
	s_lshl_b64 s[0:1], s[42:43], 12
	s_mov_b64 s[18:19], s[50:51]
	v_sqrt_f32_e32 v3, v2
	s_add_u32 s4, s18, s0
	s_addc_u32 s5, s19, s1
	s_lshl_b32 s0, s22, 8
	s_ashr_i32 s1, s0, 31
	s_lshl_b64 s[0:1], s[0:1], 1
	v_add_u32_e32 v4, -1, v3
	s_add_u32 s0, s4, s0
	v_fma_f32 v5, -v4, v3, v2
	s_addc_u32 s1, s5, s1
	v_cmp_ge_f32_e64 s[4:5], 0, v5
	v_add_u32_e32 v5, 1, v3
	s_add_u32 s22, s0, s78
	v_cndmask_b32_e64 v4, v3, v4, s[4:5]
	v_fma_f32 v3, -v5, v3, v2
	v_cmp_lt_f32_e64 s[4:5], 0, v3
	s_addc_u32 s23, s1, 0
	v_mov_b32_e32 v39, v203
	v_cndmask_b32_e64 v3, v4, v5, s[4:5]
	v_mul_f32_e32 v4, 0x37800000, v3
	v_cndmask_b32_e32 v3, v3, v4, vcc
	v_cmp_class_f32_e32 vcc, v2, v205
	v_lshl_add_u64 v[34:35], s[22:23], 0, v[38:39]
	s_mov_b32 s15, 0xf800000
	v_cndmask_b32_e32 v2, v3, v2, vcc
	v_div_scale_f32 v3, s[0:1], v2, v2, 1.0
	v_rcp_f32_e32 v4, v3
	v_readlane_b32 s45, v249, 8
	v_readlane_b32 s46, v249, 9
	v_readlane_b32 s47, v249, 10
	v_fma_f32 v5, -v3, v4, 1.0
	v_fmac_f32_e32 v4, v5, v4
	v_div_scale_f32 v5, vcc, 1.0, v2, 1.0
	v_mul_f32_e32 v39, v5, v4
	v_fma_f32 v40, -v3, v39, v5
	v_fmac_f32_e32 v39, v40, v4
	v_fma_f32 v3, -v3, v39, v5
	v_div_fmas_f32 v3, v3, v4, v39
	v_div_fixup_f32 v40, v3, v2, 1.0
	v_pk_mul_f32 v[2:3], v[190:191], v[40:41] op_sel_hi:[1,0]
	v_pk_mul_f32 v[4:5], v[192:193], v[40:41] op_sel_hi:[1,0]
	v_cvt_pk_bf16_f32 v2, v2, v3
	v_pk_mul_f32 v[42:43], v[188:189], v[40:41] op_sel_hi:[1,0]
	v_cvt_pk_bf16_f32 v3, v4, v5
	v_pk_mul_f32 v[44:45], v[186:187], v[40:41] op_sel_hi:[1,0]
	s_nop 0
	v_cvt_pk_bf16_f32 v4, v44, v45
	v_cvt_pk_bf16_f32 v5, v42, v43
	global_store_dwordx4 v38, v[2:5], s[22:23]
	v_pk_mul_f32 v[42:43], v[180:181], v[40:41] op_sel_hi:[1,0]
	s_nop 0
	v_pk_mul_f32 v[2:3], v[182:183], v[40:41] op_sel_hi:[1,0]
	v_pk_mul_f32 v[4:5], v[184:185], v[40:41] op_sel_hi:[1,0]
	v_cvt_pk_bf16_f32 v2, v2, v3
	v_pk_mul_f32 v[40:41], v[178:179], v[40:41] op_sel_hi:[1,0]
	v_cvt_pk_bf16_f32 v3, v4, v5
	s_nop 0
	v_cvt_pk_bf16_f32 v4, v40, v41
	v_cvt_pk_bf16_f32 v5, v42, v43
	global_store_dwordx4 v38, v[2:5], s[22:23] offset:256
	s_nop 1
	v_mov_b32_e32 v2, v7
	v_mov_b32_e32 v3, v8
	v_mov_b32_e32 v7, v9
	v_pk_add_f32 v[2:3], v[2:3], v[6:7]
	s_nop 0
	v_add_f32_e32 v2, v2, v3
	v_mov_b32_e32 v3, v2
	s_nop 1
	v_permlane16_swap_b32_e32 v2, v3
	s_waitcnt lgkmcnt(0)
	v_add_f32_e32 v2, v2, v3
	v_mov_b32_e32 v3, v2
	s_nop 1
	v_permlane32_swap_b32_e32 v2, v3
	s_waitcnt lgkmcnt(0)
	v_add_f32_e32 v2, v2, v3
	v_fmamk_f32 v2, v2, 0x3b800000, v204
	v_cmp_gt_f32_e32 vcc, s13, v2
	v_mul_f32_e32 v3, 0x4f800000, v2
	s_nop 0
	v_cndmask_b32_e32 v2, v2, v3, vcc
	v_sqrt_f32_e32 v3, v2
	s_nop 0
	v_add_u32_e32 v4, -1, v3
	v_fma_f32 v5, -v4, v3, v2
	v_cmp_ge_f32_e64 s[4:5], 0, v5
	v_add_u32_e32 v5, 1, v3
	s_nop 0
	v_cndmask_b32_e64 v4, v3, v4, s[4:5]
	v_fma_f32 v3, -v5, v3, v2
	v_cmp_lt_f32_e64 s[4:5], 0, v3
	s_nop 1
	v_cndmask_b32_e64 v3, v4, v5, s[4:5]
	v_mul_f32_e32 v4, 0x37800000, v3
	v_cndmask_b32_e32 v3, v3, v4, vcc
	v_cmp_class_f32_e32 vcc, v2, v205
	s_nop 1
	v_cndmask_b32_e32 v2, v3, v2, vcc
	v_div_scale_f32 v3, s[0:1], v2, v2, 1.0
	v_rcp_f32_e32 v4, v3
	s_mov_b32 s0, 0x10000
	v_fma_f32 v5, -v3, v4, 1.0
	v_fmac_f32_e32 v4, v5, v4
	v_div_scale_f32 v5, vcc, 1.0, v2, 1.0
	v_mul_f32_e32 v6, v5, v4
	v_fma_f32 v7, -v3, v6, v5
	v_fmac_f32_e32 v6, v7, v4
	v_fma_f32 v3, -v3, v6, v5
	v_div_fmas_f32 v3, v3, v4, v6
	v_div_fixup_f32 v6, v3, v2, 1.0
	v_pk_mul_f32 v[4:5], v[176:177], v[6:7] op_sel_hi:[1,0]
	v_pk_mul_f32 v[2:3], v[174:175], v[6:7] op_sel_hi:[1,0]
	v_pk_mul_f32 v[8:9], v[172:173], v[6:7] op_sel_hi:[1,0]
	v_pk_mul_f32 v[38:39], v[170:171], v[6:7] op_sel_hi:[1,0]
	v_cvt_pk_bf16_f32 v2, v2, v3
	v_cvt_pk_bf16_f32 v3, v4, v5
	s_nop 0
	v_cvt_pk_bf16_f32 v4, v38, v39
	v_cvt_pk_bf16_f32 v5, v8, v9
	v_add_co_u32_e32 v8, vcc, s0, v34
	v_pk_mul_f32 v[38:39], v[164:165], v[6:7] op_sel_hi:[1,0]
	s_nop 0
	v_addc_co_u32_e32 v9, vcc, 0, v35, vcc
	global_store_dwordx4 v[8:9], v[2:5], off
	s_nop 1
	v_pk_mul_f32 v[2:3], v[166:167], v[6:7] op_sel_hi:[1,0]
	v_pk_mul_f32 v[4:5], v[168:169], v[6:7] op_sel_hi:[1,0]
	v_cvt_pk_bf16_f32 v2, v2, v3
	v_pk_mul_f32 v[6:7], v[162:163], v[6:7] op_sel_hi:[1,0]
	v_cvt_pk_bf16_f32 v3, v4, v5
	s_nop 0
	v_cvt_pk_bf16_f32 v4, v6, v7
	v_cvt_pk_bf16_f32 v5, v38, v39
	global_store_dwordx4 v[8:9], v[2:5], off offset:256
	s_nop 1
	v_mov_b32_e32 v2, v11
	v_mov_b32_e32 v3, v12
	v_mov_b32_e32 v11, v13
	v_pk_add_f32 v[2:3], v[2:3], v[10:11]
	s_nop 0
	v_add_f32_e32 v2, v2, v3
	v_mov_b32_e32 v3, v2
	s_nop 1
	v_permlane16_swap_b32_e32 v2, v3
	s_waitcnt lgkmcnt(0)
	v_add_f32_e32 v2, v2, v3
	v_mov_b32_e32 v3, v2
	s_nop 1
	v_permlane32_swap_b32_e32 v2, v3
	s_waitcnt lgkmcnt(0)
	v_add_f32_e32 v2, v2, v3
	v_fmamk_f32 v2, v2, 0x3b800000, v204
	v_cmp_gt_f32_e32 vcc, s13, v2
	v_mul_f32_e32 v3, 0x4f800000, v2
	s_nop 0
	v_cndmask_b32_e32 v2, v2, v3, vcc
	v_sqrt_f32_e32 v3, v2
	s_nop 0
	v_add_u32_e32 v4, -1, v3
	v_fma_f32 v5, -v4, v3, v2
	v_cmp_ge_f32_e64 s[4:5], 0, v5
	v_add_u32_e32 v5, 1, v3
	s_nop 0
	v_cndmask_b32_e64 v4, v3, v4, s[4:5]
	v_fma_f32 v3, -v5, v3, v2
	v_cmp_lt_f32_e64 s[4:5], 0, v3
	s_nop 1
	v_cndmask_b32_e64 v3, v4, v5, s[4:5]
	v_mul_f32_e32 v4, 0x37800000, v3
	v_cndmask_b32_e32 v3, v3, v4, vcc
	v_cmp_class_f32_e32 vcc, v2, v205
	s_nop 1
	v_cndmask_b32_e32 v2, v3, v2, vcc
	v_div_scale_f32 v3, s[0:1], v2, v2, 1.0
	v_rcp_f32_e32 v4, v3
	s_mov_b32 s0, 0x20000
	v_fma_f32 v5, -v3, v4, 1.0
	v_fmac_f32_e32 v4, v5, v4
	v_div_scale_f32 v5, vcc, 1.0, v2, 1.0
	v_mul_f32_e32 v6, v5, v4
	v_fma_f32 v7, -v3, v6, v5
	v_fmac_f32_e32 v6, v7, v4
	v_fma_f32 v3, -v3, v6, v5
	v_div_fmas_f32 v3, v3, v4, v6
	v_div_fixup_f32 v6, v3, v2, 1.0
	v_pk_mul_f32 v[4:5], v[160:161], v[6:7] op_sel_hi:[1,0]
	v_pk_mul_f32 v[2:3], v[158:159], v[6:7] op_sel_hi:[1,0]
	v_pk_mul_f32 v[8:9], v[156:157], v[6:7] op_sel_hi:[1,0]
	v_pk_mul_f32 v[10:11], v[154:155], v[6:7] op_sel_hi:[1,0]
	v_cvt_pk_bf16_f32 v2, v2, v3
	v_cvt_pk_bf16_f32 v3, v4, v5
	s_nop 0
	v_cvt_pk_bf16_f32 v4, v10, v11
	v_cvt_pk_bf16_f32 v5, v8, v9
	v_add_co_u32_e32 v8, vcc, s0, v34
	v_pk_mul_f32 v[10:11], v[148:149], v[6:7] op_sel_hi:[1,0]
	s_nop 0
	v_addc_co_u32_e32 v9, vcc, 0, v35, vcc
	global_store_dwordx4 v[8:9], v[2:5], off
	s_nop 1
	v_pk_mul_f32 v[2:3], v[150:151], v[6:7] op_sel_hi:[1,0]
	v_pk_mul_f32 v[4:5], v[152:153], v[6:7] op_sel_hi:[1,0]
	v_cvt_pk_bf16_f32 v2, v2, v3
	v_pk_mul_f32 v[6:7], v[146:147], v[6:7] op_sel_hi:[1,0]
	v_cvt_pk_bf16_f32 v3, v4, v5
	s_nop 0
	v_cvt_pk_bf16_f32 v4, v6, v7
	v_cvt_pk_bf16_f32 v5, v10, v11
	global_store_dwordx4 v[8:9], v[2:5], off offset:256
	s_nop 1
	v_mov_b32_e32 v2, v15
	v_mov_b32_e32 v3, v16
	v_mov_b32_e32 v15, v17
	v_pk_add_f32 v[2:3], v[2:3], v[14:15]
	s_nop 0
	v_add_f32_e32 v2, v2, v3
	v_mov_b32_e32 v3, v2
	s_nop 1
	v_permlane16_swap_b32_e32 v2, v3
	s_waitcnt lgkmcnt(0)
	v_add_f32_e32 v2, v2, v3
	v_mov_b32_e32 v3, v2
	s_nop 1
	v_permlane32_swap_b32_e32 v2, v3
	s_waitcnt lgkmcnt(0)
	v_add_f32_e32 v2, v2, v3
	v_fmamk_f32 v2, v2, 0x3b800000, v204
	v_cmp_gt_f32_e32 vcc, s13, v2
	v_mul_f32_e32 v3, 0x4f800000, v2
	s_nop 0
	v_cndmask_b32_e32 v2, v2, v3, vcc
	v_sqrt_f32_e32 v3, v2
	s_nop 0
	v_add_u32_e32 v4, -1, v3
	v_fma_f32 v5, -v4, v3, v2
	v_cmp_ge_f32_e64 s[4:5], 0, v5
	v_add_u32_e32 v5, 1, v3
	s_nop 0
	v_cndmask_b32_e64 v4, v3, v4, s[4:5]
	v_fma_f32 v3, -v5, v3, v2
	v_cmp_lt_f32_e64 s[4:5], 0, v3
	s_nop 1
	v_cndmask_b32_e64 v3, v4, v5, s[4:5]
	v_mul_f32_e32 v4, 0x37800000, v3
	v_cndmask_b32_e32 v3, v3, v4, vcc
	v_cmp_class_f32_e32 vcc, v2, v205
	s_nop 1
	v_cndmask_b32_e32 v2, v3, v2, vcc
	v_div_scale_f32 v3, s[0:1], v2, v2, 1.0
	v_rcp_f32_e32 v4, v3
	s_mov_b32 s0, 0x30000
	v_fma_f32 v5, -v3, v4, 1.0
	v_fmac_f32_e32 v4, v5, v4
	v_div_scale_f32 v5, vcc, 1.0, v2, 1.0
	v_mul_f32_e32 v6, v5, v4
	v_fma_f32 v7, -v3, v6, v5
	v_fmac_f32_e32 v6, v7, v4
	v_fma_f32 v3, -v3, v6, v5
	v_div_fmas_f32 v3, v3, v4, v6
	v_div_fixup_f32 v6, v3, v2, 1.0
	v_pk_mul_f32 v[4:5], v[144:145], v[6:7] op_sel_hi:[1,0]
	v_pk_mul_f32 v[2:3], v[142:143], v[6:7] op_sel_hi:[1,0]
	v_pk_mul_f32 v[8:9], v[140:141], v[6:7] op_sel_hi:[1,0]
	v_pk_mul_f32 v[10:11], v[138:139], v[6:7] op_sel_hi:[1,0]
	v_cvt_pk_bf16_f32 v2, v2, v3
	v_cvt_pk_bf16_f32 v3, v4, v5
	s_nop 0
	v_cvt_pk_bf16_f32 v4, v10, v11
	v_cvt_pk_bf16_f32 v5, v8, v9
	v_add_co_u32_e32 v8, vcc, s0, v34
	v_pk_mul_f32 v[10:11], v[132:133], v[6:7] op_sel_hi:[1,0]
	s_nop 0
	v_addc_co_u32_e32 v9, vcc, 0, v35, vcc
	global_store_dwordx4 v[8:9], v[2:5], off
	s_nop 1
	v_pk_mul_f32 v[2:3], v[134:135], v[6:7] op_sel_hi:[1,0]
	v_pk_mul_f32 v[4:5], v[136:137], v[6:7] op_sel_hi:[1,0]
	v_cvt_pk_bf16_f32 v2, v2, v3
	v_pk_mul_f32 v[6:7], v[130:131], v[6:7] op_sel_hi:[1,0]
	v_cvt_pk_bf16_f32 v3, v4, v5
	s_nop 0
	v_cvt_pk_bf16_f32 v4, v6, v7
	v_cvt_pk_bf16_f32 v5, v10, v11
	global_store_dwordx4 v[8:9], v[2:5], off offset:256
	s_nop 1
	v_mov_b32_e32 v2, v19
	v_mov_b32_e32 v3, v20
	v_mov_b32_e32 v19, v21
	v_pk_add_f32 v[2:3], v[2:3], v[18:19]
	s_nop 0
	v_add_f32_e32 v2, v2, v3
	v_mov_b32_e32 v3, v2
	s_nop 1
	v_permlane16_swap_b32_e32 v2, v3
	s_waitcnt lgkmcnt(0)
	v_add_f32_e32 v2, v2, v3
	v_mov_b32_e32 v3, v2
	s_nop 1
	v_permlane32_swap_b32_e32 v2, v3
	s_waitcnt lgkmcnt(0)
	v_add_f32_e32 v2, v2, v3
	v_fmamk_f32 v2, v2, 0x3b800000, v204
	v_cmp_gt_f32_e32 vcc, s13, v2
	v_mul_f32_e32 v3, 0x4f800000, v2
	s_nop 0
	v_cndmask_b32_e32 v2, v2, v3, vcc
	v_sqrt_f32_e32 v3, v2
	s_nop 0
	v_add_u32_e32 v4, -1, v3
	v_fma_f32 v5, -v4, v3, v2
	v_cmp_ge_f32_e64 s[4:5], 0, v5
	v_add_u32_e32 v5, 1, v3
	s_nop 0
	v_cndmask_b32_e64 v4, v3, v4, s[4:5]
	v_fma_f32 v3, -v5, v3, v2
	v_cmp_lt_f32_e64 s[4:5], 0, v3
	s_nop 1
	v_cndmask_b32_e64 v3, v4, v5, s[4:5]
	v_mul_f32_e32 v4, 0x37800000, v3
	v_cndmask_b32_e32 v3, v3, v4, vcc
	v_cmp_class_f32_e32 vcc, v2, v205
	s_nop 1
	v_cndmask_b32_e32 v2, v3, v2, vcc
	v_div_scale_f32 v3, s[0:1], v2, v2, 1.0
	v_rcp_f32_e32 v4, v3
	s_mov_b32 s0, 0x80000
	v_fma_f32 v5, -v3, v4, 1.0
	v_fmac_f32_e32 v4, v5, v4
	v_div_scale_f32 v5, vcc, 1.0, v2, 1.0
	v_mul_f32_e32 v6, v5, v4
	v_fma_f32 v7, -v3, v6, v5
	v_fmac_f32_e32 v6, v7, v4
	v_fma_f32 v3, -v3, v6, v5
	v_div_fmas_f32 v3, v3, v4, v6
	v_div_fixup_f32 v6, v3, v2, 1.0
	v_pk_mul_f32 v[4:5], v[120:121], v[6:7] op_sel_hi:[1,0]
	v_pk_mul_f32 v[2:3], v[118:119], v[6:7] op_sel_hi:[1,0]
	v_pk_mul_f32 v[8:9], v[116:117], v[6:7] op_sel_hi:[1,0]
	v_pk_mul_f32 v[10:11], v[114:115], v[6:7] op_sel_hi:[1,0]
	v_cvt_pk_bf16_f32 v2, v2, v3
	v_cvt_pk_bf16_f32 v3, v4, v5
	s_nop 0
	v_cvt_pk_bf16_f32 v4, v10, v11
	v_cvt_pk_bf16_f32 v5, v8, v9
	v_add_co_u32_e32 v8, vcc, s0, v34
	v_pk_mul_f32 v[10:11], v[128:129], v[6:7] op_sel_hi:[1,0]
	s_nop 0
	v_addc_co_u32_e32 v9, vcc, 0, v35, vcc
	global_store_dwordx4 v[8:9], v[2:5], off
	s_nop 1
	v_pk_mul_f32 v[2:3], v[122:123], v[6:7] op_sel_hi:[1,0]
	v_pk_mul_f32 v[4:5], v[124:125], v[6:7] op_sel_hi:[1,0]
	v_cvt_pk_bf16_f32 v2, v2, v3
	v_pk_mul_f32 v[6:7], v[126:127], v[6:7] op_sel_hi:[1,0]
	v_cvt_pk_bf16_f32 v3, v4, v5
	s_nop 0
	v_cvt_pk_bf16_f32 v4, v6, v7
	v_cvt_pk_bf16_f32 v5, v10, v11
	global_store_dwordx4 v[8:9], v[2:5], off offset:256
	s_nop 1
	v_mov_b32_e32 v2, v23
	v_mov_b32_e32 v3, v24
	v_mov_b32_e32 v23, v25
	v_pk_add_f32 v[2:3], v[2:3], v[22:23]
	s_nop 0
	v_add_f32_e32 v2, v2, v3
	v_mov_b32_e32 v3, v2
	s_nop 1
	v_permlane16_swap_b32_e32 v2, v3
	s_waitcnt lgkmcnt(0)
	v_add_f32_e32 v2, v2, v3
	v_mov_b32_e32 v3, v2
	s_nop 1
	v_permlane32_swap_b32_e32 v2, v3
	s_waitcnt lgkmcnt(0)
	v_add_f32_e32 v2, v2, v3
	v_fmamk_f32 v2, v2, 0x3b800000, v204
	v_cmp_gt_f32_e32 vcc, s13, v2
	v_mul_f32_e32 v3, 0x4f800000, v2
	s_nop 0
	v_cndmask_b32_e32 v2, v2, v3, vcc
	v_sqrt_f32_e32 v3, v2
	s_nop 0
	v_add_u32_e32 v4, -1, v3
	v_fma_f32 v5, -v4, v3, v2
	v_cmp_ge_f32_e64 s[4:5], 0, v5
	v_add_u32_e32 v5, 1, v3
	s_nop 0
	v_cndmask_b32_e64 v4, v3, v4, s[4:5]
	v_fma_f32 v3, -v5, v3, v2
	v_cmp_lt_f32_e64 s[4:5], 0, v3
	s_nop 1
	v_cndmask_b32_e64 v3, v4, v5, s[4:5]
	v_mul_f32_e32 v4, 0x37800000, v3
	v_cndmask_b32_e32 v3, v3, v4, vcc
	v_cmp_class_f32_e32 vcc, v2, v205
	s_nop 1
	v_cndmask_b32_e32 v2, v3, v2, vcc
	v_div_scale_f32 v3, s[0:1], v2, v2, 1.0
	v_rcp_f32_e32 v4, v3
	s_mov_b32 s0, 0x90000
	v_fma_f32 v5, -v3, v4, 1.0
	v_fmac_f32_e32 v4, v5, v4
	v_div_scale_f32 v5, vcc, 1.0, v2, 1.0
	v_mul_f32_e32 v6, v5, v4
	v_fma_f32 v7, -v3, v6, v5
	v_fmac_f32_e32 v6, v7, v4
	v_fma_f32 v3, -v3, v6, v5
	v_div_fmas_f32 v3, v3, v4, v6
	v_div_fixup_f32 v6, v3, v2, 1.0
	v_pk_mul_f32 v[4:5], v[104:105], v[6:7] op_sel_hi:[1,0]
	v_pk_mul_f32 v[2:3], v[102:103], v[6:7] op_sel_hi:[1,0]
	v_pk_mul_f32 v[8:9], v[100:101], v[6:7] op_sel_hi:[1,0]
	v_pk_mul_f32 v[10:11], v[98:99], v[6:7] op_sel_hi:[1,0]
	v_cvt_pk_bf16_f32 v2, v2, v3
	v_cvt_pk_bf16_f32 v3, v4, v5
	s_nop 0
	v_cvt_pk_bf16_f32 v4, v10, v11
	v_cvt_pk_bf16_f32 v5, v8, v9
	v_add_co_u32_e32 v8, vcc, s0, v34
	v_pk_mul_f32 v[10:11], v[112:113], v[6:7] op_sel_hi:[1,0]
	s_nop 0
	v_addc_co_u32_e32 v9, vcc, 0, v35, vcc
	global_store_dwordx4 v[8:9], v[2:5], off
	s_nop 1
	v_pk_mul_f32 v[2:3], v[106:107], v[6:7] op_sel_hi:[1,0]
	v_pk_mul_f32 v[4:5], v[108:109], v[6:7] op_sel_hi:[1,0]
	v_cvt_pk_bf16_f32 v2, v2, v3
	v_pk_mul_f32 v[6:7], v[110:111], v[6:7] op_sel_hi:[1,0]
	v_cvt_pk_bf16_f32 v3, v4, v5
	s_nop 0
	v_cvt_pk_bf16_f32 v4, v6, v7
	v_cvt_pk_bf16_f32 v5, v10, v11
	global_store_dwordx4 v[8:9], v[2:5], off offset:256
	s_nop 1
	v_mov_b32_e32 v2, v27
	v_mov_b32_e32 v3, v28
	v_mov_b32_e32 v27, v29
	v_pk_add_f32 v[2:3], v[2:3], v[26:27]
	s_nop 0
	v_add_f32_e32 v2, v2, v3
	v_mov_b32_e32 v3, v2
	s_nop 1
	v_permlane16_swap_b32_e32 v2, v3
	s_waitcnt lgkmcnt(0)
	v_add_f32_e32 v2, v2, v3
	v_mov_b32_e32 v3, v2
	s_nop 1
	v_permlane32_swap_b32_e32 v2, v3
	s_waitcnt lgkmcnt(0)
	v_add_f32_e32 v2, v2, v3
	v_fmamk_f32 v2, v2, 0x3b800000, v204
	v_cmp_gt_f32_e32 vcc, s13, v2
	v_mul_f32_e32 v3, 0x4f800000, v2
	s_nop 0
	v_cndmask_b32_e32 v2, v2, v3, vcc
	v_sqrt_f32_e32 v3, v2
	s_nop 0
	v_add_u32_e32 v4, -1, v3
	v_fma_f32 v5, -v4, v3, v2
	v_cmp_ge_f32_e64 s[4:5], 0, v5
	v_add_u32_e32 v5, 1, v3
	s_nop 0
	v_cndmask_b32_e64 v4, v3, v4, s[4:5]
	v_fma_f32 v3, -v5, v3, v2
	v_cmp_lt_f32_e64 s[4:5], 0, v3
	s_nop 1
	v_cndmask_b32_e64 v3, v4, v5, s[4:5]
	v_mul_f32_e32 v4, 0x37800000, v3
	v_cndmask_b32_e32 v3, v3, v4, vcc
	v_cmp_class_f32_e32 vcc, v2, v205
	s_nop 1
	v_cndmask_b32_e32 v2, v3, v2, vcc
	v_div_scale_f32 v3, s[0:1], v2, v2, 1.0
	v_rcp_f32_e32 v4, v3
	s_mov_b32 s0, 0xa0000
	v_fma_f32 v5, -v3, v4, 1.0
	v_fmac_f32_e32 v4, v5, v4
	v_div_scale_f32 v5, vcc, 1.0, v2, 1.0
	v_mul_f32_e32 v6, v5, v4
	v_fma_f32 v7, -v3, v6, v5
	v_fmac_f32_e32 v6, v7, v4
	v_fma_f32 v3, -v3, v6, v5
	v_div_fmas_f32 v3, v3, v4, v6
	v_div_fixup_f32 v6, v3, v2, 1.0
	v_pk_mul_f32 v[4:5], v[88:89], v[6:7] op_sel_hi:[1,0]
	v_pk_mul_f32 v[2:3], v[86:87], v[6:7] op_sel_hi:[1,0]
	v_pk_mul_f32 v[8:9], v[84:85], v[6:7] op_sel_hi:[1,0]
	v_pk_mul_f32 v[10:11], v[82:83], v[6:7] op_sel_hi:[1,0]
	v_cvt_pk_bf16_f32 v2, v2, v3
	v_cvt_pk_bf16_f32 v3, v4, v5
	s_nop 0
	v_cvt_pk_bf16_f32 v4, v10, v11
	v_cvt_pk_bf16_f32 v5, v8, v9
	v_add_co_u32_e32 v8, vcc, s0, v34
	v_pk_mul_f32 v[10:11], v[96:97], v[6:7] op_sel_hi:[1,0]
	s_nop 0
	v_addc_co_u32_e32 v9, vcc, 0, v35, vcc
	global_store_dwordx4 v[8:9], v[2:5], off
	s_nop 1
	v_pk_mul_f32 v[2:3], v[90:91], v[6:7] op_sel_hi:[1,0]
	v_pk_mul_f32 v[4:5], v[92:93], v[6:7] op_sel_hi:[1,0]
	v_cvt_pk_bf16_f32 v2, v2, v3
	v_pk_mul_f32 v[6:7], v[94:95], v[6:7] op_sel_hi:[1,0]
	v_cvt_pk_bf16_f32 v3, v4, v5
	s_nop 0
	v_cvt_pk_bf16_f32 v4, v6, v7
	v_cvt_pk_bf16_f32 v5, v10, v11
	global_store_dwordx4 v[8:9], v[2:5], off offset:256
	s_nop 1
	v_mov_b32_e32 v2, v31
	v_mov_b32_e32 v3, v32
	v_mov_b32_e32 v31, v33
	v_pk_add_f32 v[2:3], v[2:3], v[30:31]
	s_nop 0
	v_add_f32_e32 v2, v2, v3
	v_mov_b32_e32 v3, v2
	s_nop 1
	v_permlane16_swap_b32_e32 v2, v3
	s_waitcnt lgkmcnt(0)
	v_add_f32_e32 v2, v2, v3
	v_mov_b32_e32 v3, v2
	s_nop 1
	v_permlane32_swap_b32_e32 v2, v3
	s_waitcnt lgkmcnt(0)
	v_add_f32_e32 v2, v2, v3
	v_fmamk_f32 v2, v2, 0x3b800000, v204
	v_cmp_gt_f32_e32 vcc, s13, v2
	v_mul_f32_e32 v3, 0x4f800000, v2
	s_nop 0
	v_cndmask_b32_e32 v2, v2, v3, vcc
	v_sqrt_f32_e32 v3, v2
	s_nop 0
	v_add_u32_e32 v4, -1, v3
	v_fma_f32 v5, -v4, v3, v2
	v_cmp_ge_f32_e64 s[4:5], 0, v5
	v_add_u32_e32 v5, 1, v3
	s_nop 0
	v_cndmask_b32_e64 v4, v3, v4, s[4:5]
	v_fma_f32 v3, -v5, v3, v2
	v_cmp_lt_f32_e64 s[4:5], 0, v3
	s_nop 1
	v_cndmask_b32_e64 v3, v4, v5, s[4:5]
	v_mul_f32_e32 v4, 0x37800000, v3
	v_cndmask_b32_e32 v3, v3, v4, vcc
	v_cmp_class_f32_e32 vcc, v2, v205
	s_mov_b64 s[4:5], -1
	s_nop 0
	v_cndmask_b32_e32 v2, v3, v2, vcc
	v_div_scale_f32 v3, s[0:1], v2, v2, 1.0
	v_rcp_f32_e32 v4, v3
	s_mov_b32 s0, 0xb0000
	v_fma_f32 v5, -v3, v4, 1.0
	v_fmac_f32_e32 v4, v5, v4
	v_div_scale_f32 v5, vcc, 1.0, v2, 1.0
	v_mul_f32_e32 v6, v5, v4
	v_fma_f32 v7, -v3, v6, v5
	v_fmac_f32_e32 v6, v7, v4
	v_fma_f32 v3, -v3, v6, v5
	v_div_fmas_f32 v3, v3, v4, v6
	v_div_fixup_f32 v6, v3, v2, 1.0
	v_pk_mul_f32 v[4:5], v[72:73], v[6:7] op_sel_hi:[1,0]
	v_pk_mul_f32 v[2:3], v[70:71], v[6:7] op_sel_hi:[1,0]
	v_pk_mul_f32 v[8:9], v[68:69], v[6:7] op_sel_hi:[1,0]
	v_pk_mul_f32 v[10:11], v[66:67], v[6:7] op_sel_hi:[1,0]
	v_cvt_pk_bf16_f32 v2, v2, v3
	v_cvt_pk_bf16_f32 v3, v4, v5
	s_nop 0
	v_cvt_pk_bf16_f32 v4, v10, v11
	v_cvt_pk_bf16_f32 v5, v8, v9
	v_add_co_u32_e32 v8, vcc, s0, v34
	v_pk_mul_f32 v[10:11], v[80:81], v[6:7] op_sel_hi:[1,0]
	s_nop 0
	v_addc_co_u32_e32 v9, vcc, 0, v35, vcc
	global_store_dwordx4 v[8:9], v[2:5], off
	s_and_b64 vcc, exec, s[2:3]
	s_nop 0
	v_pk_mul_f32 v[4:5], v[76:77], v[6:7] op_sel_hi:[1,0]
	v_pk_mul_f32 v[2:3], v[74:75], v[6:7] op_sel_hi:[1,0]
	v_pk_mul_f32 v[6:7], v[78:79], v[6:7] op_sel_hi:[1,0]
	v_cvt_pk_bf16_f32 v2, v2, v3
	v_cvt_pk_bf16_f32 v3, v4, v5
	s_nop 0
	v_cvt_pk_bf16_f32 v4, v6, v7
	v_cvt_pk_bf16_f32 v5, v10, v11
	global_store_dwordx4 v[8:9], v[2:5], off offset:256
	s_cbranch_vccnz .LBB0_851
	s_andn2_b64 vcc, exec, s[8:9]
	s_cbranch_vccnz .LBB0_850
	s_barrier
	s_branch .LBB0_850

.LBB0_1164:
	s_ashr_i32 s23, s22, 31
	s_lshl_b64 s[0:1], s[22:23], 8
	s_add_u32 s0, s0, s59
	s_addc_u32 s1, s1, s68
	s_lshl_b32 s16, s4, 8
	s_ashr_i32 s17, s16, 31
	s_lshl_b64 s[18:19], s[0:1], 11
	v_readlane_b32 s22, v252, 58
	v_readlane_b32 s23, v252, 59
	s_add_u32 s5, s22, s18
	s_addc_u32 s18, s23, s19
	s_lshl_b64 s[16:17], s[16:17], 1
	s_add_u32 s5, s5, s16
	v_mov_b32_e32 v196, v208
	v_mov_b32_e32 v197, v207
	s_addc_u32 s16, s18, s17
	s_add_u32 s22, s5, s70
	v_lshlrev_b32_e32 v130, 11, v196
	s_addc_u32 s23, s16, 0
	v_lshl_add_u32 v202, v197, 4, v130
	global_load_dwordx4 v[190:193], v202, s[22:23]
	global_load_dwordx4 v[186:189], v202, s[22:23] offset:256
	s_lshl_b64 s[0:1], s[0:1], 6
	v_readlane_b32 s16, v250, 7
	v_readlane_b32 s17, v250, 8
	s_add_u32 s5, s16, s0
	s_addc_u32 s16, s17, s1
	s_lshl_b32 s0, s4, 2
	s_ashr_i32 s1, s0, 31
	s_lshl_b64 s[0:1], s[0:1], 2
	s_add_u32 s0, s5, s0
	s_addc_u32 s1, s16, s1
	s_add_u32 s42, s0, s71
	v_lshl_add_u64 v[194:195], s[22:23], 0, v[202:203]
	s_mov_b32 s0, 0x8000
	v_add_co_u32_e32 v130, vcc, s0, v194
	s_mov_b32 s0, 0x10000
	s_nop 0
	v_addc_co_u32_e32 v131, vcc, 0, v195, vcc
	global_load_dwordx4 v[182:185], v[130:131], off
	global_load_dwordx4 v[178:181], v[130:131], off offset:256
	v_add_co_u32_e32 v130, vcc, s0, v194
	s_mov_b32 s0, 0x18000
	s_nop 0
	v_addc_co_u32_e32 v131, vcc, 0, v195, vcc
	global_load_dwordx4 v[174:177], v[130:131], off
	global_load_dwordx4 v[170:173], v[130:131], off offset:256
	v_add_co_u32_e32 v130, vcc, s0, v194
	s_mov_b32 s0, 0x40000
	s_nop 0
	v_addc_co_u32_e32 v131, vcc, 0, v195, vcc
	global_load_dwordx4 v[166:169], v[130:131], off
	global_load_dwordx4 v[162:165], v[130:131], off offset:256
	v_add_co_u32_e32 v130, vcc, s0, v194
	s_mov_b32 s0, 0x48000
	s_nop 0
	v_addc_co_u32_e32 v131, vcc, 0, v195, vcc
	global_load_dwordx4 v[158:161], v[130:131], off
	global_load_dwordx4 v[154:157], v[130:131], off offset:256
	v_add_co_u32_e32 v130, vcc, s0, v194
	s_mov_b32 s0, 0x50000
	s_nop 0
	v_addc_co_u32_e32 v131, vcc, 0, v195, vcc
	global_load_dwordx4 v[150:153], v[130:131], off
	global_load_dwordx4 v[146:149], v[130:131], off offset:256
	v_add_co_u32_e32 v130, vcc, s0, v194
	s_mov_b32 s0, 0x58000
	s_nop 0
	v_addc_co_u32_e32 v131, vcc, 0, v195, vcc
	global_load_dwordx4 v[142:145], v[130:131], off
	global_load_dwordx4 v[138:141], v[130:131], off offset:256
	v_add_co_u32_e32 v130, vcc, s0, v194
	v_pk_fma_f32 v[116:117], v[116:117], s[20:21], 0 op_sel_hi:[1,0,0]
	s_nop 0
	v_addc_co_u32_e32 v131, vcc, 0, v195, vcc
	global_load_dwordx4 v[134:137], v[130:131], off
	s_nop 0
	global_load_dwordx4 v[130:133], v[130:131], off offset:256
	v_pk_fma_f32 v[98:99], v[98:99], s[20:21], 0 op_sel_hi:[1,0,0]
	v_pk_fma_f32 v[114:115], v[114:115], s[20:21], 0 op_sel_hi:[1,0,0]
	v_pk_fma_f32 v[100:101], v[100:101], s[20:21], 0 op_sel_hi:[1,0,0]
	v_pk_fma_f32 v[120:121], v[120:121], s[20:21], 0 op_sel_hi:[1,0,0]
	v_pk_fma_f32 v[118:119], v[118:119], s[20:21], 0 op_sel_hi:[1,0,0]
	s_addc_u32 s43, s1, 0
	v_lshlrev_b32_e32 v196, 6, v196
	v_cmp_eq_u32_e64 s[4:5], 0, v197
	v_mov_b32_e32 v197, v203
	v_lshl_add_u64 v[196:197], s[42:43], 0, v[196:197]
	s_waitcnt vmcnt(15)
	v_lshlrev_b32_e32 v210, 16, v190
	v_and_b32_e32 v211, 0xffff0000, v190
	v_lshlrev_b32_e32 v190, 16, v191
	v_and_b32_e32 v191, 0xffff0000, v191
	s_waitcnt vmcnt(14)
	v_lshlrev_b32_e32 v218, 16, v186
	v_and_b32_e32 v219, 0xffff0000, v186
	v_lshlrev_b32_e32 v186, 16, v187
	v_and_b32_e32 v187, 0xffff0000, v187
	v_lshlrev_b32_e32 v220, 16, v188
	v_and_b32_e32 v221, 0xffff0000, v188
	v_lshlrev_b32_e32 v188, 16, v189
	v_and_b32_e32 v189, 0xffff0000, v189
	v_pk_add_f32 v[116:117], v[116:117], v[190:191]
	v_pk_add_f32 v[190:191], v[98:99], v[218:219]
	v_pk_fma_f32 v[98:99], v[104:105], s[20:21], 0 op_sel_hi:[1,0,0]
	v_lshlrev_b32_e32 v212, 16, v192
	v_and_b32_e32 v213, 0xffff0000, v192
	v_lshlrev_b32_e32 v192, 16, v193
	v_and_b32_e32 v193, 0xffff0000, v193
	v_pk_add_f32 v[114:115], v[114:115], v[210:211]
	v_pk_add_f32 v[186:187], v[100:101], v[186:187]
	v_pk_fma_f32 v[100:101], v[102:103], s[20:21], 0 op_sel_hi:[1,0,0]
	v_pk_add_f32 v[102:103], v[98:99], v[188:189]
	v_cvt_pk_bf16_f32 v98, v114, v115
	v_cvt_pk_bf16_f32 v99, v116, v117
	v_pk_add_f32 v[120:121], v[120:121], v[192:193]
	v_pk_add_f32 v[118:119], v[118:119], v[212:213]
	v_pk_add_f32 v[104:105], v[100:101], v[220:221]
	v_cvt_pk_bf16_f32 v100, v118, v119
	v_cvt_pk_bf16_f32 v101, v120, v121
	global_store_dwordx4 v202, v[98:101], s[22:23]
	s_nop 1
	v_cvt_pk_bf16_f32 v98, v190, v191
	v_cvt_pk_bf16_f32 v99, v186, v187
	v_cvt_pk_bf16_f32 v100, v104, v105
	v_cvt_pk_bf16_f32 v101, v102, v103
	global_store_dwordx4 v202, v[98:101], s[22:23] offset:256
	s_nop 1
	v_mul_f32_e32 v98, v115, v115
	v_mul_f32_e32 v99, v117, v117
	v_fmac_f32_e32 v98, v114, v114
	v_fmac_f32_e32 v99, v116, v116
	v_add_f32_e32 v98, v98, v99
	v_mul_f32_e32 v99, v119, v119
	v_mul_f32_e32 v100, v121, v121
	v_fmac_f32_e32 v99, v118, v118
	v_fmac_f32_e32 v100, v120, v120
	v_add_f32_e32 v99, v99, v100
	v_add_f32_e32 v98, v98, v99
	v_mul_f32_e32 v99, v191, v191
	v_mul_f32_e32 v100, v187, v187
	v_fmac_f32_e32 v99, v190, v190
	v_fmac_f32_e32 v100, v186, v186
	v_add_f32_e32 v99, v99, v100
	v_mul_f32_e32 v100, v105, v105
	v_mul_f32_e32 v101, v103, v103
	v_fmac_f32_e32 v100, v104, v104
	v_fmac_f32_e32 v101, v102, v102
	v_add_f32_e32 v100, v100, v101
	v_add_f32_e32 v99, v99, v100
	v_and_b32_e32 v100, 64, v248
	v_add_f32_e32 v99, v98, v99
	v_xor_b32_e32 v98, 16, v248
	v_add_u32_e32 v101, 64, v100
	v_cmp_lt_i32_e32 vcc, v98, v101
	s_nop 1
	v_cndmask_b32_e32 v98, v248, v98, vcc
	v_lshlrev_b32_e32 v98, 2, v98
	v_mov_b32_e32 v100, v99
	s_nop 1
	v_permlane16_swap_b32_e32 v99, v100
	s_waitcnt lgkmcnt(0)
	v_add_f32_e32 v100, v99, v100
	v_xor_b32_e32 v99, 32, v248
	v_cmp_lt_i32_e32 vcc, v99, v101
	s_nop 1
	v_cndmask_b32_e32 v99, v248, v99, vcc
	v_lshlrev_b32_e32 v99, 2, v99
	v_mov_b32_e32 v101, v100
	s_nop 1
	v_permlane32_swap_b32_e32 v100, v101
	s_and_saveexec_b64 s[22:23], s[4:5]
	s_cbranch_execz .LBB0_1166
	s_waitcnt lgkmcnt(0)
	v_add_f32_e32 v100, v100, v101
	global_store_dword v[196:197], v100, off
.LBB0_1166:
	s_or_b64 exec, exec, s[22:23]
	s_waitcnt vmcnt(15)
	v_lshlrev_b32_e32 v100, 16, v182
	s_waitcnt lgkmcnt(0)
	v_and_b32_e32 v101, 0xffff0000, v182
	v_pk_fma_f32 v[122:123], v[122:123], s[20:21], 0 op_sel_hi:[1,0,0]
	v_lshlrev_b32_e32 v118, 16, v185
	v_and_b32_e32 v119, 0xffff0000, v185
	v_pk_add_f32 v[122:123], v[122:123], v[100:101]
	v_pk_fma_f32 v[100:101], v[128:129], s[20:21], 0 op_sel_hi:[1,0,0]
	v_lshlrev_b32_e32 v102, 16, v183
	v_and_b32_e32 v103, 0xffff0000, v183
	s_waitcnt vmcnt(14)
	v_lshlrev_b32_e32 v120, 16, v178
	v_and_b32_e32 v121, 0xffff0000, v178
	v_lshlrev_b32_e32 v178, 16, v179
	v_and_b32_e32 v179, 0xffff0000, v179
	v_pk_fma_f32 v[124:125], v[124:125], s[20:21], 0 op_sel_hi:[1,0,0]
	v_pk_add_f32 v[118:119], v[100:101], v[118:119]
	v_pk_fma_f32 v[100:101], v[108:109], s[20:21], 0 op_sel_hi:[1,0,0]
	v_lshlrev_b32_e32 v182, 16, v180
	v_and_b32_e32 v183, 0xffff0000, v180
	v_lshlrev_b32_e32 v180, 16, v181
	v_and_b32_e32 v181, 0xffff0000, v181
	v_pk_add_f32 v[102:103], v[124:125], v[102:103]
	v_pk_fma_f32 v[106:107], v[106:107], s[20:21], 0 op_sel_hi:[1,0,0]
	v_pk_add_f32 v[108:109], v[100:101], v[178:179]
	v_pk_fma_f32 v[100:101], v[112:113], s[20:21], 0 op_sel_hi:[1,0,0]
	v_lshlrev_b32_e32 v116, 16, v184
	v_and_b32_e32 v117, 0xffff0000, v184
	v_pk_fma_f32 v[124:125], v[126:127], s[20:21], 0 op_sel_hi:[1,0,0]
	v_pk_add_f32 v[106:107], v[106:107], v[120:121]
	v_pk_add_f32 v[112:113], v[100:101], v[180:181]
	v_cvt_pk_bf16_f32 v100, v122, v123
	v_cvt_pk_bf16_f32 v101, v102, v103
	v_mul_f32_e32 v120, v123, v123
	v_mul_f32_e32 v103, v103, v103
	v_pk_add_f32 v[116:117], v[124:125], v[116:117]
	v_fmac_f32_e32 v120, v122, v122
	v_fmac_f32_e32 v103, v102, v102
	v_add_f32_e32 v102, v120, v103
	v_mul_f32_e32 v103, v117, v117
	v_mul_f32_e32 v120, v119, v119
	v_fmac_f32_e32 v103, v116, v116
	v_fmac_f32_e32 v120, v118, v118
	v_add_f32_e32 v103, v103, v120
	v_pk_fma_f32 v[110:111], v[110:111], s[20:21], 0 op_sel_hi:[1,0,0]
	v_add_f32_e32 v102, v102, v103
	v_mul_f32_e32 v103, v107, v107
	v_mul_f32_e32 v120, v109, v109
	v_pk_add_f32 v[110:111], v[110:111], v[182:183]
	v_fmac_f32_e32 v103, v106, v106
	v_fmac_f32_e32 v120, v108, v108
	v_add_f32_e32 v103, v103, v120
	v_mul_f32_e32 v120, v111, v111
	v_mul_f32_e32 v121, v113, v113
	v_fmac_f32_e32 v120, v110, v110
	v_fmac_f32_e32 v121, v112, v112
	v_add_f32_e32 v120, v120, v121
	v_add_f32_e32 v103, v103, v120
	v_add_f32_e32 v120, v102, v103
	v_mov_b32_e32 v121, v120
	s_nop 1
	v_permlane16_swap_b32_e32 v120, v121
	s_mov_b64 s[0:1], 0x8000
	v_lshl_add_u64 v[104:105], v[194:195], 0, s[0:1]
	v_cvt_pk_bf16_f32 v102, v116, v117
	v_cvt_pk_bf16_f32 v103, v118, v119
	global_store_dwordx4 v[104:105], v[100:103], off
	s_mov_b64 s[0:1], 0x8100
	v_lshl_add_u64 v[114:115], v[194:195], 0, s[0:1]
	s_waitcnt lgkmcnt(0)
	v_add_f32_e32 v100, v120, v121
	v_mov_b32_e32 v101, v100
	s_nop 1
	v_permlane32_swap_b32_e32 v100, v101
	v_cvt_pk_bf16_f32 v102, v106, v107
	v_cvt_pk_bf16_f32 v103, v108, v109
	v_cvt_pk_bf16_f32 v104, v110, v111
	v_cvt_pk_bf16_f32 v105, v112, v113
	global_store_dwordx4 v[114:115], v[102:105], off
	s_and_saveexec_b64 s[22:23], s[4:5]
	s_cbranch_execz .LBB0_1168
	s_waitcnt lgkmcnt(0)
	v_add_f32_e32 v100, v100, v101
	global_store_dword v[196:197], v100, off offset:1024
.LBB0_1168:
	s_or_b64 exec, exec, s[22:23]
	s_waitcnt vmcnt(15)
	v_lshlrev_b32_e32 v104, 16, v174
	v_and_b32_e32 v105, 0xffff0000, v174
	v_lshlrev_b32_e32 v106, 16, v175
	v_and_b32_e32 v107, 0xffff0000, v175
	s_waitcnt vmcnt(14)
	v_lshlrev_b32_e32 v114, 16, v171
	v_and_b32_e32 v115, 0xffff0000, v171
	v_pk_fma_f32 v[84:85], v[84:85], s[20:21], 0 op_sel_hi:[1,0,0]
	v_pk_fma_f32 v[82:83], v[82:83], s[20:21], 0 op_sel_hi:[1,0,0]
	v_pk_fma_f32 v[68:69], v[68:69], s[20:21], 0 op_sel_hi:[1,0,0]
	v_lshlrev_b32_e32 v116, 16, v172
	v_and_b32_e32 v117, 0xffff0000, v172
	v_pk_add_f32 v[84:85], v[84:85], v[106:107]
	v_pk_add_f32 v[82:83], v[82:83], v[104:105]
	v_pk_add_f32 v[104:105], v[68:69], v[114:115]
	v_pk_fma_f32 v[68:69], v[70:71], s[20:21], 0 op_sel_hi:[1,0,0]
	v_lshlrev_b32_e32 v108, 16, v176
	v_and_b32_e32 v109, 0xffff0000, v176
	v_lshlrev_b32_e32 v110, 16, v177
	v_and_b32_e32 v111, 0xffff0000, v177
	v_lshlrev_b32_e32 v112, 16, v170
	v_and_b32_e32 v113, 0xffff0000, v170
	v_pk_fma_f32 v[88:89], v[88:89], s[20:21], 0 op_sel_hi:[1,0,0]
	v_pk_fma_f32 v[86:87], v[86:87], s[20:21], 0 op_sel_hi:[1,0,0]
	v_pk_fma_f32 v[66:67], v[66:67], s[20:21], 0 op_sel_hi:[1,0,0]
	v_pk_add_f32 v[70:71], v[68:69], v[116:117]
	v_mul_f32_e32 v68, v83, v83
	v_mul_f32_e32 v69, v85, v85
	v_lshlrev_b32_e32 v118, 16, v173
	v_and_b32_e32 v119, 0xffff0000, v173
	v_pk_add_f32 v[88:89], v[88:89], v[110:111]
	v_pk_add_f32 v[86:87], v[86:87], v[108:109]
	v_pk_add_f32 v[106:107], v[66:67], v[112:113]
	v_pk_fma_f32 v[66:67], v[72:73], s[20:21], 0 op_sel_hi:[1,0,0]
	v_fmac_f32_e32 v68, v82, v82
	v_fmac_f32_e32 v69, v84, v84
	v_pk_add_f32 v[72:73], v[66:67], v[118:119]
	v_cvt_pk_bf16_f32 v66, v82, v83
	v_add_f32_e32 v68, v68, v69
	v_mul_f32_e32 v69, v87, v87
	v_mul_f32_e32 v82, v89, v89
	v_fmac_f32_e32 v69, v86, v86
	v_fmac_f32_e32 v82, v88, v88
	v_add_f32_e32 v69, v69, v82
	v_add_f32_e32 v68, v68, v69
	v_mul_f32_e32 v69, v107, v107
	v_mul_f32_e32 v82, v105, v105
	v_fmac_f32_e32 v69, v106, v106
	v_fmac_f32_e32 v82, v104, v104
	v_add_f32_e32 v69, v69, v82
	v_mul_f32_e32 v82, v71, v71
	v_mul_f32_e32 v83, v73, v73
	v_fmac_f32_e32 v82, v70, v70
	v_fmac_f32_e32 v83, v72, v72
	v_add_f32_e32 v82, v82, v83
	v_add_f32_e32 v69, v69, v82
	v_add_f32_e32 v82, v68, v69
	v_mov_b32_e32 v83, v82
	s_nop 1
	v_permlane16_swap_b32_e32 v82, v83
	s_mov_b64 s[0:1], 0x10000
	s_waitcnt lgkmcnt(1)
	v_lshl_add_u64 v[100:101], v[194:195], 0, s[0:1]
	v_cvt_pk_bf16_f32 v67, v84, v85
	v_cvt_pk_bf16_f32 v68, v86, v87
	v_cvt_pk_bf16_f32 v69, v88, v89
	global_store_dwordx4 v[100:101], v[66:69], off
	s_mov_b64 s[0:1], 0x10100
	v_lshl_add_u64 v[102:103], v[194:195], 0, s[0:1]
	s_waitcnt lgkmcnt(0)
	v_add_f32_e32 v66, v82, v83
	v_mov_b32_e32 v67, v66
	s_nop 1
	v_permlane32_swap_b32_e32 v66, v67
	v_cvt_pk_bf16_f32 v68, v106, v107
	v_cvt_pk_bf16_f32 v69, v104, v105
	v_cvt_pk_bf16_f32 v70, v70, v71
	v_cvt_pk_bf16_f32 v71, v72, v73
	global_store_dwordx4 v[102:103], v[68:71], off
	s_and_saveexec_b64 s[22:23], s[4:5]
	s_cbranch_execz .LBB0_1170
	s_waitcnt lgkmcnt(0)
	v_add_f32_e32 v66, v66, v67
	global_store_dword v[196:197], v66, off offset:2048
.LBB0_1170:
	s_or_b64 exec, exec, s[22:23]
	s_waitcnt vmcnt(15)
	v_lshlrev_b32_e32 v66, 16, v166
	s_waitcnt lgkmcnt(0)
	v_and_b32_e32 v67, 0xffff0000, v166
	v_pk_fma_f32 v[90:91], v[90:91], s[20:21], 0 op_sel_hi:[1,0,0]
	v_lshlrev_b32_e32 v84, 16, v169
	v_and_b32_e32 v85, 0xffff0000, v169
	v_pk_add_f32 v[90:91], v[90:91], v[66:67]
	v_pk_fma_f32 v[66:67], v[96:97], s[20:21], 0 op_sel_hi:[1,0,0]
	v_lshlrev_b32_e32 v68, 16, v167
	v_and_b32_e32 v69, 0xffff0000, v167
	s_waitcnt vmcnt(14)
	v_lshlrev_b32_e32 v88, 16, v163
	v_and_b32_e32 v89, 0xffff0000, v163
	v_pk_fma_f32 v[92:93], v[92:93], s[20:21], 0 op_sel_hi:[1,0,0]
	v_pk_add_f32 v[84:85], v[66:67], v[84:85]
	v_pk_fma_f32 v[66:67], v[76:77], s[20:21], 0 op_sel_hi:[1,0,0]
	v_lshlrev_b32_e32 v86, 16, v162
	v_and_b32_e32 v87, 0xffff0000, v162
	v_lshlrev_b32_e32 v102, 16, v165
	v_and_b32_e32 v103, 0xffff0000, v165
	v_pk_add_f32 v[68:69], v[92:93], v[68:69]
	v_pk_fma_f32 v[74:75], v[74:75], s[20:21], 0 op_sel_hi:[1,0,0]
	v_pk_add_f32 v[76:77], v[66:67], v[88:89]
	v_pk_fma_f32 v[66:67], v[80:81], s[20:21], 0 op_sel_hi:[1,0,0]
	v_lshlrev_b32_e32 v82, 16, v168
	v_and_b32_e32 v83, 0xffff0000, v168
	v_pk_fma_f32 v[92:93], v[94:95], s[20:21], 0 op_sel_hi:[1,0,0]
	v_pk_add_f32 v[74:75], v[74:75], v[86:87]
	v_pk_add_f32 v[80:81], v[66:67], v[102:103]
	v_cvt_pk_bf16_f32 v66, v90, v91
	v_cvt_pk_bf16_f32 v67, v68, v69
	v_mul_f32_e32 v86, v91, v91
	v_mul_f32_e32 v69, v69, v69
	v_pk_add_f32 v[82:83], v[92:93], v[82:83]
	v_fmac_f32_e32 v86, v90, v90
	v_fmac_f32_e32 v69, v68, v68
	v_add_f32_e32 v68, v86, v69
	v_mul_f32_e32 v69, v83, v83
	v_mul_f32_e32 v86, v85, v85
	v_fmac_f32_e32 v69, v82, v82
	v_fmac_f32_e32 v86, v84, v84
	v_add_f32_e32 v69, v69, v86
	v_lshlrev_b32_e32 v100, 16, v164
	v_and_b32_e32 v101, 0xffff0000, v164
	v_pk_fma_f32 v[78:79], v[78:79], s[20:21], 0 op_sel_hi:[1,0,0]
	v_add_f32_e32 v68, v68, v69
	v_mul_f32_e32 v69, v75, v75
	v_mul_f32_e32 v86, v77, v77
	v_pk_add_f32 v[78:79], v[78:79], v[100:101]
	v_fmac_f32_e32 v69, v74, v74
	v_fmac_f32_e32 v86, v76, v76
	v_add_f32_e32 v69, v69, v86
	v_mul_f32_e32 v86, v79, v79
	v_mul_f32_e32 v87, v81, v81
	v_fmac_f32_e32 v86, v78, v78
	v_fmac_f32_e32 v87, v80, v80
	v_add_f32_e32 v86, v86, v87
	v_add_f32_e32 v69, v69, v86
	v_add_f32_e32 v86, v68, v69
	v_mov_b32_e32 v87, v86
	s_nop 1
	v_permlane16_swap_b32_e32 v86, v87
	s_mov_b64 s[0:1], 0x18000
	v_lshl_add_u64 v[70:71], v[194:195], 0, s[0:1]
	v_cvt_pk_bf16_f32 v68, v82, v83
	v_cvt_pk_bf16_f32 v69, v84, v85
	global_store_dwordx4 v[70:71], v[66:69], off
	s_mov_b64 s[0:1], 0x18100
	v_lshl_add_u64 v[72:73], v[194:195], 0, s[0:1]
	s_waitcnt lgkmcnt(0)
	v_add_f32_e32 v66, v86, v87
	v_mov_b32_e32 v67, v66
	s_nop 1
	v_permlane32_swap_b32_e32 v66, v67
	v_cvt_pk_bf16_f32 v68, v74, v75
	v_cvt_pk_bf16_f32 v69, v76, v77
	v_cvt_pk_bf16_f32 v70, v78, v79
	v_cvt_pk_bf16_f32 v71, v80, v81
	global_store_dwordx4 v[72:73], v[68:71], off
	s_and_saveexec_b64 s[22:23], s[4:5]
	s_cbranch_execz .LBB0_1172
	s_waitcnt lgkmcnt(0)
	v_add_f32_e32 v66, v66, v67
	global_store_dword v[196:197], v66, off offset:3072
.LBB0_1172:
	s_or_b64 exec, exec, s[22:23]
	s_waitcnt vmcnt(15)
	v_lshlrev_b32_e32 v70, 16, v158
	v_and_b32_e32 v71, 0xffff0000, v158
	v_lshlrev_b32_e32 v72, 16, v159
	v_and_b32_e32 v73, 0xffff0000, v159
	s_waitcnt vmcnt(14)
	v_lshlrev_b32_e32 v80, 16, v155
	v_and_b32_e32 v81, 0xffff0000, v155
	v_pk_fma_f32 v[52:53], v[52:53], s[20:21], 0 op_sel_hi:[1,0,0]
	v_pk_fma_f32 v[50:51], v[50:51], s[20:21], 0 op_sel_hi:[1,0,0]
	v_pk_fma_f32 v[36:37], v[36:37], s[20:21], 0 op_sel_hi:[1,0,0]
	v_lshlrev_b32_e32 v82, 16, v156
	v_and_b32_e32 v83, 0xffff0000, v156
	v_pk_add_f32 v[52:53], v[52:53], v[72:73]
	v_pk_add_f32 v[50:51], v[50:51], v[70:71]
	v_pk_add_f32 v[70:71], v[36:37], v[80:81]
	v_pk_fma_f32 v[36:37], v[38:39], s[20:21], 0 op_sel_hi:[1,0,0]
	v_lshlrev_b32_e32 v74, 16, v160
	v_and_b32_e32 v75, 0xffff0000, v160
	v_lshlrev_b32_e32 v76, 16, v161
	v_and_b32_e32 v77, 0xffff0000, v161
	v_lshlrev_b32_e32 v78, 16, v154
	v_and_b32_e32 v79, 0xffff0000, v154
	v_pk_fma_f32 v[56:57], v[56:57], s[20:21], 0 op_sel_hi:[1,0,0]
	v_pk_fma_f32 v[54:55], v[54:55], s[20:21], 0 op_sel_hi:[1,0,0]
	v_pk_fma_f32 v[34:35], v[34:35], s[20:21], 0 op_sel_hi:[1,0,0]
	v_pk_add_f32 v[38:39], v[36:37], v[82:83]
	v_mul_f32_e32 v36, v51, v51
	v_mul_f32_e32 v37, v53, v53
	v_lshlrev_b32_e32 v84, 16, v157
	v_and_b32_e32 v85, 0xffff0000, v157
	v_pk_add_f32 v[56:57], v[56:57], v[76:77]
	v_pk_add_f32 v[54:55], v[54:55], v[74:75]
	v_pk_add_f32 v[72:73], v[34:35], v[78:79]
	v_pk_fma_f32 v[34:35], v[40:41], s[20:21], 0 op_sel_hi:[1,0,0]
	v_fmac_f32_e32 v36, v50, v50
	v_fmac_f32_e32 v37, v52, v52
	v_pk_add_f32 v[40:41], v[34:35], v[84:85]
	v_cvt_pk_bf16_f32 v34, v50, v51
	v_add_f32_e32 v36, v36, v37
	v_mul_f32_e32 v37, v55, v55
	v_mul_f32_e32 v50, v57, v57
	v_fmac_f32_e32 v37, v54, v54
	v_fmac_f32_e32 v50, v56, v56
	v_add_f32_e32 v37, v37, v50
	v_add_f32_e32 v36, v36, v37
	v_mul_f32_e32 v37, v73, v73
	v_mul_f32_e32 v50, v71, v71
	v_fmac_f32_e32 v37, v72, v72
	v_fmac_f32_e32 v50, v70, v70
	v_add_f32_e32 v37, v37, v50
	v_mul_f32_e32 v50, v39, v39
	v_mul_f32_e32 v51, v41, v41
	v_fmac_f32_e32 v50, v38, v38
	v_fmac_f32_e32 v51, v40, v40
	v_add_f32_e32 v50, v50, v51
	v_add_f32_e32 v37, v37, v50
	v_add_f32_e32 v50, v36, v37
	v_mov_b32_e32 v51, v50
	s_nop 1
	v_permlane16_swap_b32_e32 v50, v51
	s_mov_b64 s[0:1], 0x40000
	s_waitcnt lgkmcnt(1)
	v_lshl_add_u64 v[66:67], v[194:195], 0, s[0:1]
	v_cvt_pk_bf16_f32 v35, v52, v53
	v_cvt_pk_bf16_f32 v36, v54, v55
	v_cvt_pk_bf16_f32 v37, v56, v57
	global_store_dwordx4 v[66:67], v[34:37], off
	s_mov_b64 s[0:1], 0x40100
	v_lshl_add_u64 v[68:69], v[194:195], 0, s[0:1]
	s_waitcnt lgkmcnt(0)
	v_add_f32_e32 v34, v50, v51
	v_mov_b32_e32 v35, v34
	s_nop 1
	v_permlane32_swap_b32_e32 v34, v35
	v_cvt_pk_bf16_f32 v36, v72, v73
	v_cvt_pk_bf16_f32 v37, v70, v71
	v_cvt_pk_bf16_f32 v38, v38, v39
	v_cvt_pk_bf16_f32 v39, v40, v41
	global_store_dwordx4 v[68:69], v[36:39], off
	s_and_saveexec_b64 s[22:23], s[4:5]
	s_cbranch_execz .LBB0_1174
	s_waitcnt lgkmcnt(0)
	v_add_f32_e32 v36, v34, v35
	v_add_co_u32_e32 v34, vcc, 0x2000, v196
	s_nop 1
	v_addc_co_u32_e32 v35, vcc, 0, v197, vcc
	global_store_dword v[34:35], v36, off
.LBB0_1174:
	s_or_b64 exec, exec, s[22:23]
	s_waitcnt vmcnt(15)
	v_lshlrev_b32_e32 v34, 16, v150
	s_waitcnt lgkmcnt(0)
	v_and_b32_e32 v35, 0xffff0000, v150
	v_pk_fma_f32 v[58:59], v[58:59], s[20:21], 0 op_sel_hi:[1,0,0]
	v_lshlrev_b32_e32 v52, 16, v153
	v_and_b32_e32 v53, 0xffff0000, v153
	v_pk_add_f32 v[58:59], v[58:59], v[34:35]
	v_pk_fma_f32 v[34:35], v[64:65], s[20:21], 0 op_sel_hi:[1,0,0]
	v_lshlrev_b32_e32 v36, 16, v151
	v_and_b32_e32 v37, 0xffff0000, v151
	s_waitcnt vmcnt(14)
	v_lshlrev_b32_e32 v56, 16, v147
	v_and_b32_e32 v57, 0xffff0000, v147
	v_pk_fma_f32 v[60:61], v[60:61], s[20:21], 0 op_sel_hi:[1,0,0]
	v_pk_add_f32 v[52:53], v[34:35], v[52:53]
	v_pk_fma_f32 v[34:35], v[44:45], s[20:21], 0 op_sel_hi:[1,0,0]
	v_lshlrev_b32_e32 v54, 16, v146
	v_and_b32_e32 v55, 0xffff0000, v146
	v_lshlrev_b32_e32 v68, 16, v149
	v_and_b32_e32 v69, 0xffff0000, v149
	v_pk_add_f32 v[36:37], v[60:61], v[36:37]
	v_pk_fma_f32 v[42:43], v[42:43], s[20:21], 0 op_sel_hi:[1,0,0]
	v_pk_add_f32 v[44:45], v[34:35], v[56:57]
	v_pk_fma_f32 v[34:35], v[48:49], s[20:21], 0 op_sel_hi:[1,0,0]
	v_lshlrev_b32_e32 v50, 16, v152
	v_and_b32_e32 v51, 0xffff0000, v152
	v_pk_fma_f32 v[60:61], v[62:63], s[20:21], 0 op_sel_hi:[1,0,0]
	v_pk_add_f32 v[42:43], v[42:43], v[54:55]
	v_pk_add_f32 v[48:49], v[34:35], v[68:69]
	v_cvt_pk_bf16_f32 v34, v58, v59
	v_cvt_pk_bf16_f32 v35, v36, v37
	v_mul_f32_e32 v54, v59, v59
	v_mul_f32_e32 v37, v37, v37
	v_pk_add_f32 v[50:51], v[60:61], v[50:51]
	v_fmac_f32_e32 v54, v58, v58
	v_fmac_f32_e32 v37, v36, v36
	v_add_f32_e32 v36, v54, v37
	v_mul_f32_e32 v37, v51, v51
	v_mul_f32_e32 v54, v53, v53
	v_fmac_f32_e32 v37, v50, v50
	v_fmac_f32_e32 v54, v52, v52
	v_add_f32_e32 v37, v37, v54
	v_lshlrev_b32_e32 v66, 16, v148
	v_and_b32_e32 v67, 0xffff0000, v148
	v_pk_fma_f32 v[46:47], v[46:47], s[20:21], 0 op_sel_hi:[1,0,0]
	v_add_f32_e32 v36, v36, v37
	v_mul_f32_e32 v37, v43, v43
	v_mul_f32_e32 v54, v45, v45
	v_pk_add_f32 v[46:47], v[46:47], v[66:67]
	v_fmac_f32_e32 v37, v42, v42
	v_fmac_f32_e32 v54, v44, v44
	v_add_f32_e32 v37, v37, v54
	v_mul_f32_e32 v54, v47, v47
	v_mul_f32_e32 v55, v49, v49
	v_fmac_f32_e32 v54, v46, v46
	v_fmac_f32_e32 v55, v48, v48
	v_add_f32_e32 v54, v54, v55
	v_add_f32_e32 v37, v37, v54
	v_add_f32_e32 v54, v36, v37
	ds_bpermute_b32 v55, v98, v54
	s_mov_b64 s[0:1], 0x48000
	v_lshl_add_u64 v[38:39], v[194:195], 0, s[0:1]
	v_cvt_pk_bf16_f32 v36, v50, v51
	v_cvt_pk_bf16_f32 v37, v52, v53
	global_store_dwordx4 v[38:39], v[34:37], off
	s_mov_b64 s[0:1], 0x48100
	v_lshl_add_u64 v[40:41], v[194:195], 0, s[0:1]
	s_waitcnt lgkmcnt(0)
	v_add_f32_e32 v34, v54, v55
	v_mov_b32_e32 v35, v34
	s_nop 1
	v_permlane32_swap_b32_e32 v34, v35
	v_cvt_pk_bf16_f32 v36, v42, v43
	v_cvt_pk_bf16_f32 v37, v44, v45
	v_cvt_pk_bf16_f32 v38, v46, v47
	v_cvt_pk_bf16_f32 v39, v48, v49
	global_store_dwordx4 v[40:41], v[36:39], off
	s_and_saveexec_b64 s[22:23], s[4:5]
	s_cbranch_execz .LBB0_1176
	s_waitcnt lgkmcnt(0)
	v_add_f32_e32 v36, v34, v35
	v_add_co_u32_e32 v34, vcc, 0x2000, v196
	s_nop 1
	v_addc_co_u32_e32 v35, vcc, 0, v197, vcc
	global_store_dword v[34:35], v36, off offset:1024
.LBB0_1176:
	s_or_b64 exec, exec, s[22:23]
	s_waitcnt vmcnt(15)
	v_lshlrev_b32_e32 v38, 16, v142
	v_and_b32_e32 v39, 0xffff0000, v142
	v_lshlrev_b32_e32 v40, 16, v143
	v_and_b32_e32 v41, 0xffff0000, v143
	s_waitcnt vmcnt(14)
	v_lshlrev_b32_e32 v48, 16, v139
	v_and_b32_e32 v49, 0xffff0000, v139
	v_pk_fma_f32 v[20:21], v[20:21], s[20:21], 0 op_sel_hi:[1,0,0]
	v_pk_fma_f32 v[18:19], v[18:19], s[20:21], 0 op_sel_hi:[1,0,0]
	v_pk_fma_f32 v[4:5], v[4:5], s[20:21], 0 op_sel_hi:[1,0,0]
	v_lshlrev_b32_e32 v50, 16, v140
	v_and_b32_e32 v51, 0xffff0000, v140
	v_pk_add_f32 v[20:21], v[20:21], v[40:41]
	v_pk_add_f32 v[18:19], v[18:19], v[38:39]
	v_pk_add_f32 v[38:39], v[4:5], v[48:49]
	v_pk_fma_f32 v[4:5], v[6:7], s[20:21], 0 op_sel_hi:[1,0,0]
	v_lshlrev_b32_e32 v42, 16, v144
	v_and_b32_e32 v43, 0xffff0000, v144
	v_lshlrev_b32_e32 v44, 16, v145
	v_and_b32_e32 v45, 0xffff0000, v145
	v_lshlrev_b32_e32 v46, 16, v138
	v_and_b32_e32 v47, 0xffff0000, v138
	v_pk_fma_f32 v[24:25], v[24:25], s[20:21], 0 op_sel_hi:[1,0,0]
	v_pk_fma_f32 v[22:23], v[22:23], s[20:21], 0 op_sel_hi:[1,0,0]
	v_pk_fma_f32 v[2:3], v[2:3], s[20:21], 0 op_sel_hi:[1,0,0]
	v_pk_add_f32 v[6:7], v[4:5], v[50:51]
	v_mul_f32_e32 v4, v19, v19
	v_mul_f32_e32 v5, v21, v21
	v_lshlrev_b32_e32 v52, 16, v141
	v_and_b32_e32 v53, 0xffff0000, v141
	v_pk_add_f32 v[24:25], v[24:25], v[44:45]
	v_pk_add_f32 v[22:23], v[22:23], v[42:43]
	v_pk_add_f32 v[40:41], v[2:3], v[46:47]
	v_pk_fma_f32 v[2:3], v[8:9], s[20:21], 0 op_sel_hi:[1,0,0]
	v_fmac_f32_e32 v4, v18, v18
	v_fmac_f32_e32 v5, v20, v20
	v_pk_add_f32 v[8:9], v[2:3], v[52:53]
	v_cvt_pk_bf16_f32 v2, v18, v19
	v_add_f32_e32 v4, v4, v5
	v_mul_f32_e32 v5, v23, v23
	v_mul_f32_e32 v18, v25, v25
	v_fmac_f32_e32 v5, v22, v22
	v_fmac_f32_e32 v18, v24, v24
	v_add_f32_e32 v5, v5, v18
	v_add_f32_e32 v4, v4, v5
	v_mul_f32_e32 v5, v41, v41
	v_mul_f32_e32 v18, v39, v39
	v_fmac_f32_e32 v5, v40, v40
	v_fmac_f32_e32 v18, v38, v38
	v_add_f32_e32 v5, v5, v18
	v_mul_f32_e32 v18, v7, v7
	v_mul_f32_e32 v19, v9, v9
	v_fmac_f32_e32 v18, v6, v6
	v_fmac_f32_e32 v19, v8, v8
	v_add_f32_e32 v18, v18, v19
	v_add_f32_e32 v5, v5, v18
	v_add_f32_e32 v18, v4, v5
	v_mov_b32_e32 v19, v18
	s_nop 1
	v_permlane16_swap_b32_e32 v18, v19
	s_mov_b64 s[0:1], 0x50000
	s_waitcnt lgkmcnt(1)
	v_lshl_add_u64 v[34:35], v[194:195], 0, s[0:1]
	v_cvt_pk_bf16_f32 v3, v20, v21
	v_cvt_pk_bf16_f32 v4, v22, v23
	v_cvt_pk_bf16_f32 v5, v24, v25
	global_store_dwordx4 v[34:35], v[2:5], off
	s_mov_b64 s[0:1], 0x50100
	v_lshl_add_u64 v[36:37], v[194:195], 0, s[0:1]
	s_waitcnt lgkmcnt(0)
	v_add_f32_e32 v2, v18, v19
	v_mov_b32_e32 v3, v2
	s_nop 1
	v_permlane32_swap_b32_e32 v2, v3
	v_cvt_pk_bf16_f32 v4, v40, v41
	v_cvt_pk_bf16_f32 v5, v38, v39
	v_cvt_pk_bf16_f32 v6, v6, v7
	v_cvt_pk_bf16_f32 v7, v8, v9
	global_store_dwordx4 v[36:37], v[4:7], off
	s_and_saveexec_b64 s[22:23], s[4:5]
	s_cbranch_execz .LBB0_1178
	s_waitcnt lgkmcnt(0)
	v_add_f32_e32 v4, v2, v3
	v_add_co_u32_e32 v2, vcc, 0x2000, v196
	s_nop 1
	v_addc_co_u32_e32 v3, vcc, 0, v197, vcc
	global_store_dword v[2:3], v4, off offset:2048
.LBB0_1178:
	s_or_b64 exec, exec, s[22:23]
	s_waitcnt vmcnt(15)
	v_lshlrev_b32_e32 v2, 16, v134
	s_waitcnt lgkmcnt(0)
	v_and_b32_e32 v3, 0xffff0000, v134
	v_pk_fma_f32 v[26:27], v[26:27], s[20:21], 0 op_sel_hi:[1,0,0]
	v_lshlrev_b32_e32 v20, 16, v137
	v_and_b32_e32 v21, 0xffff0000, v137
	v_pk_add_f32 v[26:27], v[26:27], v[2:3]
	v_pk_fma_f32 v[2:3], v[32:33], s[20:21], 0 op_sel_hi:[1,0,0]
	v_lshlrev_b32_e32 v4, 16, v135
	v_and_b32_e32 v5, 0xffff0000, v135
	s_waitcnt vmcnt(14)
	v_lshlrev_b32_e32 v24, 16, v131
	v_and_b32_e32 v25, 0xffff0000, v131
	v_pk_fma_f32 v[28:29], v[28:29], s[20:21], 0 op_sel_hi:[1,0,0]
	v_pk_add_f32 v[20:21], v[2:3], v[20:21]
	v_pk_fma_f32 v[2:3], v[12:13], s[20:21], 0 op_sel_hi:[1,0,0]
	v_lshlrev_b32_e32 v22, 16, v130
	v_and_b32_e32 v23, 0xffff0000, v130
	v_lshlrev_b32_e32 v36, 16, v133
	v_and_b32_e32 v37, 0xffff0000, v133
	v_pk_add_f32 v[4:5], v[28:29], v[4:5]
	v_pk_fma_f32 v[10:11], v[10:11], s[20:21], 0 op_sel_hi:[1,0,0]
	v_pk_add_f32 v[12:13], v[2:3], v[24:25]
	v_pk_fma_f32 v[2:3], v[16:17], s[20:21], 0 op_sel_hi:[1,0,0]
	v_lshlrev_b32_e32 v18, 16, v136
	v_and_b32_e32 v19, 0xffff0000, v136
	v_pk_fma_f32 v[28:29], v[30:31], s[20:21], 0 op_sel_hi:[1,0,0]
	v_pk_add_f32 v[10:11], v[10:11], v[22:23]
	v_pk_add_f32 v[16:17], v[2:3], v[36:37]
	v_cvt_pk_bf16_f32 v2, v26, v27
	v_cvt_pk_bf16_f32 v3, v4, v5
	v_mul_f32_e32 v22, v27, v27
	v_mul_f32_e32 v5, v5, v5
	v_pk_add_f32 v[18:19], v[28:29], v[18:19]
	v_fmac_f32_e32 v22, v26, v26
	v_fmac_f32_e32 v5, v4, v4
	v_add_f32_e32 v4, v22, v5
	v_mul_f32_e32 v5, v19, v19
	v_mul_f32_e32 v22, v21, v21
	v_fmac_f32_e32 v5, v18, v18
	v_fmac_f32_e32 v22, v20, v20
	v_add_f32_e32 v5, v5, v22
	v_lshlrev_b32_e32 v34, 16, v132
	v_and_b32_e32 v35, 0xffff0000, v132
	v_pk_fma_f32 v[14:15], v[14:15], s[20:21], 0 op_sel_hi:[1,0,0]
	v_add_f32_e32 v4, v4, v5
	v_mul_f32_e32 v5, v11, v11
	v_mul_f32_e32 v22, v13, v13
	v_pk_add_f32 v[14:15], v[14:15], v[34:35]
	v_fmac_f32_e32 v5, v10, v10
	v_fmac_f32_e32 v22, v12, v12
	v_add_f32_e32 v5, v5, v22
	v_mul_f32_e32 v22, v15, v15
	v_mul_f32_e32 v23, v17, v17
	v_fmac_f32_e32 v22, v14, v14
	v_fmac_f32_e32 v23, v16, v16
	v_add_f32_e32 v22, v22, v23
	v_add_f32_e32 v5, v5, v22
	v_add_f32_e32 v22, v4, v5
	ds_bpermute_b32 v23, v98, v22
	s_mov_b64 s[0:1], 0x58000
	v_lshl_add_u64 v[6:7], v[194:195], 0, s[0:1]
	v_cvt_pk_bf16_f32 v4, v18, v19
	v_cvt_pk_bf16_f32 v5, v20, v21
	global_store_dwordx4 v[6:7], v[2:5], off
	s_mov_b64 s[0:1], 0x58100
	v_lshl_add_u64 v[8:9], v[194:195], 0, s[0:1]
	s_waitcnt lgkmcnt(0)
	v_add_f32_e32 v2, v22, v23
	v_mov_b32_e32 v3, v2
	s_nop 1
	v_permlane32_swap_b32_e32 v2, v3
	v_cvt_pk_bf16_f32 v4, v10, v11
	v_cvt_pk_bf16_f32 v5, v12, v13
	v_cvt_pk_bf16_f32 v6, v14, v15
	v_cvt_pk_bf16_f32 v7, v16, v17
	global_store_dwordx4 v[8:9], v[4:7], off
	s_and_saveexec_b64 s[22:23], s[4:5]
	s_cbranch_execz .LBB0_1180
	s_waitcnt lgkmcnt(0)
	v_add_f32_e32 v4, v2, v3
	v_add_co_u32_e32 v2, vcc, 0x2000, v196
	s_nop 1
	v_addc_co_u32_e32 v3, vcc, 0, v197, vcc
	global_store_dword v[2:3], v4, off offset:3072

.LBB0_1835:
	v_and_b32_e32 v99, 64, v248
	v_xor_b32_e32 v98, 16, v248
	v_add_u32_e32 v99, 64, v99
	v_cmp_lt_i32_e32 vcc, v98, v99
	v_xor_b32_e32 v100, 32, v248
	s_and_b64 s[0:1], s[4:5], s[8:9]
	v_cndmask_b32_e32 v98, v248, v98, vcc
	v_lshlrev_b32_e32 v98, 2, v98
	v_mov_b32_e32 v98, v230
	s_nop 1
	v_permlane16_swap_b32_e32 v230, v98
	v_cmp_lt_i32_e32 vcc, v100, v99
	s_waitcnt lgkmcnt(0)
	v_add_f32_e32 v98, v230, v98
	v_cndmask_b32_e32 v99, v248, v100, vcc
	v_lshlrev_b32_e32 v99, 2, v99
	v_mov_b32_e32 v99, v98
	s_nop 1
	v_permlane32_swap_b32_e32 v98, v99
	s_and_saveexec_b64 s[8:9], s[0:1]
	s_cbranch_execz .LBB0_1837
	v_lshlrev_b32_e32 v100, 6, v200
	s_waitcnt lgkmcnt(0)
	v_add_f32_e32 v98, v98, v99
	global_store_dword v100, v98, s[56:57]

.LBB0_1839:
	v_and_b32_e32 v100, 64, v248
	s_waitcnt lgkmcnt(0)
	v_xor_b32_e32 v99, 16, v248
	v_add_u32_e32 v100, 64, v100
	v_cmp_lt_i32_e32 vcc, v99, v100
	s_and_b64 s[0:1], s[4:5], s[8:9]
	s_nop 0
	v_cndmask_b32_e32 v99, v248, v99, vcc
	v_lshlrev_b32_e32 v99, 2, v99
	v_mov_b32_e32 v99, v98
	s_nop 1
	v_permlane16_swap_b32_e32 v98, v99
	s_waitcnt lgkmcnt(0)
	v_add_f32_e32 v98, v98, v99
	v_xor_b32_e32 v99, 32, v248
	v_cmp_lt_i32_e32 vcc, v99, v100
	s_nop 1
	v_cndmask_b32_e32 v99, v248, v99, vcc
	v_lshlrev_b32_e32 v99, 2, v99
	v_mov_b32_e32 v99, v98
	s_nop 1
	v_permlane32_swap_b32_e32 v98, v99
	s_and_saveexec_b64 s[8:9], s[0:1]
	s_cbranch_execz .LBB0_1841
	v_lshlrev_b32_e32 v100, 6, v201
	s_waitcnt lgkmcnt(0)
	v_add_f32_e32 v98, v98, v99
	global_store_dword v100, v98, s[56:57]

.LBB0_1843:
	v_and_b32_e32 v67, 64, v248
	v_xor_b32_e32 v66, 16, v248
	v_add_u32_e32 v67, 64, v67
	v_cmp_lt_i32_e32 vcc, v66, v67
	v_xor_b32_e32 v68, 32, v248
	s_and_b64 s[0:1], s[4:5], s[8:9]
	v_cndmask_b32_e32 v66, v248, v66, vcc
	v_lshlrev_b32_e32 v66, 2, v66
	v_mov_b32_e32 v66, v98
	s_nop 1
	v_permlane16_swap_b32_e32 v98, v66
	v_cmp_lt_i32_e32 vcc, v68, v67
	s_waitcnt lgkmcnt(0)
	v_add_f32_e32 v66, v98, v66
	v_cndmask_b32_e32 v67, v248, v68, vcc
	v_lshlrev_b32_e32 v67, 2, v67
	v_mov_b32_e32 v67, v66
	s_nop 1
	v_permlane32_swap_b32_e32 v66, v67
	s_and_saveexec_b64 s[8:9], s[0:1]
	s_cbranch_execz .LBB0_1845
	v_lshlrev_b32_e32 v68, 6, v196
	s_waitcnt lgkmcnt(0)
	v_add_f32_e32 v66, v66, v67
	global_store_dword v68, v66, s[56:57]

.LBB0_1847:
	v_and_b32_e32 v68, 64, v248
	s_waitcnt lgkmcnt(0)
	v_xor_b32_e32 v67, 16, v248
	v_add_u32_e32 v68, 64, v68
	v_cmp_lt_i32_e32 vcc, v67, v68
	s_and_b64 s[0:1], s[4:5], s[8:9]
	s_nop 0
	v_cndmask_b32_e32 v67, v248, v67, vcc
	v_lshlrev_b32_e32 v67, 2, v67
	v_mov_b32_e32 v67, v66
	s_nop 1
	v_permlane16_swap_b32_e32 v66, v67
	s_waitcnt lgkmcnt(0)
	v_add_f32_e32 v66, v66, v67
	v_xor_b32_e32 v67, 32, v248
	v_cmp_lt_i32_e32 vcc, v67, v68
	s_nop 1
	v_cndmask_b32_e32 v67, v248, v67, vcc
	v_lshlrev_b32_e32 v67, 2, v67
	v_mov_b32_e32 v67, v66
	s_nop 1
	v_permlane32_swap_b32_e32 v66, v67
	s_and_saveexec_b64 s[8:9], s[0:1]
	s_cbranch_execz .LBB0_1849
	v_lshlrev_b32_e32 v68, 6, v197
	s_waitcnt lgkmcnt(0)
	v_add_f32_e32 v66, v66, v67
	global_store_dword v68, v66, s[56:57]

.LBB0_1851:
	v_and_b32_e32 v35, 64, v248
	v_xor_b32_e32 v34, 16, v248
	v_add_u32_e32 v35, 64, v35
	v_cmp_lt_i32_e32 vcc, v34, v35
	v_xor_b32_e32 v36, 32, v248
	s_and_b64 s[0:1], s[4:5], s[8:9]
	v_cndmask_b32_e32 v34, v248, v34, vcc
	v_lshlrev_b32_e32 v34, 2, v34
	v_mov_b32_e32 v34, v66
	s_nop 1
	v_permlane16_swap_b32_e32 v66, v34
	v_cmp_lt_i32_e32 vcc, v36, v35
	s_waitcnt lgkmcnt(0)
	v_add_f32_e32 v34, v66, v34
	v_cndmask_b32_e32 v35, v248, v36, vcc
	v_lshlrev_b32_e32 v35, 2, v35
	v_mov_b32_e32 v35, v34
	s_nop 1
	v_permlane32_swap_b32_e32 v34, v35
	s_and_saveexec_b64 s[8:9], s[0:1]
	s_cbranch_execz .LBB0_1853
	v_lshlrev_b32_e32 v36, 6, v192
	s_waitcnt lgkmcnt(0)
	v_add_f32_e32 v34, v34, v35
	global_store_dword v36, v34, s[56:57]

.LBB0_1855:
	v_and_b32_e32 v36, 64, v248
	s_waitcnt lgkmcnt(0)
	v_xor_b32_e32 v35, 16, v248
	v_add_u32_e32 v36, 64, v36
	v_cmp_lt_i32_e32 vcc, v35, v36
	s_and_b64 s[0:1], s[4:5], s[8:9]
	s_nop 0
	v_cndmask_b32_e32 v35, v248, v35, vcc
	v_lshlrev_b32_e32 v35, 2, v35
	v_mov_b32_e32 v35, v34
	s_nop 1
	v_permlane16_swap_b32_e32 v34, v35
	s_waitcnt lgkmcnt(0)
	v_add_f32_e32 v34, v34, v35
	v_xor_b32_e32 v35, 32, v248
	v_cmp_lt_i32_e32 vcc, v35, v36
	s_nop 1
	v_cndmask_b32_e32 v35, v248, v35, vcc
	v_lshlrev_b32_e32 v35, 2, v35
	v_mov_b32_e32 v35, v34
	s_nop 1
	v_permlane32_swap_b32_e32 v34, v35
	s_and_saveexec_b64 s[8:9], s[0:1]
	s_cbranch_execz .LBB0_1857
	v_lshlrev_b32_e32 v36, 6, v193
	s_waitcnt lgkmcnt(0)
	v_add_f32_e32 v34, v34, v35
	global_store_dword v36, v34, s[56:57]

.LBB0_1859:
	v_and_b32_e32 v3, 64, v248
	v_xor_b32_e32 v2, 16, v248
	v_add_u32_e32 v3, 64, v3
	v_cmp_lt_i32_e32 vcc, v2, v3
	v_xor_b32_e32 v4, 32, v248
	s_and_b64 s[0:1], s[4:5], s[8:9]
	v_cndmask_b32_e32 v2, v248, v2, vcc
	v_lshlrev_b32_e32 v2, 2, v2
	ds_bpermute_b32 v2, v2, v34
	v_cmp_lt_i32_e32 vcc, v4, v3
	s_waitcnt lgkmcnt(0)
	v_add_f32_e32 v2, v34, v2
	v_cndmask_b32_e32 v3, v248, v4, vcc
	v_lshlrev_b32_e32 v3, 2, v3
	v_mov_b32_e32 v3, v2
	s_nop 1
	v_permlane32_swap_b32_e32 v2, v3
	s_and_saveexec_b64 s[8:9], s[0:1]
	s_cbranch_execz .LBB0_1861
	v_lshlrev_b32_e32 v4, 6, v190
	s_waitcnt lgkmcnt(0)
	v_add_f32_e32 v2, v2, v3
	global_store_dword v4, v2, s[56:57]

.LBB0_1863:
	v_and_b32_e32 v4, 64, v248
	s_waitcnt lgkmcnt(0)
	v_xor_b32_e32 v3, 16, v248
	v_add_u32_e32 v4, 64, v4
	v_cmp_lt_i32_e32 vcc, v3, v4
	s_and_b64 s[0:1], s[4:5], s[8:9]
	s_nop 0
	v_cndmask_b32_e32 v3, v248, v3, vcc
	v_lshlrev_b32_e32 v3, 2, v3
	v_mov_b32_e32 v3, v2
	s_nop 1
	v_permlane16_swap_b32_e32 v2, v3
	s_waitcnt lgkmcnt(0)
	v_add_f32_e32 v2, v2, v3
	v_xor_b32_e32 v3, 32, v248
	v_cmp_lt_i32_e32 vcc, v3, v4
	s_nop 1
	v_cndmask_b32_e32 v3, v248, v3, vcc
	v_lshlrev_b32_e32 v3, 2, v3
	v_mov_b32_e32 v3, v2
	s_nop 1
	v_permlane32_swap_b32_e32 v2, v3
	s_and_saveexec_b64 s[4:5], s[0:1]
	s_cbranch_execz .LBB0_1865
	v_lshlrev_b32_e32 v4, 6, v191
	s_waitcnt lgkmcnt(0)
	v_add_f32_e32 v2, v2, v3
	global_store_dword v4, v2, s[56:57]

.LBB0_1942:
	s_ashr_i32 s3, s2, 31
	s_lshl_b64 s[0:1], s[2:3], 8
	s_add_u32 s0, s0, s61
	s_addc_u32 s1, s1, s70
	v_mov_b32_e32 v158, v167
	v_mov_b32_e32 v50, v168
	s_lshl_b64 s[2:3], s[0:1], 6
	v_readlane_b32 s12, v250, 7
	v_readlane_b32 s13, v250, 8
	v_lshlrev_b32_e32 v51, 6, v158
	s_add_u32 s2, s12, s2
	v_lshl_add_u32 v202, v50, 4, v51
	s_addc_u32 s3, s13, s3
	global_load_dwordx4 v[174:177], v202, s[2:3]
	global_load_dwordx4 v[154:157], v202, s[2:3] offset:1024
	global_load_dwordx4 v[134:137], v202, s[2:3] offset:2048
	global_load_dwordx4 v[130:133], v202, s[2:3] offset:3072
	v_lshl_add_u64 v[50:51], s[2:3], 0, v[202:203]
	s_movk_i32 s2, 0x2000
	v_add_co_u32_e32 v50, vcc, s2, v50
	s_movk_i32 s2, 0x15c0
	v_mad_u64_u32 v[160:161], s[2:3], v158, s2, v[202:203]
	s_mulk_i32 s1, 0x1600
	s_mul_hi_u32 s2, s0, 0x1600
	s_add_i32 s2, s2, s1
	s_mulk_i32 s0, 0x1600
	v_readlane_b32 s12, v250, 9
	v_readlane_b32 s13, v250, 10
	s_add_u32 s3, s12, s0
	s_addc_u32 s2, s13, s2
	s_lshl_b32 s0, s16, 7
	v_and_b32_e32 v159, 64, v248
	v_addc_co_u32_e32 v51, vcc, 0, v51, vcc
	s_ashr_i32 s1, s0, 31
	v_xor_b32_e32 v158, 16, v248
	v_add_u32_e32 v159, 64, v159
	s_lshl_b64 s[0:1], s[0:1], 1
	v_cmp_lt_i32_e32 vcc, v158, v159
	s_add_u32 s0, s3, s0
	s_addc_u32 s1, s2, s1
	v_cndmask_b32_e32 v158, v248, v158, vcc
	v_lshlrev_b32_e32 v171, 2, v158
	v_xor_b32_e32 v158, 32, v248
	s_add_u32 s12, s0, s72
	v_cmp_lt_i32_e32 vcc, v158, v159
	s_addc_u32 s13, s1, 0
	v_mov_b32_e32 v161, v203
	v_cndmask_b32_e32 v158, v248, v158, vcc
	v_lshlrev_b32_e32 v172, 2, v158
	v_lshl_add_u64 v[158:159], s[12:13], 0, v[160:161]
	s_mov_b32 s11, 0xf800000
	global_load_dwordx4 v[110:113], v[50:51], off
	global_load_dwordx4 v[90:93], v[50:51], off offset:1024
	global_load_dwordx4 v[70:73], v[50:51], off offset:2048
	s_nop 0
	global_load_dwordx4 v[50:53], v[50:51], off offset:3072
	s_mov_b32 s15, 0xf800000
	s_waitcnt vmcnt(7)
	v_add_f32_e32 v161, v174, v175
	v_add_f32_e32 v173, v176, v177
	v_add_f32_e32 v161, v161, v173
	v_mov_b32_e32 v173, v161
	s_nop 1
	v_permlane16_swap_b32_e32 v161, v173
	s_waitcnt lgkmcnt(0)
	v_add_f32_e32 v161, v161, v173
	v_mov_b32_e32 v173, v161
	s_nop 1
	v_permlane32_swap_b32_e32 v161, v173
	s_waitcnt lgkmcnt(0)
	v_add_f32_e32 v161, v161, v173
	v_fmamk_f32 v161, v161, 0x3a800000, v204
	v_cmp_gt_f32_e32 vcc, s11, v161
	v_mul_f32_e32 v173, 0x4f800000, v161
	s_nop 0
	v_cndmask_b32_e32 v161, v161, v173, vcc
	v_sqrt_f32_e32 v173, v161
	s_nop 0
	v_add_u32_e32 v174, -1, v173
	v_fma_f32 v175, -v174, v173, v161
	v_cmp_ge_f32_e64 s[2:3], 0, v175
	v_add_u32_e32 v175, 1, v173
	s_nop 0
	v_cndmask_b32_e64 v174, v173, v174, s[2:3]
	v_fma_f32 v173, -v175, v173, v161
	v_cmp_lt_f32_e64 s[2:3], 0, v173
	s_nop 1
	v_cndmask_b32_e64 v173, v174, v175, s[2:3]
	v_mul_f32_e32 v174, 0x37800000, v173
	v_cndmask_b32_e32 v173, v173, v174, vcc
	v_cmp_class_f32_e32 vcc, v161, v205
	s_nop 1
	v_cndmask_b32_e32 v161, v173, v161, vcc
	v_div_scale_f32 v173, s[0:1], v161, v161, 1.0
	v_rcp_f32_e32 v174, v173
	s_nop 0
	v_fma_f32 v175, -v173, v174, 1.0
	v_fmac_f32_e32 v174, v175, v174
	v_div_scale_f32 v175, vcc, 1.0, v161, 1.0
	v_mul_f32_e32 v176, v175, v174
	v_fma_f32 v177, -v173, v176, v175
	v_fmac_f32_e32 v176, v177, v174
	v_fma_f32 v173, -v173, v176, v175
	v_div_fmas_f32 v173, v173, v174, v176
	v_div_fixup_f32 v161, v173, v161, 1.0
	v_mul_f32_e32 v173, 0xbfb8aa3b, v161
	v_mul_f32_e32 v174, v150, v173
	v_exp_f32_e32 v174, v174
	v_mul_f32_e32 v161, v161, v161
	v_add_f32_e32 v174, 1.0, v174
	v_rcp_f32_e32 v174, v174
	s_nop 0
	v_mul_f32_e32 v174, v161, v174
	v_mul_f32_e32 v146, v146, v174
	v_mul_f32_e32 v146, v150, v146
	v_mul_f32_e32 v150, v151, v173
	v_exp_f32_e32 v150, v150
	s_nop 0
	v_add_f32_e32 v150, 1.0, v150
	v_rcp_f32_e32 v150, v150
	s_nop 0
	v_mul_f32_e32 v150, v161, v150
	v_mul_f32_e32 v147, v147, v150
	v_mul_f32_e32 v150, v152, v173
	v_exp_f32_e32 v150, v150
	v_mul_f32_e32 v147, v151, v147
	v_add_f32_e32 v150, 1.0, v150
	v_rcp_f32_e32 v150, v150
	s_nop 0
	v_mul_f32_e32 v150, v161, v150
	v_mul_f32_e32 v148, v148, v150
	v_mul_f32_e32 v150, v153, v173
	v_exp_f32_e32 v150, v150
	v_mul_f32_e32 v148, v152, v148
	v_add_f32_e32 v150, 1.0, v150
	v_rcp_f32_e32 v150, v150
	s_nop 0
	v_mul_f32_e32 v150, v161, v150
	v_mul_f32_e32 v149, v149, v150
	v_mul_f32_e32 v150, v142, v173
	v_exp_f32_e32 v150, v150
	v_mul_f32_e32 v149, v153, v149
	v_add_f32_e32 v150, 1.0, v150
	v_rcp_f32_e32 v150, v150
	s_nop 0
	v_mul_f32_e32 v150, v161, v150
	v_mul_f32_e32 v138, v138, v150
	v_mul_f32_e32 v142, v142, v138
	v_mul_f32_e32 v138, v143, v173
	v_exp_f32_e32 v138, v138
	s_nop 0
	v_add_f32_e32 v138, 1.0, v138
	v_rcp_f32_e32 v138, v138
	s_nop 0
	v_mul_f32_e32 v138, v161, v138
	v_mul_f32_e32 v138, v139, v138
	v_mul_f32_e32 v143, v143, v138
	v_mul_f32_e32 v138, v144, v173
	v_exp_f32_e32 v138, v138
	s_nop 0
	v_add_f32_e32 v138, 1.0, v138
	v_rcp_f32_e32 v138, v138
	s_nop 0
	v_mul_f32_e32 v138, v161, v138
	v_mul_f32_e32 v138, v140, v138
	v_mul_f32_e32 v144, v144, v138
	v_mul_f32_e32 v138, v145, v173
	v_exp_f32_e32 v138, v138
	s_nop 0
	v_add_f32_e32 v138, 1.0, v138
	v_rcp_f32_e32 v138, v138
	s_nop 0
	v_mul_f32_e32 v138, v161, v138
	v_mul_f32_e32 v138, v141, v138
	v_mul_f32_e32 v141, v145, v138
	v_cvt_pk_bf16_f32 v138, v146, v147
	v_cvt_pk_bf16_f32 v139, v148, v149
	v_cvt_pk_bf16_f32 v140, v142, v143
	v_cvt_pk_bf16_f32 v141, v144, v141
	global_store_dwordx4 v160, v[138:141], s[12:13]
	s_waitcnt vmcnt(7)
	s_nop 0
	v_add_f32_e32 v138, v154, v155
	v_add_f32_e32 v139, v156, v157
	v_add_f32_e32 v138, v138, v139
	v_mov_b32_e32 v139, v138
	s_nop 1
	v_permlane16_swap_b32_e32 v138, v139
	s_waitcnt lgkmcnt(0)
	v_add_f32_e32 v138, v138, v139
	v_mov_b32_e32 v139, v138
	s_nop 1
	v_permlane32_swap_b32_e32 v138, v139
	s_waitcnt lgkmcnt(0)
	v_add_f32_e32 v138, v138, v139
	v_fmamk_f32 v138, v138, 0x3a800000, v204
	v_cmp_gt_f32_e32 vcc, s11, v138
	v_mul_f32_e32 v139, 0x4f800000, v138
	s_nop 0
	v_cndmask_b32_e32 v138, v138, v139, vcc
	v_sqrt_f32_e32 v139, v138
	s_nop 0
	v_add_u32_e32 v140, -1, v139
	v_fma_f32 v141, -v140, v139, v138
	v_cmp_ge_f32_e64 s[2:3], 0, v141
	v_add_u32_e32 v141, 1, v139
	s_nop 0
	v_cndmask_b32_e64 v140, v139, v140, s[2:3]
	v_fma_f32 v139, -v141, v139, v138
	v_cmp_lt_f32_e64 s[2:3], 0, v139
	s_nop 1
	v_cndmask_b32_e64 v139, v140, v141, s[2:3]
	v_mul_f32_e32 v140, 0x37800000, v139
	v_cndmask_b32_e32 v139, v139, v140, vcc
	v_cmp_class_f32_e32 vcc, v138, v205
	s_nop 1
	v_cndmask_b32_e32 v138, v139, v138, vcc
	v_div_scale_f32 v139, s[0:1], v138, v138, 1.0
	v_rcp_f32_e32 v140, v139
	s_mov_b32 s0, 0x16000
	v_fma_f32 v141, -v139, v140, 1.0
	v_fmac_f32_e32 v140, v141, v140
	v_div_scale_f32 v141, vcc, 1.0, v138, 1.0
	v_mul_f32_e32 v142, v141, v140
	v_fma_f32 v143, -v139, v142, v141
	v_fmac_f32_e32 v142, v143, v140
	v_fma_f32 v139, -v139, v142, v141
	v_div_fmas_f32 v139, v139, v140, v142
	v_div_fixup_f32 v138, v139, v138, 1.0
	v_mul_f32_e32 v139, 0xbfb8aa3b, v138
	v_mul_f32_e32 v140, v126, v139
	v_exp_f32_e32 v140, v140
	v_mul_f32_e32 v138, v138, v138
	v_add_f32_e32 v140, 1.0, v140
	v_rcp_f32_e32 v140, v140
	s_nop 0
	v_mul_f32_e32 v140, v138, v140
	v_mul_f32_e32 v122, v122, v140
	v_mul_f32_e32 v122, v126, v122
	v_mul_f32_e32 v126, v127, v139
	v_exp_f32_e32 v126, v126
	s_nop 0
	v_add_f32_e32 v126, 1.0, v126
	v_rcp_f32_e32 v126, v126
	s_nop 0
	v_mul_f32_e32 v126, v138, v126
	v_mul_f32_e32 v123, v123, v126
	v_mul_f32_e32 v126, v128, v139
	v_exp_f32_e32 v126, v126
	v_mul_f32_e32 v123, v127, v123
	v_add_f32_e32 v126, 1.0, v126
	v_rcp_f32_e32 v126, v126
	s_nop 0
	v_mul_f32_e32 v126, v138, v126
	v_mul_f32_e32 v124, v124, v126
	v_mul_f32_e32 v126, v129, v139
	v_exp_f32_e32 v126, v126
	v_mul_f32_e32 v124, v128, v124
	v_add_f32_e32 v126, 1.0, v126
	v_rcp_f32_e32 v126, v126
	s_nop 0
	v_mul_f32_e32 v126, v138, v126
	v_mul_f32_e32 v125, v125, v126
	v_mul_f32_e32 v126, v118, v139
	v_exp_f32_e32 v126, v126
	v_mul_f32_e32 v125, v129, v125
	v_add_f32_e32 v126, 1.0, v126
	v_rcp_f32_e32 v126, v126
	s_nop 0
	v_mul_f32_e32 v126, v138, v126
	v_mul_f32_e32 v114, v114, v126
	v_mul_f32_e32 v118, v118, v114
	v_mul_f32_e32 v114, v119, v139
	v_exp_f32_e32 v114, v114
	s_nop 0
	v_add_f32_e32 v114, 1.0, v114
	v_rcp_f32_e32 v114, v114
	s_nop 0
	v_mul_f32_e32 v114, v138, v114
	v_mul_f32_e32 v114, v115, v114
	v_mul_f32_e32 v119, v119, v114
	v_mul_f32_e32 v114, v120, v139
	v_exp_f32_e32 v114, v114
	s_nop 0
	v_add_f32_e32 v114, 1.0, v114
	v_rcp_f32_e32 v114, v114
	s_nop 0
	v_mul_f32_e32 v114, v138, v114
	v_mul_f32_e32 v114, v116, v114
	v_mul_f32_e32 v120, v120, v114
	v_mul_f32_e32 v114, v121, v139
	v_exp_f32_e32 v114, v114
	s_nop 0
	v_add_f32_e32 v114, 1.0, v114
	v_rcp_f32_e32 v114, v114
	s_nop 0
	v_mul_f32_e32 v114, v138, v114
	v_mul_f32_e32 v114, v117, v114
	v_mul_f32_e32 v117, v121, v114
	v_cvt_pk_bf16_f32 v114, v122, v123
	v_cvt_pk_bf16_f32 v115, v124, v125
	v_cvt_pk_bf16_f32 v116, v118, v119
	v_add_co_u32_e32 v118, vcc, s0, v158
	v_cvt_pk_bf16_f32 v117, v120, v117
	s_nop 1
	v_addc_co_u32_e32 v119, vcc, 0, v159, vcc
	global_store_dwordx4 v[118:119], v[114:117], off
	s_waitcnt vmcnt(7)
	s_nop 0
	v_add_f32_e32 v114, v134, v135
	v_add_f32_e32 v115, v136, v137
	v_add_f32_e32 v114, v114, v115
	v_mov_b32_e32 v115, v114
	s_nop 1
	v_permlane16_swap_b32_e32 v114, v115
	s_waitcnt lgkmcnt(0)
	v_add_f32_e32 v114, v114, v115
	v_mov_b32_e32 v115, v114
	s_nop 1
	v_permlane32_swap_b32_e32 v114, v115
	s_waitcnt lgkmcnt(0)
	v_add_f32_e32 v114, v114, v115
	v_fmamk_f32 v114, v114, 0x3a800000, v204
	v_cmp_gt_f32_e32 vcc, s11, v114
	v_mul_f32_e32 v115, 0x4f800000, v114
	s_nop 0
	v_cndmask_b32_e32 v114, v114, v115, vcc
	v_sqrt_f32_e32 v115, v114
	s_nop 0
	v_add_u32_e32 v116, -1, v115
	v_fma_f32 v117, -v116, v115, v114
	v_cmp_ge_f32_e64 s[2:3], 0, v117
	v_add_u32_e32 v117, 1, v115
	s_nop 0
	v_cndmask_b32_e64 v116, v115, v116, s[2:3]
	v_fma_f32 v115, -v117, v115, v114
	v_cmp_lt_f32_e64 s[2:3], 0, v115
	s_nop 1
	v_cndmask_b32_e64 v115, v116, v117, s[2:3]
	v_mul_f32_e32 v116, 0x37800000, v115
	v_cndmask_b32_e32 v115, v115, v116, vcc
	v_cmp_class_f32_e32 vcc, v114, v205
	s_nop 1
	v_cndmask_b32_e32 v114, v115, v114, vcc
	v_div_scale_f32 v115, s[0:1], v114, v114, 1.0
	v_rcp_f32_e32 v116, v115
	s_mov_b32 s0, 0x2c000
	v_fma_f32 v117, -v115, v116, 1.0
	v_fmac_f32_e32 v116, v117, v116
	v_div_scale_f32 v117, vcc, 1.0, v114, 1.0
	v_mul_f32_e32 v118, v117, v116
	v_fma_f32 v119, -v115, v118, v117
	v_fmac_f32_e32 v118, v119, v116
	v_fma_f32 v115, -v115, v118, v117
	v_div_fmas_f32 v115, v115, v116, v118
	v_div_fixup_f32 v114, v115, v114, 1.0
	v_mul_f32_e32 v115, 0xbfb8aa3b, v114
	v_mul_f32_e32 v116, v106, v115
	v_exp_f32_e32 v116, v116
	v_mul_f32_e32 v114, v114, v114
	v_add_f32_e32 v116, 1.0, v116
	v_rcp_f32_e32 v116, v116
	s_nop 0
	v_mul_f32_e32 v116, v114, v116
	v_mul_f32_e32 v102, v102, v116
	v_mul_f32_e32 v102, v106, v102
	v_mul_f32_e32 v106, v107, v115
	v_exp_f32_e32 v106, v106
	s_nop 0
	v_add_f32_e32 v106, 1.0, v106
	v_rcp_f32_e32 v106, v106
	s_nop 0
	v_mul_f32_e32 v106, v114, v106
	v_mul_f32_e32 v103, v103, v106
	v_mul_f32_e32 v106, v108, v115
	v_exp_f32_e32 v106, v106
	v_mul_f32_e32 v103, v107, v103
	v_add_f32_e32 v106, 1.0, v106
	v_rcp_f32_e32 v106, v106
	s_nop 0
	v_mul_f32_e32 v106, v114, v106
	v_mul_f32_e32 v104, v104, v106
	v_mul_f32_e32 v106, v109, v115
	v_exp_f32_e32 v106, v106
	v_mul_f32_e32 v104, v108, v104
	v_add_f32_e32 v106, 1.0, v106
	v_rcp_f32_e32 v106, v106
	s_nop 0
	v_mul_f32_e32 v106, v114, v106
	v_mul_f32_e32 v105, v105, v106
	v_mul_f32_e32 v106, v98, v115
	v_exp_f32_e32 v106, v106
	v_mul_f32_e32 v105, v109, v105
	v_add_f32_e32 v106, 1.0, v106
	v_rcp_f32_e32 v106, v106
	s_nop 0
	v_mul_f32_e32 v106, v114, v106
	v_mul_f32_e32 v94, v94, v106
	v_mul_f32_e32 v98, v98, v94
	v_mul_f32_e32 v94, v99, v115
	v_exp_f32_e32 v94, v94
	s_nop 0
	v_add_f32_e32 v94, 1.0, v94
	v_rcp_f32_e32 v94, v94
	s_nop 0
	v_mul_f32_e32 v94, v114, v94
	v_mul_f32_e32 v94, v95, v94
	v_mul_f32_e32 v99, v99, v94
	v_mul_f32_e32 v94, v100, v115
	v_exp_f32_e32 v94, v94
	s_nop 0
	v_add_f32_e32 v94, 1.0, v94
	v_rcp_f32_e32 v94, v94
	s_nop 0
	v_mul_f32_e32 v94, v114, v94
	v_mul_f32_e32 v94, v96, v94
	v_mul_f32_e32 v100, v100, v94
	v_mul_f32_e32 v94, v101, v115
	v_exp_f32_e32 v94, v94
	s_nop 0
	v_add_f32_e32 v94, 1.0, v94
	v_rcp_f32_e32 v94, v94
	s_nop 0
	v_mul_f32_e32 v94, v114, v94
	v_mul_f32_e32 v94, v97, v94
	v_mul_f32_e32 v97, v101, v94
	v_cvt_pk_bf16_f32 v94, v102, v103
	v_cvt_pk_bf16_f32 v95, v104, v105
	v_cvt_pk_bf16_f32 v96, v98, v99
	v_add_co_u32_e32 v98, vcc, s0, v158
	v_cvt_pk_bf16_f32 v97, v100, v97
	s_nop 1
	v_addc_co_u32_e32 v99, vcc, 0, v159, vcc
	global_store_dwordx4 v[98:99], v[94:97], off
	s_waitcnt vmcnt(7)
	s_nop 0
	v_add_f32_e32 v94, v130, v131
	v_add_f32_e32 v95, v132, v133
	v_add_f32_e32 v94, v94, v95
	v_mov_b32_e32 v95, v94
	s_nop 1
	v_permlane16_swap_b32_e32 v94, v95
	s_waitcnt lgkmcnt(0)
	v_add_f32_e32 v94, v94, v95
	v_mov_b32_e32 v95, v94
	s_nop 1
	v_permlane32_swap_b32_e32 v94, v95
	s_waitcnt lgkmcnt(0)
	v_add_f32_e32 v94, v94, v95
	v_fmamk_f32 v94, v94, 0x3a800000, v204
	v_cmp_gt_f32_e32 vcc, s11, v94
	v_mul_f32_e32 v95, 0x4f800000, v94
	s_nop 0
	v_cndmask_b32_e32 v94, v94, v95, vcc
	v_sqrt_f32_e32 v95, v94
	s_nop 0
	v_add_u32_e32 v96, -1, v95
	v_fma_f32 v97, -v96, v95, v94
	v_cmp_ge_f32_e64 s[2:3], 0, v97
	v_add_u32_e32 v97, 1, v95
	s_nop 0
	v_cndmask_b32_e64 v96, v95, v96, s[2:3]
	v_fma_f32 v95, -v97, v95, v94
	v_cmp_lt_f32_e64 s[2:3], 0, v95
	s_nop 1
	v_cndmask_b32_e64 v95, v96, v97, s[2:3]
	v_mul_f32_e32 v96, 0x37800000, v95
	v_cndmask_b32_e32 v95, v95, v96, vcc
	v_cmp_class_f32_e32 vcc, v94, v205
	s_nop 1
	v_cndmask_b32_e32 v94, v95, v94, vcc
	v_div_scale_f32 v95, s[0:1], v94, v94, 1.0
	v_rcp_f32_e32 v96, v95
	s_mov_b32 s0, 0x42000
	v_fma_f32 v97, -v95, v96, 1.0
	v_fmac_f32_e32 v96, v97, v96
	v_div_scale_f32 v97, vcc, 1.0, v94, 1.0
	v_mul_f32_e32 v98, v97, v96
	v_fma_f32 v99, -v95, v98, v97
	v_fmac_f32_e32 v98, v99, v96
	v_fma_f32 v95, -v95, v98, v97
	v_div_fmas_f32 v95, v95, v96, v98
	v_div_fixup_f32 v94, v95, v94, 1.0
	v_mul_f32_e32 v95, 0xbfb8aa3b, v94
	v_mul_f32_e32 v96, v86, v95
	v_exp_f32_e32 v96, v96
	v_mul_f32_e32 v94, v94, v94
	v_add_f32_e32 v96, 1.0, v96
	v_rcp_f32_e32 v96, v96
	s_nop 0
	v_mul_f32_e32 v96, v94, v96
	v_mul_f32_e32 v82, v82, v96
	v_mul_f32_e32 v82, v86, v82
	v_mul_f32_e32 v86, v87, v95
	v_exp_f32_e32 v86, v86
	s_nop 0
	v_add_f32_e32 v86, 1.0, v86
	v_rcp_f32_e32 v86, v86
	s_nop 0
	v_mul_f32_e32 v86, v94, v86
	v_mul_f32_e32 v83, v83, v86
	v_mul_f32_e32 v86, v88, v95
	v_exp_f32_e32 v86, v86
	v_mul_f32_e32 v83, v87, v83
	v_add_f32_e32 v86, 1.0, v86
	v_rcp_f32_e32 v86, v86
	s_nop 0
	v_mul_f32_e32 v86, v94, v86
	v_mul_f32_e32 v84, v84, v86
	v_mul_f32_e32 v86, v89, v95
	v_exp_f32_e32 v86, v86
	v_mul_f32_e32 v84, v88, v84
	v_add_f32_e32 v86, 1.0, v86
	v_rcp_f32_e32 v86, v86
	s_nop 0
	v_mul_f32_e32 v86, v94, v86
	v_mul_f32_e32 v85, v85, v86
	v_mul_f32_e32 v86, v78, v95
	v_exp_f32_e32 v86, v86
	v_mul_f32_e32 v85, v89, v85
	v_add_f32_e32 v86, 1.0, v86
	v_rcp_f32_e32 v86, v86
	s_nop 0
	v_mul_f32_e32 v86, v94, v86
	v_mul_f32_e32 v74, v74, v86
	v_mul_f32_e32 v78, v78, v74
	v_mul_f32_e32 v74, v79, v95
	v_exp_f32_e32 v74, v74
	s_nop 0
	v_add_f32_e32 v74, 1.0, v74
	v_rcp_f32_e32 v74, v74
	s_nop 0
	v_mul_f32_e32 v74, v94, v74
	v_mul_f32_e32 v74, v75, v74
	v_mul_f32_e32 v79, v79, v74
	v_mul_f32_e32 v74, v80, v95
	v_exp_f32_e32 v74, v74
	s_nop 0
	v_add_f32_e32 v74, 1.0, v74
	v_rcp_f32_e32 v74, v74
	s_nop 0
	v_mul_f32_e32 v74, v94, v74
	v_mul_f32_e32 v74, v76, v74
	v_mul_f32_e32 v80, v80, v74
	v_mul_f32_e32 v74, v81, v95
	v_exp_f32_e32 v74, v74
	s_nop 0
	v_add_f32_e32 v74, 1.0, v74
	v_rcp_f32_e32 v74, v74
	s_nop 0
	v_mul_f32_e32 v74, v94, v74
	v_mul_f32_e32 v74, v77, v74
	v_mul_f32_e32 v77, v81, v74
	v_cvt_pk_bf16_f32 v74, v82, v83
	v_cvt_pk_bf16_f32 v75, v84, v85
	v_cvt_pk_bf16_f32 v76, v78, v79
	v_add_co_u32_e32 v78, vcc, s0, v158
	v_cvt_pk_bf16_f32 v77, v80, v77
	s_nop 1
	v_addc_co_u32_e32 v79, vcc, 0, v159, vcc
	global_store_dwordx4 v[78:79], v[74:77], off
	s_waitcnt vmcnt(7)
	s_nop 0
	v_add_f32_e32 v74, v110, v111
	v_add_f32_e32 v75, v112, v113
	v_add_f32_e32 v74, v74, v75
	v_mov_b32_e32 v75, v74
	s_nop 1
	v_permlane16_swap_b32_e32 v74, v75
	s_waitcnt lgkmcnt(0)
	v_add_f32_e32 v74, v74, v75
	v_mov_b32_e32 v75, v74
	s_nop 1
	v_permlane32_swap_b32_e32 v74, v75
	s_waitcnt lgkmcnt(0)
	v_add_f32_e32 v74, v74, v75
	v_fmamk_f32 v74, v74, 0x3a800000, v204
	v_cmp_gt_f32_e32 vcc, s11, v74
	v_mul_f32_e32 v75, 0x4f800000, v74
	s_nop 0
	v_cndmask_b32_e32 v74, v74, v75, vcc
	v_sqrt_f32_e32 v75, v74
	s_nop 0
	v_add_u32_e32 v76, -1, v75
	v_fma_f32 v77, -v76, v75, v74
	v_cmp_ge_f32_e64 s[2:3], 0, v77
	v_add_u32_e32 v77, 1, v75
	s_nop 0
	v_cndmask_b32_e64 v76, v75, v76, s[2:3]
	v_fma_f32 v75, -v77, v75, v74
	v_cmp_lt_f32_e64 s[2:3], 0, v75
	s_nop 1
	v_cndmask_b32_e64 v75, v76, v77, s[2:3]
	v_mul_f32_e32 v76, 0x37800000, v75
	v_cndmask_b32_e32 v75, v75, v76, vcc
	v_cmp_class_f32_e32 vcc, v74, v205
	s_nop 1
	v_cndmask_b32_e32 v74, v75, v74, vcc
	v_div_scale_f32 v75, s[0:1], v74, v74, 1.0
	v_rcp_f32_e32 v76, v75
	s_mov_b32 s0, 0xb0000
	v_fma_f32 v77, -v75, v76, 1.0
	v_fmac_f32_e32 v76, v77, v76
	v_div_scale_f32 v77, vcc, 1.0, v74, 1.0
	v_mul_f32_e32 v78, v77, v76
	v_fma_f32 v79, -v75, v78, v77
	v_fmac_f32_e32 v78, v79, v76
	v_fma_f32 v75, -v75, v78, v77
	v_div_fmas_f32 v75, v75, v76, v78
	v_div_fixup_f32 v74, v75, v74, 1.0
	v_mul_f32_e32 v75, 0xbfb8aa3b, v74
	v_mul_f32_e32 v76, v62, v75
	v_exp_f32_e32 v76, v76
	v_mul_f32_e32 v74, v74, v74
	v_add_f32_e32 v76, 1.0, v76
	v_rcp_f32_e32 v76, v76
	s_nop 0
	v_mul_f32_e32 v76, v74, v76
	v_mul_f32_e32 v66, v66, v76
	v_mul_f32_e32 v62, v62, v66
	v_mul_f32_e32 v66, v63, v75
	v_exp_f32_e32 v66, v66
	s_nop 0
	v_add_f32_e32 v66, 1.0, v66
	v_rcp_f32_e32 v66, v66
	s_nop 0
	v_mul_f32_e32 v66, v74, v66
	v_mul_f32_e32 v66, v67, v66
	v_mul_f32_e32 v63, v63, v66
	v_mul_f32_e32 v66, v64, v75
	v_exp_f32_e32 v66, v66
	s_nop 0
	v_add_f32_e32 v66, 1.0, v66
	v_rcp_f32_e32 v66, v66
	s_nop 0
	v_mul_f32_e32 v66, v74, v66
	v_mul_f32_e32 v66, v68, v66
	v_mul_f32_e32 v64, v64, v66
	v_mul_f32_e32 v66, v65, v75
	v_exp_f32_e32 v66, v66
	s_nop 0
	v_add_f32_e32 v66, 1.0, v66
	v_rcp_f32_e32 v66, v66
	s_nop 0
	v_mul_f32_e32 v66, v74, v66
	v_mul_f32_e32 v66, v69, v66
	v_mul_f32_e32 v65, v65, v66
	v_mul_f32_e32 v66, v54, v75
	v_exp_f32_e32 v66, v66
	s_nop 0
	v_add_f32_e32 v66, 1.0, v66
	v_rcp_f32_e32 v66, v66
	s_nop 0
	v_mul_f32_e32 v66, v74, v66
	v_mul_f32_e32 v58, v58, v66
	v_mul_f32_e32 v58, v54, v58
	v_mul_f32_e32 v54, v55, v75
	v_exp_f32_e32 v54, v54
	s_nop 0
	v_add_f32_e32 v54, 1.0, v54
	v_rcp_f32_e32 v54, v54
	s_nop 0
	v_mul_f32_e32 v54, v74, v54
	v_mul_f32_e32 v54, v59, v54
	v_mul_f32_e32 v59, v55, v54
	v_mul_f32_e32 v54, v56, v75
	v_exp_f32_e32 v54, v54
	s_nop 0
	v_add_f32_e32 v54, 1.0, v54
	v_rcp_f32_e32 v54, v54
	s_nop 0
	v_mul_f32_e32 v54, v74, v54
	v_mul_f32_e32 v54, v60, v54
	v_mul_f32_e32 v60, v56, v54
	v_mul_f32_e32 v54, v57, v75
	v_exp_f32_e32 v54, v54
	s_nop 0
	v_add_f32_e32 v54, 1.0, v54
	v_rcp_f32_e32 v54, v54
	s_nop 0
	v_mul_f32_e32 v54, v74, v54
	v_mul_f32_e32 v54, v61, v54
	v_mul_f32_e32 v57, v57, v54
	v_cvt_pk_bf16_f32 v54, v62, v63
	v_cvt_pk_bf16_f32 v55, v64, v65
	v_cvt_pk_bf16_f32 v56, v58, v59
	v_add_co_u32_e32 v58, vcc, s0, v158
	v_cvt_pk_bf16_f32 v57, v60, v57
	s_nop 1
	v_addc_co_u32_e32 v59, vcc, 0, v159, vcc
	global_store_dwordx4 v[58:59], v[54:57], off
	s_waitcnt vmcnt(7)
	s_nop 0
	v_add_f32_e32 v54, v90, v91
	v_add_f32_e32 v55, v92, v93
	v_add_f32_e32 v54, v54, v55
	v_mov_b32_e32 v55, v54
	s_nop 1
	v_permlane16_swap_b32_e32 v54, v55
	s_waitcnt lgkmcnt(0)
	v_add_f32_e32 v54, v54, v55
	v_mov_b32_e32 v55, v54
	s_nop 1
	v_permlane32_swap_b32_e32 v54, v55
	s_waitcnt lgkmcnt(0)
	v_add_f32_e32 v54, v54, v55
	v_fmamk_f32 v54, v54, 0x3a800000, v204
	v_cmp_gt_f32_e32 vcc, s11, v54
	v_mul_f32_e32 v55, 0x4f800000, v54
	s_nop 0
	v_cndmask_b32_e32 v54, v54, v55, vcc
	v_sqrt_f32_e32 v55, v54
	s_nop 0
	v_add_u32_e32 v56, -1, v55
	v_fma_f32 v57, -v56, v55, v54
	v_cmp_ge_f32_e64 s[2:3], 0, v57
	v_add_u32_e32 v57, 1, v55
	s_nop 0
	v_cndmask_b32_e64 v56, v55, v56, s[2:3]
	v_fma_f32 v55, -v57, v55, v54
	v_cmp_lt_f32_e64 s[2:3], 0, v55
	s_nop 1
	v_cndmask_b32_e64 v55, v56, v57, s[2:3]
	v_mul_f32_e32 v56, 0x37800000, v55
	v_cndmask_b32_e32 v55, v55, v56, vcc
	v_cmp_class_f32_e32 vcc, v54, v205
	s_nop 1
	v_cndmask_b32_e32 v54, v55, v54, vcc
	v_div_scale_f32 v55, s[0:1], v54, v54, 1.0
	v_rcp_f32_e32 v56, v55
	s_mov_b32 s0, 0xc6000
	v_fma_f32 v57, -v55, v56, 1.0
	v_fmac_f32_e32 v56, v57, v56
	v_div_scale_f32 v57, vcc, 1.0, v54, 1.0
	v_mul_f32_e32 v58, v57, v56
	v_fma_f32 v59, -v55, v58, v57
	v_fmac_f32_e32 v58, v59, v56
	v_fma_f32 v55, -v55, v58, v57
	v_div_fmas_f32 v55, v55, v56, v58
	v_div_fixup_f32 v54, v55, v54, 1.0
	v_mul_f32_e32 v55, 0xbfb8aa3b, v54
	v_mul_f32_e32 v56, v42, v55
	v_exp_f32_e32 v56, v56
	v_mul_f32_e32 v54, v54, v54
	v_add_f32_e32 v56, 1.0, v56
	v_rcp_f32_e32 v56, v56
	s_nop 0
	v_mul_f32_e32 v56, v54, v56
	v_mul_f32_e32 v46, v46, v56
	v_mul_f32_e32 v42, v42, v46
	v_mul_f32_e32 v46, v43, v55
	v_exp_f32_e32 v46, v46
	s_nop 0
	v_add_f32_e32 v46, 1.0, v46
	v_rcp_f32_e32 v46, v46
	s_nop 0
	v_mul_f32_e32 v46, v54, v46
	v_mul_f32_e32 v46, v47, v46
	v_mul_f32_e32 v43, v43, v46
	v_mul_f32_e32 v46, v44, v55
	v_exp_f32_e32 v46, v46
	s_nop 0
	v_add_f32_e32 v46, 1.0, v46
	v_rcp_f32_e32 v46, v46
	s_nop 0
	v_mul_f32_e32 v46, v54, v46
	v_mul_f32_e32 v46, v48, v46
	v_mul_f32_e32 v44, v44, v46
	v_mul_f32_e32 v46, v45, v55
	v_exp_f32_e32 v46, v46
	s_nop 0
	v_add_f32_e32 v46, 1.0, v46
	v_rcp_f32_e32 v46, v46
	s_nop 0
	v_mul_f32_e32 v46, v54, v46
	v_mul_f32_e32 v46, v49, v46
	v_mul_f32_e32 v45, v45, v46
	v_mul_f32_e32 v46, v34, v55
	v_exp_f32_e32 v46, v46
	s_nop 0
	v_add_f32_e32 v46, 1.0, v46
	v_rcp_f32_e32 v46, v46
	s_nop 0
	v_mul_f32_e32 v46, v54, v46
	v_mul_f32_e32 v38, v38, v46
	v_mul_f32_e32 v38, v34, v38
	v_mul_f32_e32 v34, v35, v55
	v_exp_f32_e32 v34, v34
	s_nop 0
	v_add_f32_e32 v34, 1.0, v34
	v_rcp_f32_e32 v34, v34
	s_nop 0
	v_mul_f32_e32 v34, v54, v34
	v_mul_f32_e32 v34, v39, v34
	v_mul_f32_e32 v39, v35, v34
	v_mul_f32_e32 v34, v36, v55
	v_exp_f32_e32 v34, v34
	s_nop 0
	v_add_f32_e32 v34, 1.0, v34
	v_rcp_f32_e32 v34, v34
	s_nop 0
	v_mul_f32_e32 v34, v54, v34
	v_mul_f32_e32 v34, v40, v34
	v_mul_f32_e32 v40, v36, v34
	v_mul_f32_e32 v34, v37, v55
	v_exp_f32_e32 v34, v34
	s_nop 0
	v_add_f32_e32 v34, 1.0, v34
	v_rcp_f32_e32 v34, v34
	s_nop 0
	v_mul_f32_e32 v34, v54, v34
	v_mul_f32_e32 v34, v41, v34
	v_mul_f32_e32 v37, v37, v34
	v_cvt_pk_bf16_f32 v34, v42, v43
	v_cvt_pk_bf16_f32 v35, v44, v45
	v_cvt_pk_bf16_f32 v36, v38, v39
	v_add_co_u32_e32 v38, vcc, s0, v158
	v_cvt_pk_bf16_f32 v37, v40, v37
	s_nop 1
	v_addc_co_u32_e32 v39, vcc, 0, v159, vcc
	global_store_dwordx4 v[38:39], v[34:37], off
	s_waitcnt vmcnt(7)
	s_nop 0
	v_add_f32_e32 v34, v70, v71
	v_add_f32_e32 v35, v72, v73
	v_add_f32_e32 v34, v34, v35
	v_mov_b32_e32 v35, v34
	s_nop 1
	v_permlane16_swap_b32_e32 v34, v35
	s_waitcnt lgkmcnt(0)
	v_add_f32_e32 v34, v34, v35
	v_mov_b32_e32 v35, v34
	s_nop 1
	v_permlane32_swap_b32_e32 v34, v35
	s_waitcnt lgkmcnt(0)
	v_add_f32_e32 v34, v34, v35
	v_fmamk_f32 v34, v34, 0x3a800000, v204
	v_cmp_gt_f32_e32 vcc, s11, v34
	v_mul_f32_e32 v35, 0x4f800000, v34
	s_nop 0
	v_cndmask_b32_e32 v34, v34, v35, vcc
	v_sqrt_f32_e32 v35, v34
	s_nop 0
	v_add_u32_e32 v36, -1, v35
	v_fma_f32 v37, -v36, v35, v34
	v_cmp_ge_f32_e64 s[2:3], 0, v37
	v_add_u32_e32 v37, 1, v35
	s_nop 0
	v_cndmask_b32_e64 v36, v35, v36, s[2:3]
	v_fma_f32 v35, -v37, v35, v34
	v_cmp_lt_f32_e64 s[2:3], 0, v35
	s_nop 1
	v_cndmask_b32_e64 v35, v36, v37, s[2:3]
	v_mul_f32_e32 v36, 0x37800000, v35
	v_cndmask_b32_e32 v35, v35, v36, vcc
	v_cmp_class_f32_e32 vcc, v34, v205
	s_nop 1
	v_cndmask_b32_e32 v34, v35, v34, vcc
	v_div_scale_f32 v35, s[0:1], v34, v34, 1.0
	v_rcp_f32_e32 v36, v35
	s_mov_b32 s0, 0xdc000
	v_fma_f32 v37, -v35, v36, 1.0
	v_fmac_f32_e32 v36, v37, v36
	v_div_scale_f32 v37, vcc, 1.0, v34, 1.0
	v_mul_f32_e32 v38, v37, v36
	v_fma_f32 v39, -v35, v38, v37
	v_fmac_f32_e32 v38, v39, v36
	v_fma_f32 v35, -v35, v38, v37
	v_div_fmas_f32 v35, v35, v36, v38
	v_div_fixup_f32 v34, v35, v34, 1.0
	v_mul_f32_e32 v35, 0xbfb8aa3b, v34
	v_mul_f32_e32 v36, v26, v35
	v_exp_f32_e32 v36, v36
	v_mul_f32_e32 v34, v34, v34
	v_add_f32_e32 v36, 1.0, v36
	v_rcp_f32_e32 v36, v36
	s_nop 0
	v_mul_f32_e32 v36, v34, v36
	v_mul_f32_e32 v30, v30, v36
	v_mul_f32_e32 v26, v26, v30
	v_mul_f32_e32 v30, v27, v35
	v_exp_f32_e32 v30, v30
	s_nop 0
	v_add_f32_e32 v30, 1.0, v30
	v_rcp_f32_e32 v30, v30
	s_nop 0
	v_mul_f32_e32 v30, v34, v30
	v_mul_f32_e32 v30, v31, v30
	v_mul_f32_e32 v27, v27, v30
	v_mul_f32_e32 v30, v28, v35
	v_exp_f32_e32 v30, v30
	s_nop 0
	v_add_f32_e32 v30, 1.0, v30
	v_rcp_f32_e32 v30, v30
	s_nop 0
	v_mul_f32_e32 v30, v34, v30
	v_mul_f32_e32 v30, v32, v30
	v_mul_f32_e32 v28, v28, v30
	v_mul_f32_e32 v30, v29, v35
	v_exp_f32_e32 v30, v30
	s_nop 0
	v_add_f32_e32 v30, 1.0, v30
	v_rcp_f32_e32 v30, v30
	s_nop 0
	v_mul_f32_e32 v30, v34, v30
	v_mul_f32_e32 v30, v33, v30
	v_mul_f32_e32 v29, v29, v30
	v_mul_f32_e32 v30, v18, v35
	v_exp_f32_e32 v30, v30
	s_nop 0
	v_add_f32_e32 v30, 1.0, v30
	v_rcp_f32_e32 v30, v30
	s_nop 0
	v_mul_f32_e32 v30, v34, v30
	v_mul_f32_e32 v22, v22, v30
	v_mul_f32_e32 v22, v18, v22
	v_mul_f32_e32 v18, v19, v35
	v_exp_f32_e32 v18, v18
	s_nop 0
	v_add_f32_e32 v18, 1.0, v18
	v_rcp_f32_e32 v18, v18
	s_nop 0
	v_mul_f32_e32 v18, v34, v18
	v_mul_f32_e32 v18, v23, v18
	v_mul_f32_e32 v23, v19, v18
	v_mul_f32_e32 v18, v20, v35
	v_exp_f32_e32 v18, v18
	s_nop 0
	v_add_f32_e32 v18, 1.0, v18
	v_rcp_f32_e32 v18, v18
	s_nop 0
	v_mul_f32_e32 v18, v34, v18
	v_mul_f32_e32 v18, v24, v18
	v_mul_f32_e32 v24, v20, v18
	v_mul_f32_e32 v18, v21, v35
	v_exp_f32_e32 v18, v18
	s_nop 0
	v_add_f32_e32 v18, 1.0, v18
	v_rcp_f32_e32 v18, v18
	s_nop 0
	v_mul_f32_e32 v18, v34, v18
	v_mul_f32_e32 v18, v25, v18
	v_mul_f32_e32 v21, v21, v18
	v_cvt_pk_bf16_f32 v18, v26, v27
	v_cvt_pk_bf16_f32 v19, v28, v29
	v_cvt_pk_bf16_f32 v20, v22, v23
	v_add_co_u32_e32 v22, vcc, s0, v158
	v_cvt_pk_bf16_f32 v21, v24, v21
	s_nop 1
	v_addc_co_u32_e32 v23, vcc, 0, v159, vcc
	global_store_dwordx4 v[22:23], v[18:21], off
	s_waitcnt vmcnt(7)
	s_nop 0
	v_add_f32_e32 v18, v50, v51
	v_add_f32_e32 v19, v52, v53
	v_add_f32_e32 v18, v18, v19
	v_mov_b32_e32 v19, v18
	s_nop 1
	v_permlane16_swap_b32_e32 v18, v19
	s_waitcnt lgkmcnt(0)
	v_add_f32_e32 v18, v18, v19
	v_mov_b32_e32 v19, v18
	s_nop 1
	v_permlane32_swap_b32_e32 v18, v19
	s_waitcnt lgkmcnt(0)
	v_add_f32_e32 v18, v18, v19
	v_fmamk_f32 v18, v18, 0x3a800000, v204
	v_cmp_gt_f32_e32 vcc, s11, v18
	v_mul_f32_e32 v19, 0x4f800000, v18
	s_nop 0
	v_cndmask_b32_e32 v18, v18, v19, vcc
	v_sqrt_f32_e32 v19, v18
	s_nop 0
	v_add_u32_e32 v20, -1, v19
	v_fma_f32 v21, -v20, v19, v18
	v_cmp_ge_f32_e64 s[2:3], 0, v21
	v_add_u32_e32 v21, 1, v19
	s_nop 0
	v_cndmask_b32_e64 v20, v19, v20, s[2:3]
	v_fma_f32 v19, -v21, v19, v18
	v_cmp_lt_f32_e64 s[2:3], 0, v19
	s_nop 1
	v_cndmask_b32_e64 v19, v20, v21, s[2:3]
	v_mul_f32_e32 v20, 0x37800000, v19
	v_cndmask_b32_e32 v19, v19, v20, vcc
	v_cmp_class_f32_e32 vcc, v18, v205
	s_mov_b64 s[2:3], -1
	s_nop 0
	v_cndmask_b32_e32 v18, v19, v18, vcc
	v_div_scale_f32 v19, s[0:1], v18, v18, 1.0
	v_rcp_f32_e32 v20, v19
	s_nop 0
	v_fma_f32 v21, -v19, v20, 1.0
	v_fmac_f32_e32 v20, v21, v20
	v_div_scale_f32 v21, vcc, 1.0, v18, 1.0
	v_mul_f32_e32 v22, v21, v20
	v_fma_f32 v23, -v19, v22, v21
	v_fmac_f32_e32 v22, v23, v20
	v_fma_f32 v19, -v19, v22, v21
	v_div_fmas_f32 v19, v19, v20, v22
	v_div_fixup_f32 v18, v19, v18, 1.0
	v_mul_f32_e32 v19, 0xbfb8aa3b, v18
	v_mul_f32_e32 v20, v10, v19
	v_exp_f32_e32 v20, v20
	v_mul_f32_e32 v18, v18, v18
	v_add_f32_e32 v20, 1.0, v20
	v_rcp_f32_e32 v20, v20
	s_nop 0
	v_mul_f32_e32 v20, v18, v20
	v_mul_f32_e32 v14, v14, v20
	v_mul_f32_e32 v10, v10, v14
	v_mul_f32_e32 v14, v11, v19
	v_exp_f32_e32 v14, v14
	s_nop 0
	v_add_f32_e32 v14, 1.0, v14
	v_rcp_f32_e32 v14, v14
	s_nop 0
	v_mul_f32_e32 v14, v18, v14
	v_mul_f32_e32 v14, v15, v14
	v_mul_f32_e32 v11, v11, v14
	v_mul_f32_e32 v14, v12, v19
	v_exp_f32_e32 v14, v14
	s_nop 0
	v_add_f32_e32 v14, 1.0, v14
	v_rcp_f32_e32 v14, v14
	s_nop 0
	v_mul_f32_e32 v14, v18, v14
	v_mul_f32_e32 v14, v16, v14
	v_mul_f32_e32 v12, v12, v14
	v_mul_f32_e32 v14, v13, v19
	v_exp_f32_e32 v14, v14
	s_nop 0
	v_add_f32_e32 v14, 1.0, v14
	v_rcp_f32_e32 v14, v14
	s_nop 0
	v_mul_f32_e32 v14, v18, v14
	v_mul_f32_e32 v14, v17, v14
	v_mul_f32_e32 v13, v13, v14
	v_mul_f32_e32 v14, v2, v19
	v_exp_f32_e32 v14, v14
	s_nop 0
	v_add_f32_e32 v14, 1.0, v14
	v_rcp_f32_e32 v14, v14
	s_nop 0
	v_mul_f32_e32 v14, v18, v14
	v_mul_f32_e32 v6, v6, v14
	v_mul_f32_e32 v6, v2, v6
	v_mul_f32_e32 v2, v3, v19
	v_exp_f32_e32 v2, v2
	s_nop 0
	v_add_f32_e32 v2, 1.0, v2
	v_rcp_f32_e32 v2, v2
	s_nop 0
	v_mul_f32_e32 v2, v18, v2
	v_mul_f32_e32 v2, v7, v2
	v_mul_f32_e32 v7, v3, v2
	v_mul_f32_e32 v2, v4, v19
	v_exp_f32_e32 v2, v2
	s_nop 0
	v_add_f32_e32 v2, 1.0, v2
	v_rcp_f32_e32 v2, v2
	s_nop 0
	v_mul_f32_e32 v2, v18, v2
	v_mul_f32_e32 v2, v8, v2
	v_mul_f32_e32 v8, v4, v2
	v_mul_f32_e32 v2, v5, v19
	v_exp_f32_e32 v2, v2
	s_nop 0
	v_add_f32_e32 v2, 1.0, v2
	v_rcp_f32_e32 v2, v2
	s_nop 0
	v_mul_f32_e32 v2, v18, v2
	v_mul_f32_e32 v2, v9, v2
	v_mul_f32_e32 v5, v5, v2
	v_cvt_pk_bf16_f32 v2, v10, v11
	v_cvt_pk_bf16_f32 v3, v12, v13
	v_cvt_pk_bf16_f32 v4, v6, v7
	v_add_co_u32_e32 v6, vcc, 0xf2000, v158
	v_cvt_pk_bf16_f32 v5, v8, v5
	s_nop 1
	v_addc_co_u32_e32 v7, vcc, 0, v159, vcc
	s_and_b64 vcc, exec, s[40:41]
	global_store_dwordx4 v[6:7], v[2:5], off
	s_cbranch_vccnz .LBB0_1933
	s_andn2_b64 vcc, exec, s[4:5]
	s_cbranch_vccnz .LBB0_1932
	s_barrier
	s_branch .LBB0_1932

.LBB0_1962:
	s_ashr_i32 s5, s4, 31
	s_lshl_b64 s[0:1], s[4:5], 8
	s_add_u32 s0, s0, s54
	s_addc_u32 s1, s1, s64
	v_mov_b32_e32 v134, v167
	v_mov_b32_e32 v135, v168
	s_lshl_b64 s[4:5], s[0:1], 6
	v_readlane_b32 s18, v250, 7
	v_readlane_b32 s19, v250, 8
	s_add_u32 s4, s18, s4
	v_lshlrev_b32_e32 v130, 6, v134
	s_addc_u32 s5, s19, s5
	v_lshl_add_u32 v202, v135, 4, v130
	global_load_dwordx4 v[130:133], v202, s[4:5]
	global_load_dwordx4 v[158:161], v202, s[4:5] offset:1024
	v_and_b32_e32 v137, 64, v248
	v_xor_b32_e32 v136, 16, v248
	v_add_u32_e32 v137, 64, v137
	v_cmp_lt_i32_e32 vcc, v136, v137
	v_xor_b32_e32 v138, 32, v248
	s_movk_i32 s13, 0xb00
	v_cndmask_b32_e32 v136, v248, v136, vcc
	v_lshlrev_b32_e32 v157, 2, v136
	v_cmp_lt_i32_e32 vcc, v138, v137
	v_mul_lo_u32 v134, v134, s13
	s_mul_hi_u32 s13, s0, 0xb00
	v_cndmask_b32_e32 v137, v248, v138, vcc
	v_lshlrev_b32_e32 v156, 2, v137
	s_mulk_i32 s1, 0xb00
	s_mulk_i32 s0, 0xb00
	v_lshl_add_u32 v154, v135, 3, v134
	s_add_i32 s13, s13, s1
	v_readlane_b32 s18, v250, 9
	v_lshl_add_u64 v[134:135], s[4:5], 0, v[202:203]
	global_load_dwordx4 v[150:153], v202, s[4:5] offset:2048
	global_load_dwordx4 v[146:149], v202, s[4:5] offset:3072
	s_movk_i32 s5, 0x2000
	v_readlane_b32 s19, v250, 10
	s_add_u32 s0, s18, s0
	v_add_co_u32_e32 v172, vcc, s5, v134
	s_addc_u32 s1, s19, s13
	s_nop 0
	v_addc_co_u32_e32 v173, vcc, 0, v135, vcc
	s_mov_b32 s13, 0xf800000
	s_lshl_b32 s4, s16, 7
	s_ashr_i32 s5, s4, 31
	s_add_u32 s0, s0, s4
	s_addc_u32 s1, s1, s5
	s_add_u32 s22, s0, s55
	s_addc_u32 s23, s1, 0
	s_mov_b32 s15, 0xf800000
	s_waitcnt vmcnt(3)
	v_add_f32_e32 v130, v130, v131
	v_add_f32_e32 v131, v132, v133
	v_add_f32_e32 v155, v130, v131
	v_mov_b32_e32 v171, v155
	s_nop 1
	v_permlane16_swap_b32_e32 v155, v171
	s_waitcnt vmcnt(2)
	v_add_f32_e32 v158, v158, v159
	v_add_f32_e32 v159, v160, v161
	v_add_f32_e32 v158, v158, v159
	global_load_dwordx4 v[142:145], v[172:173], off
	global_load_dwordx4 v[138:141], v[172:173], off offset:1024
	global_load_dwordx4 v[134:137], v[172:173], off offset:2048
	global_load_dwordx4 v[130:133], v[172:173], off offset:3072
	s_waitcnt lgkmcnt(0)
	v_add_f32_e32 v155, v155, v171
	v_mov_b32_e32 v171, v155
	s_nop 1
	v_permlane32_swap_b32_e32 v155, v171
	s_waitcnt lgkmcnt(0)
	v_add_f32_e32 v155, v155, v171
	v_fmamk_f32 v155, v155, 0x3a800000, v204
	v_mul_f32_e32 v171, 0x4f800000, v155
	v_cmp_gt_f32_e32 vcc, s13, v155
	s_nop 1
	v_cndmask_b32_e32 v155, v155, v171, vcc
	v_sqrt_f32_e32 v171, v155
	s_nop 0
	v_add_u32_e32 v159, -1, v171
	v_add_u32_e32 v160, 1, v171
	v_fma_f32 v161, -v159, v171, v155
	v_fma_f32 v172, -v160, v171, v155
	v_cmp_ge_f32_e64 s[4:5], 0, v161
	ds_bpermute_b32 v161, v157, v158
	s_nop 0
	v_cndmask_b32_e64 v159, v171, v159, s[4:5]
	v_cmp_lt_f32_e64 s[4:5], 0, v172
	s_nop 1
	v_cndmask_b32_e64 v159, v159, v160, s[4:5]
	v_mul_f32_e32 v160, 0x37800000, v159
	v_cndmask_b32_e32 v159, v159, v160, vcc
	v_cmp_class_f32_e32 vcc, v155, v205
	s_nop 1
	v_cndmask_b32_e32 v155, v159, v155, vcc
	v_div_scale_f32 v159, s[0:1], v155, v155, 1.0
	v_rcp_f32_e32 v160, v159
	v_div_scale_f32 v171, vcc, 1.0, v155, 1.0
	v_fma_f32 v172, -v159, v160, 1.0
	v_fmac_f32_e32 v160, v172, v160
	v_mul_f32_e32 v172, v171, v160
	v_fma_f32 v173, -v159, v172, v171
	v_fmac_f32_e32 v172, v173, v160
	v_fma_f32 v159, -v159, v172, v171
	v_div_fmas_f32 v159, v159, v160, v172
	v_div_fixup_f32 v155, v159, v155, 1.0
	v_mul_f32_e32 v155, 0x3d000000, v155
	v_mul_f32_e32 v159, 0xbfb8aa3b, v155
	v_mul_f32_e32 v160, v114, v159
	v_mul_f32_e32 v172, v116, v159
	v_mul_f32_e32 v171, v115, v159
	v_mul_f32_e32 v173, v117, v159
	v_mul_f32_e32 v176, v120, v159
	v_exp_f32_e32 v160, v160
	v_exp_f32_e32 v172, v172
	v_exp_f32_e32 v171, v171
	v_exp_f32_e32 v173, v173
	v_exp_f32_e32 v176, v176
	v_add_f32_e32 v160, 1.0, v160
	v_add_f32_e32 v172, 1.0, v172
	v_add_f32_e32 v171, 1.0, v171
	v_add_f32_e32 v173, 1.0, v173
	v_add_f32_e32 v176, 1.0, v176
	v_rcp_f32_e32 v160, v160
	v_rcp_f32_e32 v172, v172
	v_rcp_f32_e32 v171, v171
	v_rcp_f32_e32 v173, v173
	v_rcp_f32_e32 v176, v176
	v_mul_f32_e32 v174, v118, v159
	v_mul_f32_e32 v175, v119, v159
	v_mul_f32_e32 v159, v121, v159
	v_mul_f32_e32 v155, v155, v155
	v_exp_f32_e32 v159, v159
	v_mul_f32_e32 v160, v155, v160
	v_mul_f32_e32 v172, v155, v172
	v_mul_f32_e32 v171, v155, v171
	v_mul_f32_e32 v173, v155, v173
	v_mul_f32_e32 v176, v155, v176
	v_mul_f32_e32 v98, v98, v160
	v_mul_f32_e32 v100, v100, v172
	v_mul_f32_e32 v99, v99, v171
	v_mul_f32_e32 v101, v101, v173
	v_mul_f32_e32 v98, v114, v98
	v_mul_f32_e32 v114, v116, v100
	v_mul_f32_e32 v100, v104, v176
	s_waitcnt lgkmcnt(0)
	v_add_f32_e32 v104, v158, v161
	v_mul_f32_e32 v99, v115, v99
	v_mul_f32_e32 v115, v117, v101
	v_add_f32_e32 v101, 1.0, v159
	v_mov_b32_e32 v116, v104
	s_nop 1
	v_permlane32_swap_b32_e32 v104, v116
	v_rcp_f32_e32 v101, v101
	v_exp_f32_e32 v174, v174
	v_exp_f32_e32 v175, v175
	v_mul_f32_e32 v117, v120, v100
	v_mul_f32_e32 v100, v155, v101
	s_waitcnt lgkmcnt(0)
	v_add_f32_e32 v101, v104, v116
	v_fmamk_f32 v101, v101, 0x3a800000, v204
	v_mul_f32_e32 v104, 0x4f800000, v101
	v_cmp_gt_f32_e32 vcc, s13, v101
	v_add_f32_e32 v174, 1.0, v174
	v_add_f32_e32 v175, 1.0, v175
	v_cndmask_b32_e32 v104, v101, v104, vcc
	v_rcp_f32_e32 v174, v174
	v_rcp_f32_e32 v175, v175
	v_sqrt_f32_e32 v116, v104
	v_mul_f32_e32 v105, v105, v100
	v_mov_b32_e32 v100, v203
	v_mul_f32_e32 v174, v155, v174
	v_mul_f32_e32 v175, v155, v175
	v_cvt_pk_fp8_f32 v100, v98, v99
	v_add_u32_e32 v98, -1, v116
	v_mul_f32_e32 v102, v102, v174
	v_mul_f32_e32 v103, v103, v175
	v_fma_f32 v99, -v98, v116, v104
	v_mul_f32_e32 v102, v118, v102
	v_mul_f32_e32 v103, v119, v103
	v_mov_b32_e32 v101, v203
	v_cmp_ge_f32_e64 s[4:5], 0, v99
	v_add_u32_e32 v99, 1, v116
	v_cvt_pk_fp8_f32 v101, v102, v103
	v_fma_f32 v102, -v99, v116, v104
	v_cndmask_b32_e64 v98, v116, v98, s[4:5]
	v_cmp_lt_f32_e64 s[4:5], 0, v102
	v_mul_f32_e32 v103, v121, v105
	v_cvt_pk_fp8_f32 v101, v117, v103 op_sel:[0,0,1]
	v_cndmask_b32_e64 v98, v98, v99, s[4:5]
	v_mul_f32_e32 v99, 0x37800000, v98
	v_cndmask_b32_e32 v98, v98, v99, vcc
	v_cmp_class_f32_e32 vcc, v104, v205
	v_cvt_pk_fp8_f32 v100, v114, v115 op_sel:[0,0,1]
	v_mov_b32_e32 v155, v203
	v_cndmask_b32_e32 v98, v98, v104, vcc
	v_div_scale_f32 v99, s[0:1], v98, v98, 1.0
	v_rcp_f32_e32 v102, v99
	global_store_dwordx2 v154, v[100:101], s[22:23]
	v_fma_f32 v103, -v99, v102, 1.0
	v_fmac_f32_e32 v102, v103, v102
	v_div_scale_f32 v103, vcc, 1.0, v98, 1.0
	v_mul_f32_e32 v104, v103, v102
	v_fma_f32 v105, -v99, v104, v103
	v_fmac_f32_e32 v104, v105, v102
	v_fma_f32 v99, -v99, v104, v103
	v_div_fmas_f32 v99, v99, v102, v104
	v_div_fixup_f32 v98, v99, v98, 1.0
	v_mul_f32_e32 v102, 0x3d000000, v98
	v_mul_f32_e32 v103, 0xbfb8aa3b, v102
	v_mul_f32_e32 v98, v122, v103
	v_exp_f32_e32 v104, v98
	v_mul_f32_e32 v101, v123, v103
	v_exp_f32_e32 v101, v101
	v_mul_f32_e32 v102, v102, v102
	v_add_f32_e32 v100, 1.0, v104
	v_rcp_f32_e32 v100, v100
	v_add_f32_e32 v101, 1.0, v101
	v_mul_f32_e32 v104, v124, v103
	v_rcp_f32_e32 v101, v101
	v_exp_f32_e32 v104, v104
	v_mul_f32_e32 v100, v102, v100
	v_mul_f32_e32 v100, v106, v100
	v_mul_f32_e32 v105, v122, v100
	v_mul_f32_e32 v100, v102, v101
	v_add_f32_e32 v101, 1.0, v104
	v_mul_f32_e32 v104, v125, v103
	v_rcp_f32_e32 v101, v101
	v_exp_f32_e32 v104, v104
	v_mul_f32_e32 v100, v107, v100
	v_mul_f32_e32 v106, v123, v100
	v_mul_f32_e32 v100, v102, v101
	v_add_f32_e32 v101, 1.0, v104
	v_mul_f32_e32 v104, v126, v103
	v_rcp_f32_e32 v101, v101
	v_exp_f32_e32 v104, v104
	v_mul_f32_e32 v100, v108, v100
	v_mul_f32_e32 v107, v124, v100
	v_mul_f32_e32 v100, v102, v101
	v_add_f32_e32 v101, 1.0, v104
	v_mul_f32_e32 v104, v127, v103
	v_rcp_f32_e32 v101, v101
	v_exp_f32_e32 v104, v104
	v_mul_f32_e32 v100, v109, v100
	v_mul_f32_e32 v108, v125, v100
	v_mul_f32_e32 v100, v102, v101
	v_add_f32_e32 v101, 1.0, v104
	v_rcp_f32_e32 v101, v101
	v_mul_f32_e32 v100, v110, v100
	v_mul_f32_e32 v104, v126, v100
	v_mul_f32_e32 v100, v128, v103
	v_mul_f32_e32 v101, v102, v101
	v_mul_f32_e32 v101, v111, v101
	v_mul_f32_e32 v109, v127, v101
	v_mul_f32_e32 v101, v129, v103
	s_waitcnt vmcnt(6)
	v_add_f32_e32 v103, v150, v151
	v_add_f32_e32 v110, v152, v153
	v_add_f32_e32 v103, v103, v110
	v_exp_f32_e32 v100, v100
	v_mov_b32_e32 v110, v103
	s_nop 1
	v_permlane16_swap_b32_e32 v103, v110
	v_exp_f32_e32 v101, v101
	v_lshl_add_u64 v[98:99], s[22:23], 0, v[154:155]
	v_add_f32_e32 v100, 1.0, v100
	v_rcp_f32_e32 v100, v100
	s_waitcnt lgkmcnt(0)
	v_add_f32_e32 v103, v103, v110
	v_add_f32_e32 v101, 1.0, v101
	v_mov_b32_e32 v110, v103
	s_nop 1
	v_permlane32_swap_b32_e32 v103, v110
	v_rcp_f32_e32 v101, v101
	v_mul_f32_e32 v100, v102, v100
	v_mul_f32_e32 v100, v112, v100
	v_mul_f32_e32 v111, v128, v100
	v_mul_f32_e32 v100, v102, v101
	s_waitcnt lgkmcnt(0)
	v_add_f32_e32 v101, v103, v110
	v_fmamk_f32 v101, v101, 0x3a800000, v204
	v_mul_f32_e32 v103, 0x4f800000, v101
	v_cmp_gt_f32_e32 vcc, s13, v101
	v_mul_f32_e32 v102, v113, v100
	v_mov_b32_e32 v100, v203
	v_cndmask_b32_e32 v103, v101, v103, vcc
	v_sqrt_f32_e32 v110, v103
	v_mov_b32_e32 v101, v203
	v_cvt_pk_fp8_f32 v101, v104, v109
	v_cvt_pk_fp8_f32 v100, v105, v106
	v_add_u32_e32 v104, -1, v110
	v_fma_f32 v105, -v104, v110, v103
	v_cmp_ge_f32_e64 s[4:5], 0, v105
	v_add_u32_e32 v105, 1, v110
	v_fma_f32 v106, -v105, v110, v103
	v_cndmask_b32_e64 v104, v110, v104, s[4:5]
	v_cmp_lt_f32_e64 s[4:5], 0, v106
	v_mul_f32_e32 v102, v129, v102
	v_cvt_pk_fp8_f32 v101, v111, v102 op_sel:[0,0,1]
	v_cndmask_b32_e64 v104, v104, v105, s[4:5]
	v_mul_f32_e32 v105, 0x37800000, v104
	v_cndmask_b32_e32 v104, v104, v105, vcc
	v_cmp_class_f32_e32 vcc, v103, v205
	v_cvt_pk_fp8_f32 v100, v107, v108 op_sel:[0,0,1]
	s_nop 0
	v_cndmask_b32_e32 v103, v104, v103, vcc
	v_div_scale_f32 v104, s[0:1], v103, v103, 1.0
	v_rcp_f32_e32 v105, v104
	s_mov_b32 s0, 0xb000
	v_fma_f32 v102, -v104, v105, 1.0
	v_fmac_f32_e32 v105, v102, v105
	v_div_scale_f32 v102, vcc, 1.0, v103, 1.0
	v_mul_f32_e32 v106, v102, v105
	v_fma_f32 v107, -v104, v106, v102
	v_fmac_f32_e32 v106, v107, v105
	v_fma_f32 v102, -v104, v106, v102
	v_div_fmas_f32 v102, v102, v105, v106
	v_div_fixup_f32 v102, v102, v103, 1.0
	v_mul_f32_e32 v104, 0x3d000000, v102
	v_mul_f32_e32 v105, 0xbfb8aa3b, v104
	v_mul_f32_e32 v102, v82, v105
	v_exp_f32_e32 v106, v102
	v_add_co_u32_e32 v102, vcc, s0, v98
	s_nop 1
	v_addc_co_u32_e32 v103, vcc, 0, v99, vcc
	global_store_dwordx2 v[102:103], v[100:101], off
	v_add_f32_e32 v100, 1.0, v106
	v_rcp_f32_e32 v100, v100
	v_mul_f32_e32 v101, v83, v105
	v_exp_f32_e32 v101, v101
	v_mul_f32_e32 v102, v104, v104
	v_mul_f32_e32 v100, v102, v100
	v_mul_f32_e32 v66, v66, v100
	v_add_f32_e32 v100, 1.0, v101
	v_rcp_f32_e32 v100, v100
	v_mul_f32_e32 v101, v84, v105
	v_exp_f32_e32 v101, v101
	v_mul_f32_e32 v82, v82, v66
	v_mul_f32_e32 v66, v102, v100
	v_mul_f32_e32 v66, v67, v66
	v_add_f32_e32 v67, 1.0, v101
	v_rcp_f32_e32 v67, v67
	v_mul_f32_e32 v100, v85, v105
	v_exp_f32_e32 v100, v100
	v_mul_f32_e32 v83, v83, v66
	v_mul_f32_e32 v66, v102, v67
	v_mul_f32_e32 v66, v68, v66
	v_add_f32_e32 v67, 1.0, v100
	v_mul_f32_e32 v68, v86, v105
	v_rcp_f32_e32 v67, v67
	v_exp_f32_e32 v68, v68
	v_mul_f32_e32 v84, v84, v66
	v_mul_f32_e32 v66, v102, v67
	v_add_f32_e32 v67, 1.0, v68
	v_mul_f32_e32 v68, v87, v105
	v_rcp_f32_e32 v67, v67
	v_exp_f32_e32 v68, v68
	v_mul_f32_e32 v66, v69, v66
	v_mul_f32_e32 v69, v85, v66
	v_mul_f32_e32 v66, v102, v67
	v_add_f32_e32 v67, 1.0, v68
	v_rcp_f32_e32 v67, v67
	v_mul_f32_e32 v66, v70, v66
	v_mul_f32_e32 v68, v86, v66
	v_mul_f32_e32 v66, v88, v105
	v_exp_f32_e32 v66, v66
	v_mul_f32_e32 v67, v102, v67
	v_mul_f32_e32 v67, v71, v67
	s_waitcnt vmcnt(6)
	v_add_f32_e32 v71, v146, v147
	v_add_f32_e32 v85, v148, v149
	v_add_f32_e32 v71, v71, v85
	v_add_f32_e32 v66, 1.0, v66
	v_mov_b32_e32 v85, v71
	s_nop 1
	v_permlane16_swap_b32_e32 v71, v85
	v_mul_f32_e32 v70, v87, v67
	v_rcp_f32_e32 v66, v66
	v_mul_f32_e32 v67, v89, v105
	v_exp_f32_e32 v67, v67
	s_waitcnt lgkmcnt(0)
	v_add_f32_e32 v71, v71, v85
	v_mul_f32_e32 v66, v102, v66
	v_mul_f32_e32 v66, v72, v66
	v_add_f32_e32 v67, 1.0, v67
	v_mov_b32_e32 v72, v71
	s_nop 1
	v_permlane32_swap_b32_e32 v71, v72
	v_rcp_f32_e32 v67, v67
	v_mul_f32_e32 v85, v88, v66
	v_mul_f32_e32 v66, v102, v67
	s_waitcnt lgkmcnt(0)
	v_add_f32_e32 v67, v71, v72
	v_fmamk_f32 v67, v67, 0x3a800000, v204
	v_mul_f32_e32 v71, 0x4f800000, v67
	v_cmp_gt_f32_e32 vcc, s13, v67
	v_mul_f32_e32 v73, v73, v66
	v_mov_b32_e32 v66, v203
	v_cndmask_b32_e32 v71, v67, v71, vcc
	v_sqrt_f32_e32 v72, v71
	v_mov_b32_e32 v67, v203
	v_cvt_pk_fp8_f32 v67, v68, v70
	v_cvt_pk_fp8_f32 v66, v82, v83
	v_add_u32_e32 v68, -1, v72
	v_fma_f32 v70, -v68, v72, v71
	v_cmp_ge_f32_e64 s[4:5], 0, v70
	v_add_u32_e32 v70, 1, v72
	v_cvt_pk_fp8_f32 v66, v84, v69 op_sel:[0,0,1]
	v_cndmask_b32_e64 v68, v72, v68, s[4:5]
	v_fma_f32 v72, -v70, v72, v71
	v_cmp_lt_f32_e64 s[4:5], 0, v72
	v_mul_f32_e32 v72, v89, v73
	v_cvt_pk_fp8_f32 v67, v85, v72 op_sel:[0,0,1]
	v_cndmask_b32_e64 v68, v68, v70, s[4:5]
	v_mul_f32_e32 v70, 0x37800000, v68
	v_cndmask_b32_e32 v68, v68, v70, vcc
	v_cmp_class_f32_e32 vcc, v71, v205
	s_nop 1
	v_cndmask_b32_e32 v68, v68, v71, vcc
	v_div_scale_f32 v70, s[0:1], v68, v68, 1.0
	v_rcp_f32_e32 v71, v70
	s_mov_b32 s0, 0x16000
	v_fma_f32 v69, -v70, v71, 1.0
	v_fmac_f32_e32 v71, v69, v71
	v_div_scale_f32 v69, vcc, 1.0, v68, 1.0
	v_mul_f32_e32 v72, v69, v71
	v_fma_f32 v73, -v70, v72, v69
	v_fmac_f32_e32 v72, v73, v71
	v_fma_f32 v69, -v70, v72, v69
	v_div_fmas_f32 v69, v69, v71, v72
	v_div_fixup_f32 v68, v69, v68, 1.0
	v_mul_f32_e32 v70, 0x3d000000, v68
	v_mul_f32_e32 v71, 0xbfb8aa3b, v70
	v_mul_f32_e32 v68, v90, v71
	v_exp_f32_e32 v72, v68
	v_add_co_u32_e32 v68, vcc, s0, v98
	s_nop 1
	v_addc_co_u32_e32 v69, vcc, 0, v99, vcc
	global_store_dwordx2 v[68:69], v[66:67], off
	v_mul_f32_e32 v67, v91, v71
	v_exp_f32_e32 v67, v67
	v_add_f32_e32 v66, 1.0, v72
	v_rcp_f32_e32 v66, v66
	v_mul_f32_e32 v69, v92, v71
	v_add_f32_e32 v67, 1.0, v67
	v_rcp_f32_e32 v67, v67
	v_exp_f32_e32 v69, v69
	v_mul_f32_e32 v68, v70, v70
	v_mul_f32_e32 v66, v68, v66
	v_mul_f32_e32 v66, v74, v66
	v_mul_f32_e32 v70, v90, v66
	v_mul_f32_e32 v66, v68, v67
	v_add_f32_e32 v67, 1.0, v69
	v_mul_f32_e32 v69, v93, v71
	v_rcp_f32_e32 v67, v67
	v_exp_f32_e32 v69, v69
	v_mul_f32_e32 v66, v75, v66
	v_mul_f32_e32 v72, v91, v66
	v_mul_f32_e32 v66, v68, v67
	v_add_f32_e32 v67, 1.0, v69
	v_mul_f32_e32 v69, v94, v71
	v_rcp_f32_e32 v67, v67
	v_exp_f32_e32 v69, v69
	v_mul_f32_e32 v66, v76, v66
	v_mul_f32_e32 v73, v92, v66
	v_mul_f32_e32 v66, v68, v67
	v_add_f32_e32 v67, 1.0, v69
	v_mul_f32_e32 v69, v95, v71
	v_rcp_f32_e32 v67, v67
	v_exp_f32_e32 v69, v69
	v_mul_f32_e32 v66, v77, v66
	v_mul_f32_e32 v74, v93, v66
	v_mul_f32_e32 v66, v68, v67
	v_add_f32_e32 v67, 1.0, v69
	v_rcp_f32_e32 v67, v67
	v_mul_f32_e32 v66, v78, v66
	v_mul_f32_e32 v69, v94, v66
	v_mul_f32_e32 v66, v96, v71
	v_mul_f32_e32 v67, v68, v67
	v_mul_f32_e32 v67, v79, v67
	v_mul_f32_e32 v75, v95, v67
	v_mul_f32_e32 v67, v97, v71
	s_waitcnt vmcnt(6)
	v_add_f32_e32 v71, v142, v143
	v_add_f32_e32 v76, v144, v145
	v_add_f32_e32 v71, v71, v76
	v_exp_f32_e32 v66, v66
	v_mov_b32_e32 v76, v71
	s_nop 1
	v_permlane16_swap_b32_e32 v71, v76
	v_exp_f32_e32 v67, v67
	v_add_f32_e32 v66, 1.0, v66
	v_rcp_f32_e32 v66, v66
	s_waitcnt lgkmcnt(0)
	v_add_f32_e32 v71, v71, v76
	v_add_f32_e32 v67, 1.0, v67
	v_mov_b32_e32 v76, v71
	s_nop 1
	v_permlane32_swap_b32_e32 v71, v76
	v_rcp_f32_e32 v67, v67
	v_mul_f32_e32 v66, v68, v66
	v_mul_f32_e32 v66, v80, v66
	v_mul_f32_e32 v77, v96, v66
	v_mul_f32_e32 v66, v68, v67
	s_waitcnt lgkmcnt(0)
	v_add_f32_e32 v67, v71, v76
	v_fmamk_f32 v67, v67, 0x3a800000, v204
	v_mul_f32_e32 v71, 0x4f800000, v67
	v_cmp_gt_f32_e32 vcc, s13, v67
	v_mul_f32_e32 v68, v81, v66
	v_mov_b32_e32 v66, v203
	v_cndmask_b32_e32 v71, v67, v71, vcc
	v_sqrt_f32_e32 v76, v71
	v_mov_b32_e32 v67, v203
	v_cvt_pk_fp8_f32 v67, v69, v75
	v_cvt_pk_fp8_f32 v66, v70, v72
	v_add_u32_e32 v69, -1, v76
	v_fma_f32 v70, -v69, v76, v71
	v_cmp_ge_f32_e64 s[4:5], 0, v70
	v_add_u32_e32 v70, 1, v76
	v_fma_f32 v72, -v70, v76, v71
	v_cndmask_b32_e64 v69, v76, v69, s[4:5]
	v_cmp_lt_f32_e64 s[4:5], 0, v72
	v_mul_f32_e32 v68, v97, v68
	v_cvt_pk_fp8_f32 v67, v77, v68 op_sel:[0,0,1]
	v_cndmask_b32_e64 v69, v69, v70, s[4:5]
	v_mul_f32_e32 v70, 0x37800000, v69
	v_cndmask_b32_e32 v69, v69, v70, vcc
	v_cmp_class_f32_e32 vcc, v71, v205
	v_cvt_pk_fp8_f32 v66, v73, v74 op_sel:[0,0,1]
	s_nop 0
	v_cndmask_b32_e32 v69, v69, v71, vcc
	v_div_scale_f32 v70, s[0:1], v69, v69, 1.0
	v_rcp_f32_e32 v71, v70
	s_mov_b32 s0, 0x21000
	v_fma_f32 v68, -v70, v71, 1.0
	v_fmac_f32_e32 v71, v68, v71
	v_div_scale_f32 v68, vcc, 1.0, v69, 1.0
	v_mul_f32_e32 v72, v68, v71
	v_fma_f32 v73, -v70, v72, v68
	v_fmac_f32_e32 v72, v73, v71
	v_fma_f32 v68, -v70, v72, v68
	v_div_fmas_f32 v68, v68, v71, v72
	v_div_fixup_f32 v68, v68, v69, 1.0
	v_mul_f32_e32 v70, 0x3d000000, v68
	v_mul_f32_e32 v71, 0xbfb8aa3b, v70
	v_mul_f32_e32 v68, v50, v71
	v_exp_f32_e32 v72, v68
	v_add_co_u32_e32 v68, vcc, s0, v98
	s_nop 1
	v_addc_co_u32_e32 v69, vcc, 0, v99, vcc
	global_store_dwordx2 v[68:69], v[66:67], off
	v_add_f32_e32 v66, 1.0, v72
	v_rcp_f32_e32 v66, v66
	v_mul_f32_e32 v67, v51, v71
	v_exp_f32_e32 v67, v67
	v_mul_f32_e32 v68, v70, v70
	v_mul_f32_e32 v66, v68, v66
	v_mul_f32_e32 v34, v34, v66
	v_add_f32_e32 v66, 1.0, v67
	v_rcp_f32_e32 v66, v66
	v_mul_f32_e32 v67, v52, v71
	v_exp_f32_e32 v67, v67
	v_mul_f32_e32 v50, v50, v34
	v_mul_f32_e32 v34, v68, v66
	v_mul_f32_e32 v34, v35, v34
	v_add_f32_e32 v35, 1.0, v67
	v_rcp_f32_e32 v35, v35
	v_mul_f32_e32 v66, v53, v71
	v_exp_f32_e32 v66, v66
	v_mul_f32_e32 v51, v51, v34
	v_mul_f32_e32 v34, v68, v35
	v_mul_f32_e32 v34, v36, v34
	v_add_f32_e32 v35, 1.0, v66
	v_mul_f32_e32 v36, v54, v71
	v_rcp_f32_e32 v35, v35
	v_exp_f32_e32 v36, v36
	v_mul_f32_e32 v52, v52, v34
	v_mul_f32_e32 v34, v68, v35
	v_add_f32_e32 v35, 1.0, v36
	v_mul_f32_e32 v36, v55, v71
	v_rcp_f32_e32 v35, v35
	v_exp_f32_e32 v36, v36
	v_mul_f32_e32 v34, v37, v34
	v_mul_f32_e32 v37, v53, v34
	v_mul_f32_e32 v34, v68, v35
	v_add_f32_e32 v35, 1.0, v36
	v_rcp_f32_e32 v35, v35
	v_mul_f32_e32 v34, v38, v34
	v_mul_f32_e32 v36, v54, v34
	v_mul_f32_e32 v34, v56, v71
	v_exp_f32_e32 v34, v34
	v_mul_f32_e32 v35, v68, v35
	v_mul_f32_e32 v35, v39, v35
	s_waitcnt vmcnt(6)
	v_add_f32_e32 v39, v138, v139
	v_add_f32_e32 v53, v140, v141
	v_add_f32_e32 v39, v39, v53
	v_add_f32_e32 v34, 1.0, v34
	v_mov_b32_e32 v53, v39
	s_nop 1
	v_permlane16_swap_b32_e32 v39, v53
	v_mul_f32_e32 v38, v55, v35
	v_rcp_f32_e32 v34, v34
	v_mul_f32_e32 v35, v57, v71
	v_exp_f32_e32 v35, v35
	s_waitcnt lgkmcnt(0)
	v_add_f32_e32 v39, v39, v53
	v_mul_f32_e32 v34, v68, v34
	v_mul_f32_e32 v34, v40, v34
	v_add_f32_e32 v35, 1.0, v35
	v_mov_b32_e32 v40, v39
	s_nop 1
	v_permlane32_swap_b32_e32 v39, v40
	v_rcp_f32_e32 v35, v35
	v_mul_f32_e32 v53, v56, v34
	v_mul_f32_e32 v34, v68, v35
	s_waitcnt lgkmcnt(0)
	v_add_f32_e32 v35, v39, v40
	v_fmamk_f32 v35, v35, 0x3a800000, v204
	v_mul_f32_e32 v39, 0x4f800000, v35
	v_cmp_gt_f32_e32 vcc, s13, v35
	v_mul_f32_e32 v41, v41, v34
	v_mov_b32_e32 v34, v203
	v_cndmask_b32_e32 v39, v35, v39, vcc
	v_sqrt_f32_e32 v40, v39
	v_mov_b32_e32 v35, v203
	v_cvt_pk_fp8_f32 v35, v36, v38
	v_cvt_pk_fp8_f32 v34, v50, v51
	v_add_u32_e32 v36, -1, v40
	v_fma_f32 v38, -v36, v40, v39
	v_cmp_ge_f32_e64 s[4:5], 0, v38
	v_add_u32_e32 v38, 1, v40
	v_cvt_pk_fp8_f32 v34, v52, v37 op_sel:[0,0,1]
	v_cndmask_b32_e64 v36, v40, v36, s[4:5]
	v_fma_f32 v40, -v38, v40, v39
	v_cmp_lt_f32_e64 s[4:5], 0, v40
	v_mul_f32_e32 v40, v57, v41
	v_cvt_pk_fp8_f32 v35, v53, v40 op_sel:[0,0,1]
	v_cndmask_b32_e64 v36, v36, v38, s[4:5]
	v_mul_f32_e32 v38, 0x37800000, v36
	v_cndmask_b32_e32 v36, v36, v38, vcc
	v_cmp_class_f32_e32 vcc, v39, v205
	s_nop 1
	v_cndmask_b32_e32 v36, v36, v39, vcc
	v_div_scale_f32 v38, s[0:1], v36, v36, 1.0
	v_rcp_f32_e32 v39, v38
	s_mov_b32 s0, 0x58000
	v_fma_f32 v37, -v38, v39, 1.0
	v_fmac_f32_e32 v39, v37, v39
	v_div_scale_f32 v37, vcc, 1.0, v36, 1.0
	v_mul_f32_e32 v40, v37, v39
	v_fma_f32 v41, -v38, v40, v37
	v_fmac_f32_e32 v40, v41, v39
	v_fma_f32 v37, -v38, v40, v37
	v_div_fmas_f32 v37, v37, v39, v40
	v_div_fixup_f32 v36, v37, v36, 1.0
	v_mul_f32_e32 v38, 0x3d000000, v36
	v_mul_f32_e32 v39, 0xbfb8aa3b, v38
	v_mul_f32_e32 v36, v58, v39
	v_exp_f32_e32 v40, v36
	v_add_co_u32_e32 v36, vcc, s0, v98
	s_nop 1
	v_addc_co_u32_e32 v37, vcc, 0, v99, vcc
	global_store_dwordx2 v[36:37], v[34:35], off
	v_mul_f32_e32 v35, v59, v39
	v_exp_f32_e32 v35, v35
	v_add_f32_e32 v34, 1.0, v40
	v_rcp_f32_e32 v34, v34
	v_mul_f32_e32 v37, v60, v39
	v_add_f32_e32 v35, 1.0, v35
	v_rcp_f32_e32 v35, v35
	v_exp_f32_e32 v37, v37
	v_mul_f32_e32 v36, v38, v38
	v_mul_f32_e32 v34, v36, v34
	v_mul_f32_e32 v34, v42, v34
	v_mul_f32_e32 v38, v58, v34
	v_mul_f32_e32 v34, v36, v35
	v_add_f32_e32 v35, 1.0, v37
	v_mul_f32_e32 v37, v61, v39
	v_rcp_f32_e32 v35, v35
	v_exp_f32_e32 v37, v37
	v_mul_f32_e32 v34, v43, v34
	v_mul_f32_e32 v40, v59, v34
	v_mul_f32_e32 v34, v36, v35
	v_add_f32_e32 v35, 1.0, v37
	v_mul_f32_e32 v37, v62, v39
	v_rcp_f32_e32 v35, v35
	v_exp_f32_e32 v37, v37
	v_mul_f32_e32 v34, v44, v34
	v_mul_f32_e32 v41, v60, v34
	v_mul_f32_e32 v34, v36, v35
	v_add_f32_e32 v35, 1.0, v37
	v_mul_f32_e32 v37, v63, v39
	v_rcp_f32_e32 v35, v35
	v_exp_f32_e32 v37, v37
	v_mul_f32_e32 v34, v45, v34
	v_mul_f32_e32 v42, v61, v34
	v_mul_f32_e32 v34, v36, v35
	v_add_f32_e32 v35, 1.0, v37
	v_rcp_f32_e32 v35, v35
	v_mul_f32_e32 v34, v46, v34
	v_mul_f32_e32 v37, v62, v34
	v_mul_f32_e32 v34, v64, v39
	v_mul_f32_e32 v35, v36, v35
	v_mul_f32_e32 v35, v47, v35
	v_mul_f32_e32 v43, v63, v35
	v_mul_f32_e32 v35, v65, v39
	s_waitcnt vmcnt(6)
	v_add_f32_e32 v39, v134, v135
	v_add_f32_e32 v44, v136, v137
	v_add_f32_e32 v39, v39, v44
	v_exp_f32_e32 v34, v34
	v_mov_b32_e32 v44, v39
	s_nop 1
	v_permlane16_swap_b32_e32 v39, v44
	v_exp_f32_e32 v35, v35
	v_add_f32_e32 v34, 1.0, v34
	v_rcp_f32_e32 v34, v34
	s_waitcnt lgkmcnt(0)
	v_add_f32_e32 v39, v39, v44
	v_add_f32_e32 v35, 1.0, v35
	v_mov_b32_e32 v44, v39
	s_nop 1
	v_permlane32_swap_b32_e32 v39, v44
	v_rcp_f32_e32 v35, v35
	v_mul_f32_e32 v34, v36, v34
	v_mul_f32_e32 v34, v48, v34
	v_mul_f32_e32 v45, v64, v34
	v_mul_f32_e32 v34, v36, v35
	s_waitcnt lgkmcnt(0)
	v_add_f32_e32 v35, v39, v44
	v_fmamk_f32 v35, v35, 0x3a800000, v204
	v_mul_f32_e32 v39, 0x4f800000, v35
	v_cmp_gt_f32_e32 vcc, s13, v35
	v_mul_f32_e32 v36, v49, v34
	v_mov_b32_e32 v34, v203
	v_cndmask_b32_e32 v39, v35, v39, vcc
	v_sqrt_f32_e32 v44, v39
	v_mov_b32_e32 v35, v203
	v_cvt_pk_fp8_f32 v35, v37, v43
	v_cvt_pk_fp8_f32 v34, v38, v40
	v_add_u32_e32 v37, -1, v44
	v_fma_f32 v38, -v37, v44, v39
	v_cmp_ge_f32_e64 s[4:5], 0, v38
	v_add_u32_e32 v38, 1, v44
	v_fma_f32 v40, -v38, v44, v39
	v_cndmask_b32_e64 v37, v44, v37, s[4:5]
	v_cmp_lt_f32_e64 s[4:5], 0, v40
	v_mul_f32_e32 v36, v65, v36
	v_cvt_pk_fp8_f32 v35, v45, v36 op_sel:[0,0,1]
	v_cndmask_b32_e64 v37, v37, v38, s[4:5]
	v_mul_f32_e32 v38, 0x37800000, v37
	v_cndmask_b32_e32 v37, v37, v38, vcc
	v_cmp_class_f32_e32 vcc, v39, v205
	v_cvt_pk_fp8_f32 v34, v41, v42 op_sel:[0,0,1]
	s_nop 0
	v_cndmask_b32_e32 v37, v37, v39, vcc
	v_div_scale_f32 v38, s[0:1], v37, v37, 1.0
	v_rcp_f32_e32 v39, v38
	s_mov_b32 s0, 0x63000
	v_fma_f32 v36, -v38, v39, 1.0
	v_fmac_f32_e32 v39, v36, v39
	v_div_scale_f32 v36, vcc, 1.0, v37, 1.0
	v_mul_f32_e32 v40, v36, v39
	v_fma_f32 v41, -v38, v40, v36
	v_fmac_f32_e32 v40, v41, v39
	v_fma_f32 v36, -v38, v40, v36
	v_div_fmas_f32 v36, v36, v39, v40
	v_div_fixup_f32 v36, v36, v37, 1.0
	v_mul_f32_e32 v38, 0x3d000000, v36
	v_mul_f32_e32 v39, 0xbfb8aa3b, v38
	v_mul_f32_e32 v36, v18, v39
	v_exp_f32_e32 v40, v36
	v_mul_f32_e32 v41, v19, v39
	v_exp_f32_e32 v41, v41
	v_add_co_u32_e32 v36, vcc, s0, v98
	v_add_f32_e32 v40, 1.0, v40
	s_nop 0
	v_addc_co_u32_e32 v37, vcc, 0, v99, vcc
	v_rcp_f32_e32 v40, v40
	global_store_dwordx2 v[36:37], v[34:35], off
	v_add_f32_e32 v36, 1.0, v41
	v_mul_f32_e32 v37, v20, v39
	v_rcp_f32_e32 v36, v36
	v_exp_f32_e32 v37, v37
	v_mul_f32_e32 v34, v38, v38
	v_mul_f32_e32 v35, v34, v40
	v_mul_f32_e32 v2, v2, v35
	v_mul_f32_e32 v18, v18, v2
	v_mul_f32_e32 v2, v34, v36
	v_add_f32_e32 v35, 1.0, v37
	v_mul_f32_e32 v36, v21, v39
	v_rcp_f32_e32 v35, v35
	v_exp_f32_e32 v36, v36
	v_mul_f32_e32 v2, v3, v2
	v_mul_f32_e32 v3, v19, v2
	v_mul_f32_e32 v2, v34, v35
	v_add_f32_e32 v19, 1.0, v36
	v_mul_f32_e32 v35, v22, v39
	v_rcp_f32_e32 v19, v19
	v_exp_f32_e32 v35, v35
	v_mul_f32_e32 v2, v4, v2
	v_mul_f32_e32 v4, v20, v2
	v_mul_f32_e32 v2, v34, v19
	v_add_f32_e32 v19, 1.0, v35
	v_mul_f32_e32 v20, v23, v39
	v_rcp_f32_e32 v19, v19
	v_exp_f32_e32 v20, v20
	v_mul_f32_e32 v2, v5, v2
	v_mul_f32_e32 v5, v21, v2
	v_mul_f32_e32 v2, v34, v19
	v_add_f32_e32 v19, 1.0, v20
	v_mul_f32_e32 v20, v24, v39
	v_rcp_f32_e32 v19, v19
	v_exp_f32_e32 v20, v20
	v_mul_f32_e32 v2, v6, v2
	v_mul_f32_e32 v6, v22, v2
	v_mul_f32_e32 v2, v34, v19
	v_add_f32_e32 v19, 1.0, v20
	v_mul_f32_e32 v20, v25, v39
	v_rcp_f32_e32 v19, v19
	v_exp_f32_e32 v20, v20
	v_mul_f32_e32 v2, v7, v2
	v_mul_f32_e32 v7, v23, v2
	v_mul_f32_e32 v2, v34, v19
	v_add_f32_e32 v19, 1.0, v20
	s_waitcnt vmcnt(6)
	v_add_f32_e32 v20, v130, v131
	v_add_f32_e32 v21, v132, v133
	v_add_f32_e32 v20, v20, v21
	v_mov_b32_e32 v21, v20
	s_nop 1
	v_permlane16_swap_b32_e32 v20, v21
	v_rcp_f32_e32 v19, v19
	v_mul_f32_e32 v2, v8, v2
	v_mul_f32_e32 v8, v24, v2
	v_mul_f32_e32 v2, v34, v19
	s_waitcnt lgkmcnt(0)
	v_add_f32_e32 v19, v20, v21
	v_mov_b32_e32 v20, v19
	s_nop 1
	v_permlane32_swap_b32_e32 v19, v20
	v_mul_f32_e32 v9, v9, v2
	v_mov_b32_e32 v2, v203
	v_cvt_pk_fp8_f32 v2, v18, v3
	v_mov_b32_e32 v3, v203
	v_cvt_pk_fp8_f32 v3, v6, v7
	s_waitcnt lgkmcnt(0)
	v_add_f32_e32 v6, v19, v20
	v_fmamk_f32 v6, v6, 0x3a800000, v204
	v_mul_f32_e32 v7, 0x4f800000, v6
	v_cmp_gt_f32_e32 vcc, s13, v6
	v_cvt_pk_fp8_f32 v2, v4, v5 op_sel:[0,0,1]
	v_mul_f32_e32 v9, v25, v9
	v_cndmask_b32_e32 v6, v6, v7, vcc
	v_sqrt_f32_e32 v7, v6
	v_cvt_pk_fp8_f32 v3, v8, v9 op_sel:[0,0,1]
	v_add_u32_e32 v4, -1, v7
	v_fma_f32 v5, -v4, v7, v6
	v_cmp_ge_f32_e64 s[4:5], 0, v5
	v_add_u32_e32 v5, 1, v7
	s_nop 0
	v_cndmask_b32_e64 v4, v7, v4, s[4:5]
	v_fma_f32 v7, -v5, v7, v6
	v_cmp_lt_f32_e64 s[4:5], 0, v7
	s_nop 1
	v_cndmask_b32_e64 v4, v4, v5, s[4:5]
	v_mul_f32_e32 v5, 0x37800000, v4
	v_cndmask_b32_e32 v4, v4, v5, vcc
	v_cmp_class_f32_e32 vcc, v6, v205
	s_nop 1
	v_cndmask_b32_e32 v6, v4, v6, vcc
	v_div_scale_f32 v7, s[0:1], v6, v6, 1.0
	v_rcp_f32_e32 v8, v7
	s_mov_b32 s0, 0x6e000
	v_add_co_u32_e32 v4, vcc, s0, v98
	v_fma_f32 v9, -v7, v8, 1.0
	s_nop 0
	v_addc_co_u32_e32 v5, vcc, 0, v99, vcc
	v_fmac_f32_e32 v8, v9, v8
	v_div_scale_f32 v9, vcc, 1.0, v6, 1.0
	v_mul_f32_e32 v18, v9, v8
	v_fma_f32 v19, -v7, v18, v9
	v_fmac_f32_e32 v18, v19, v8
	v_fma_f32 v7, -v7, v18, v9
	v_div_fmas_f32 v7, v7, v8, v18
	v_div_fixup_f32 v6, v7, v6, 1.0
	v_mul_f32_e32 v6, 0x3d000000, v6
	v_mul_f32_e32 v7, 0xbfb8aa3b, v6
	global_store_dwordx2 v[4:5], v[2:3], off
	v_mul_f32_e32 v2, v27, v7
	v_exp_f32_e32 v2, v2
	v_mul_f32_e32 v8, v26, v7
	v_mul_f32_e32 v4, v6, v6
	v_mul_f32_e32 v6, v29, v7
	v_add_f32_e32 v2, 1.0, v2
	v_rcp_f32_e32 v2, v2
	v_exp_f32_e32 v8, v8
	v_exp_f32_e32 v6, v6
	v_mul_f32_e32 v9, v31, v7
	v_mul_f32_e32 v2, v4, v2
	v_mul_f32_e32 v2, v11, v2
	v_add_f32_e32 v3, 1.0, v8
	v_mul_f32_e32 v8, v27, v2
	v_add_f32_e32 v2, 1.0, v6
	v_rcp_f32_e32 v2, v2
	v_rcp_f32_e32 v3, v3
	v_exp_f32_e32 v9, v9
	v_mul_f32_e32 v6, v30, v7
	v_mul_f32_e32 v2, v4, v2
	v_mul_f32_e32 v3, v4, v3
	v_mul_f32_e32 v2, v13, v2
	v_mul_f32_e32 v3, v10, v3
	v_mul_f32_e32 v10, v29, v2
	v_add_f32_e32 v2, 1.0, v9
	v_rcp_f32_e32 v2, v2
	v_mul_f32_e32 v5, v28, v7
	v_exp_f32_e32 v6, v6
	v_mul_f32_e32 v9, v32, v7
	v_mul_f32_e32 v7, v33, v7
	v_exp_f32_e32 v5, v5
	v_exp_f32_e32 v9, v9
	v_exp_f32_e32 v7, v7
	v_mul_f32_e32 v2, v4, v2
	v_add_f32_e32 v6, 1.0, v6
	v_mul_f32_e32 v2, v15, v2
	v_add_f32_e32 v5, 1.0, v5
	v_rcp_f32_e32 v6, v6
	v_add_f32_e32 v9, 1.0, v9
	v_mul_f32_e32 v11, v31, v2
	v_add_f32_e32 v2, 1.0, v7
	v_rcp_f32_e32 v5, v5
	v_rcp_f32_e32 v9, v9
	v_rcp_f32_e32 v2, v2
	v_mul_f32_e32 v6, v4, v6
	v_mul_f32_e32 v3, v26, v3
	v_mul_f32_e32 v5, v4, v5
	v_mul_f32_e32 v6, v14, v6
	v_mul_f32_e32 v7, v4, v9
	v_mul_f32_e32 v4, v4, v2
	v_mov_b32_e32 v2, v203
	v_mul_f32_e32 v6, v30, v6
	v_cvt_pk_fp8_f32 v2, v3, v8
	v_mov_b32_e32 v3, v203
	v_cvt_pk_fp8_f32 v3, v6, v11
	v_mul_f32_e32 v5, v12, v5
	v_mul_f32_e32 v7, v16, v7
	v_mul_f32_e32 v4, v17, v4
	v_mul_f32_e32 v5, v28, v5
	v_mul_f32_e32 v7, v32, v7
	v_mul_f32_e32 v4, v33, v4
	v_cvt_pk_fp8_f32 v2, v5, v10 op_sel:[0,0,1]
	v_cvt_pk_fp8_f32 v3, v7, v4 op_sel:[0,0,1]
	s_mov_b32 s0, 0x79000
	v_add_co_u32_e32 v4, vcc, s0, v98
	s_nop 1
	v_addc_co_u32_e32 v5, vcc, 0, v99, vcc
	global_store_dwordx2 v[4:5], v[2:3], off
	v_mov_b32 v2, 0
	v_mov_b32 v3, 0
	v_mov_b32 v4, 0
	v_mov_b32 v5, 0
	s_and_b64 vcc, exec, s[2:3]
	s_mov_b64 s[2:3], -1
	v_mfma_f32_32x32x16_bf16 v[114:129], v[2:5], v[2:5], 0
	s_nop 0
	v_mfma_f32_32x32x16_bf16 v[82:97], v[2:5], v[2:5], 0
	s_nop 0
	v_mfma_f32_32x32x16_bf16 v[98:113], v[2:5], v[2:5], 0
	s_nop 0
	v_mfma_f32_32x32x16_bf16 v[66:81], v[2:5], v[2:5], 0
	s_nop 0
	v_mfma_f32_32x32x16_bf16 v[50:65], v[2:5], v[2:5], 0
	s_nop 0
	v_mfma_f32_32x32x16_bf16 v[18:33], v[2:5], v[2:5], 0
	s_nop 0
	v_mfma_f32_32x32x16_bf16 v[34:49], v[2:5], v[2:5], 0
	s_nop 0
	v_mfma_f32_32x32x16_bf16 v[2:17], v[2:5], v[2:5], 0
	s_cbranch_vccnz .LBB0_1953
	s_andn2_b64 vcc, exec, s[8:9]
	s_cbranch_vccnz .LBB0_1952
	s_barrier
	s_branch .LBB0_1952

.LBB0_2038:
	s_ashr_i32 s5, s4, 31
	s_lshl_b64 s[0:1], s[4:5], 8
	s_add_u32 s0, s0, s47
	s_addc_u32 s1, s1, s56
	s_lshl_b32 s4, s62, 8
	s_ashr_i32 s5, s4, 31
	s_lshl_b64 s[22:23], s[0:1], 11
	v_readlane_b32 s26, v252, 58
	v_readlane_b32 s27, v252, 59
	s_add_u32 s22, s26, s22
	s_addc_u32 s23, s27, s23
	s_lshl_b64 s[4:5], s[4:5], 1
	s_add_u32 s4, s22, s4
	v_mov_b32_e32 v200, v207
	v_mov_b32_e32 v201, v208
	s_addc_u32 s5, s23, s5
	s_add_u32 s22, s4, s58
	v_lshlrev_b32_e32 v106, 11, v200
	s_addc_u32 s23, s5, 0
	v_lshl_add_u32 v202, v201, 4, v106
	global_load_dwordx4 v[190:193], v202, s[22:23]
	global_load_dwordx4 v[186:189], v202, s[22:23] offset:256
	s_lshl_b64 s[0:1], s[0:1], 6
	v_readlane_b32 s4, v250, 7
	v_readlane_b32 s5, v250, 8
	s_add_u32 s4, s4, s0
	s_addc_u32 s5, s5, s1
	s_lshl_b32 s0, s62, 2
	s_ashr_i32 s1, s0, 31
	s_lshl_b64 s[0:1], s[0:1], 2
	s_add_u32 s0, s4, s0
	s_addc_u32 s1, s5, s1
	s_add_u32 s26, s0, s59
	v_lshl_add_u64 v[198:199], s[22:23], 0, v[202:203]
	s_mov_b32 s0, 0x8000
	v_add_co_u32_e32 v106, vcc, s0, v198
	s_mov_b32 s0, 0x10000
	s_nop 0
	v_addc_co_u32_e32 v107, vcc, 0, v199, vcc
	global_load_dwordx4 v[182:185], v[106:107], off
	global_load_dwordx4 v[178:181], v[106:107], off offset:256
	v_add_co_u32_e32 v106, vcc, s0, v198
	s_mov_b32 s0, 0x18000
	s_nop 0
	v_addc_co_u32_e32 v107, vcc, 0, v199, vcc
	global_load_dwordx4 v[174:177], v[106:107], off
	global_load_dwordx4 v[170:173], v[106:107], off offset:256
	v_add_co_u32_e32 v106, vcc, s0, v198
	s_mov_b32 s0, 0x40000
	s_nop 0
	v_addc_co_u32_e32 v107, vcc, 0, v199, vcc
	global_load_dwordx4 v[166:169], v[106:107], off
	global_load_dwordx4 v[162:165], v[106:107], off offset:256
	v_add_co_u32_e32 v106, vcc, s0, v198
	s_mov_b32 s0, 0x48000
	s_nop 0
	v_addc_co_u32_e32 v107, vcc, 0, v199, vcc
	global_load_dwordx4 v[158:161], v[106:107], off
	global_load_dwordx4 v[154:157], v[106:107], off offset:256
	v_add_co_u32_e32 v106, vcc, s0, v198
	s_mov_b32 s0, 0x50000
	s_nop 0
	v_addc_co_u32_e32 v107, vcc, 0, v199, vcc
	global_load_dwordx4 v[150:153], v[106:107], off
	global_load_dwordx4 v[146:149], v[106:107], off offset:256
	v_add_co_u32_e32 v106, vcc, s0, v198
	s_mov_b32 s0, 0x58000
	s_nop 0
	v_addc_co_u32_e32 v107, vcc, 0, v199, vcc
	global_load_dwordx4 v[126:129], v[106:107], off
	global_load_dwordx4 v[122:125], v[106:107], off offset:256
	v_add_co_u32_e32 v106, vcc, s0, v198
	v_pk_add_f32 v[144:145], v[144:145], 0 op_sel_hi:[1,0]
	s_nop 0
	v_addc_co_u32_e32 v107, vcc, 0, v199, vcc
	global_load_dwordx4 v[110:113], v[106:107], off
	s_nop 0
	global_load_dwordx4 v[106:109], v[106:107], off offset:256
	v_pk_add_f32 v[142:143], v[142:143], 0 op_sel_hi:[1,0]
	v_pk_add_f32 v[136:137], v[136:137], 0 op_sel_hi:[1,0]
	v_pk_add_f32 v[132:133], v[132:133], 0 op_sel_hi:[1,0]
	v_pk_add_f32 v[130:131], v[130:131], 0 op_sel_hi:[1,0]
	v_pk_add_f32 v[140:141], v[140:141], 0 op_sel_hi:[1,0]
	v_pk_add_f32 v[138:139], v[138:139], 0 op_sel_hi:[1,0]
	v_pk_add_f32 v[134:135], v[134:135], 0 op_sel_hi:[1,0]
	s_addc_u32 s27, s1, 0
	v_lshlrev_b32_e32 v200, 6, v200
	v_cmp_eq_u32_e64 s[4:5], 0, v201
	v_mov_b32_e32 v201, v203
	v_lshl_add_u64 v[200:201], s[26:27], 0, v[200:201]
	s_waitcnt vmcnt(15)
	v_lshlrev_b32_e32 v210, 16, v190
	v_and_b32_e32 v211, 0xffff0000, v190
	v_lshlrev_b32_e32 v190, 16, v191
	v_and_b32_e32 v191, 0xffff0000, v191
	s_waitcnt vmcnt(14)
	v_lshlrev_b32_e32 v218, 16, v186
	v_and_b32_e32 v219, 0xffff0000, v186
	v_lshlrev_b32_e32 v186, 16, v187
	v_and_b32_e32 v187, 0xffff0000, v187
	v_lshlrev_b32_e32 v220, 16, v188
	v_and_b32_e32 v221, 0xffff0000, v188
	v_lshlrev_b32_e32 v188, 16, v189
	v_and_b32_e32 v189, 0xffff0000, v189
	v_lshlrev_b32_e32 v212, 16, v192
	v_and_b32_e32 v213, 0xffff0000, v192
	v_lshlrev_b32_e32 v192, 16, v193
	v_and_b32_e32 v193, 0xffff0000, v193
	v_pk_add_f32 v[144:145], v[144:145], v[190:191]
	v_pk_add_f32 v[142:143], v[142:143], v[210:211]
	v_pk_add_f32 v[136:137], v[136:137], v[186:187]
	v_pk_add_f32 v[186:187], v[132:133], v[188:189]
	v_pk_add_f32 v[188:189], v[130:131], v[220:221]
	v_cvt_pk_bf16_f32 v130, v142, v143
	v_cvt_pk_bf16_f32 v131, v144, v145
	v_pk_add_f32 v[140:141], v[140:141], v[192:193]
	v_pk_add_f32 v[138:139], v[138:139], v[212:213]
	v_pk_add_f32 v[134:135], v[134:135], v[218:219]
	v_cvt_pk_bf16_f32 v132, v138, v139
	v_cvt_pk_bf16_f32 v133, v140, v141
	global_store_dwordx4 v202, v[130:133], s[22:23]
	s_nop 1
	v_cvt_pk_bf16_f32 v130, v134, v135
	v_cvt_pk_bf16_f32 v131, v136, v137
	v_cvt_pk_bf16_f32 v132, v188, v189
	v_cvt_pk_bf16_f32 v133, v186, v187
	global_store_dwordx4 v202, v[130:133], s[22:23] offset:256
	s_nop 1
	v_mul_f32_e32 v130, v143, v143
	v_mul_f32_e32 v131, v145, v145
	v_fmac_f32_e32 v130, v142, v142
	v_fmac_f32_e32 v131, v144, v144
	v_add_f32_e32 v130, v130, v131
	v_mul_f32_e32 v131, v139, v139
	v_mul_f32_e32 v132, v141, v141
	v_fmac_f32_e32 v131, v138, v138
	v_fmac_f32_e32 v132, v140, v140
	v_add_f32_e32 v131, v131, v132
	v_add_f32_e32 v130, v130, v131
	v_mul_f32_e32 v131, v135, v135
	v_mul_f32_e32 v132, v137, v137
	v_fmac_f32_e32 v131, v134, v134
	v_fmac_f32_e32 v132, v136, v136
	v_add_f32_e32 v131, v131, v132
	v_mul_f32_e32 v132, v189, v189
	v_mul_f32_e32 v133, v187, v187
	v_fmac_f32_e32 v132, v188, v188
	v_fmac_f32_e32 v133, v186, v186
	v_add_f32_e32 v132, v132, v133
	v_add_f32_e32 v131, v131, v132
	v_and_b32_e32 v132, 64, v248
	v_add_f32_e32 v131, v130, v131
	v_xor_b32_e32 v130, 16, v248
	v_add_u32_e32 v133, 64, v132
	v_cmp_lt_i32_e32 vcc, v130, v133
	s_nop 1
	v_cndmask_b32_e32 v130, v248, v130, vcc
	v_lshlrev_b32_e32 v130, 2, v130
	v_mov_b32_e32 v132, v131
	s_nop 1
	v_permlane16_swap_b32_e32 v131, v132
	s_waitcnt lgkmcnt(0)
	v_add_f32_e32 v132, v131, v132
	v_xor_b32_e32 v131, 32, v248
	v_cmp_lt_i32_e32 vcc, v131, v133
	s_nop 1
	v_cndmask_b32_e32 v131, v248, v131, vcc
	v_lshlrev_b32_e32 v131, 2, v131
	v_mov_b32_e32 v133, v132
	s_nop 1
	v_permlane32_swap_b32_e32 v132, v133
	s_and_saveexec_b64 s[22:23], s[4:5]
	s_cbranch_execz .LBB0_2040
	s_waitcnt lgkmcnt(0)
	v_add_f32_e32 v132, v132, v133
	global_store_dword v[200:201], v132, off
.LBB0_2040:
	s_or_b64 exec, exec, s[22:23]
	s_waitcnt vmcnt(15)
	v_lshlrev_b32_e32 v136, 16, v182
	v_and_b32_e32 v137, 0xffff0000, v182
	v_lshlrev_b32_e32 v138, 16, v183
	v_and_b32_e32 v139, 0xffff0000, v183
	v_pk_add_f32 v[120:121], v[120:121], 0 op_sel_hi:[1,0]
	v_pk_add_f32 v[118:119], v[118:119], 0 op_sel_hi:[1,0]
	s_waitcnt vmcnt(14)
	v_lshlrev_b32_e32 v182, 16, v180
	v_and_b32_e32 v183, 0xffff0000, v180
	v_lshlrev_b32_e32 v180, 16, v181
	v_and_b32_e32 v181, 0xffff0000, v181
	v_pk_add_f32 v[120:121], v[120:121], v[138:139]
	v_pk_add_f32 v[118:119], v[118:119], v[136:137]
	v_pk_add_f32 v[100:101], v[100:101], 0 op_sel_hi:[1,0]
	v_lshlrev_b32_e32 v140, 16, v184
	v_and_b32_e32 v141, 0xffff0000, v184
	v_lshlrev_b32_e32 v142, 16, v185
	v_and_b32_e32 v143, 0xffff0000, v185
	v_pk_add_f32 v[116:117], v[116:117], 0 op_sel_hi:[1,0]
	v_pk_add_f32 v[114:115], v[114:115], 0 op_sel_hi:[1,0]
	v_pk_add_f32 v[136:137], v[100:101], v[180:181]
	v_mul_f32_e32 v100, v119, v119
	v_mul_f32_e32 v101, v121, v121
	v_pk_add_f32 v[116:117], v[116:117], v[142:143]
	v_pk_add_f32 v[114:115], v[114:115], v[140:141]
	v_pk_add_f32 v[98:99], v[98:99], 0 op_sel_hi:[1,0]
	v_fmac_f32_e32 v100, v118, v118
	v_fmac_f32_e32 v101, v120, v120
	v_pk_add_f32 v[138:139], v[98:99], v[182:183]
	v_cvt_pk_bf16_f32 v98, v118, v119
	v_add_f32_e32 v100, v100, v101
	v_mul_f32_e32 v101, v115, v115
	v_mul_f32_e32 v118, v117, v117
	v_lshlrev_b32_e32 v144, 16, v178
	v_and_b32_e32 v145, 0xffff0000, v178
	v_lshlrev_b32_e32 v178, 16, v179
	v_and_b32_e32 v179, 0xffff0000, v179
	v_pk_add_f32 v[104:105], v[104:105], 0 op_sel_hi:[1,0]
	v_pk_add_f32 v[102:103], v[102:103], 0 op_sel_hi:[1,0]
	v_fmac_f32_e32 v101, v114, v114
	v_fmac_f32_e32 v118, v116, v116
	v_pk_add_f32 v[104:105], v[104:105], v[178:179]
	v_pk_add_f32 v[102:103], v[102:103], v[144:145]
	v_add_f32_e32 v101, v101, v118
	v_add_f32_e32 v100, v100, v101
	v_mul_f32_e32 v101, v103, v103
	v_mul_f32_e32 v118, v105, v105
	v_fmac_f32_e32 v101, v102, v102
	v_fmac_f32_e32 v118, v104, v104
	v_add_f32_e32 v101, v101, v118
	v_mul_f32_e32 v118, v139, v139
	v_mul_f32_e32 v119, v137, v137
	v_fmac_f32_e32 v118, v138, v138
	v_fmac_f32_e32 v119, v136, v136
	v_add_f32_e32 v118, v118, v119
	v_add_f32_e32 v101, v101, v118
	v_add_f32_e32 v118, v100, v101
	v_mov_b32_e32 v119, v118
	s_nop 1
	v_permlane16_swap_b32_e32 v118, v119
	s_mov_b64 s[0:1], 0x8000
	s_waitcnt lgkmcnt(1)
	v_lshl_add_u64 v[132:133], v[198:199], 0, s[0:1]
	v_cvt_pk_bf16_f32 v99, v120, v121
	v_cvt_pk_bf16_f32 v100, v114, v115
	v_cvt_pk_bf16_f32 v101, v116, v117
	global_store_dwordx4 v[132:133], v[98:101], off
	s_mov_b64 s[0:1], 0x8100
	v_lshl_add_u64 v[134:135], v[198:199], 0, s[0:1]
	s_waitcnt lgkmcnt(0)
	v_add_f32_e32 v98, v118, v119
	v_mov_b32_e32 v99, v98
	s_nop 1
	v_permlane32_swap_b32_e32 v98, v99
	v_cvt_pk_bf16_f32 v100, v102, v103
	v_cvt_pk_bf16_f32 v101, v104, v105
	v_cvt_pk_bf16_f32 v102, v138, v139
	v_cvt_pk_bf16_f32 v103, v136, v137
	global_store_dwordx4 v[134:135], v[100:103], off
	s_and_saveexec_b64 s[22:23], s[4:5]
	s_cbranch_execz .LBB0_2042
	s_waitcnt lgkmcnt(0)
	v_add_f32_e32 v98, v98, v99
	global_store_dword v[200:201], v98, off offset:1024
.LBB0_2042:
	s_or_b64 exec, exec, s[22:23]
	s_waitcnt vmcnt(15)
	v_lshlrev_b32_e32 v102, 16, v174
	v_and_b32_e32 v103, 0xffff0000, v174
	v_lshlrev_b32_e32 v104, 16, v175
	v_and_b32_e32 v105, 0xffff0000, v175
	v_pk_add_f32 v[96:97], v[96:97], 0 op_sel_hi:[1,0]
	v_pk_add_f32 v[94:95], v[94:95], 0 op_sel_hi:[1,0]
	s_waitcnt vmcnt(14)
	v_lshlrev_b32_e32 v134, 16, v173
	v_and_b32_e32 v135, 0xffff0000, v173
	v_pk_add_f32 v[96:97], v[96:97], v[104:105]
	v_pk_add_f32 v[94:95], v[94:95], v[102:103]
	v_pk_add_f32 v[84:85], v[84:85], 0 op_sel_hi:[1,0]
	v_lshlrev_b32_e32 v114, 16, v176
	v_and_b32_e32 v115, 0xffff0000, v176
	v_lshlrev_b32_e32 v116, 16, v177
	v_and_b32_e32 v117, 0xffff0000, v177
	v_pk_add_f32 v[92:93], v[92:93], 0 op_sel_hi:[1,0]
	v_pk_add_f32 v[90:91], v[90:91], 0 op_sel_hi:[1,0]
	v_pk_add_f32 v[102:103], v[84:85], v[134:135]
	v_mul_f32_e32 v84, v95, v95
	v_mul_f32_e32 v85, v97, v97
	v_lshlrev_b32_e32 v132, 16, v172
	v_and_b32_e32 v133, 0xffff0000, v172
	v_pk_add_f32 v[92:93], v[92:93], v[116:117]
	v_pk_add_f32 v[90:91], v[90:91], v[114:115]
	v_pk_add_f32 v[82:83], v[82:83], 0 op_sel_hi:[1,0]
	v_fmac_f32_e32 v84, v94, v94
	v_fmac_f32_e32 v85, v96, v96
	v_pk_add_f32 v[104:105], v[82:83], v[132:133]
	v_cvt_pk_bf16_f32 v82, v94, v95
	v_add_f32_e32 v84, v84, v85
	v_mul_f32_e32 v85, v91, v91
	v_mul_f32_e32 v94, v93, v93
	v_lshlrev_b32_e32 v118, 16, v170
	v_and_b32_e32 v119, 0xffff0000, v170
	v_lshlrev_b32_e32 v120, 16, v171
	v_and_b32_e32 v121, 0xffff0000, v171
	v_pk_add_f32 v[88:89], v[88:89], 0 op_sel_hi:[1,0]
	v_pk_add_f32 v[86:87], v[86:87], 0 op_sel_hi:[1,0]
	v_fmac_f32_e32 v85, v90, v90
	v_fmac_f32_e32 v94, v92, v92
	v_pk_add_f32 v[88:89], v[88:89], v[120:121]
	v_pk_add_f32 v[86:87], v[86:87], v[118:119]
	v_add_f32_e32 v85, v85, v94
	v_add_f32_e32 v84, v84, v85
	v_mul_f32_e32 v85, v87, v87
	v_mul_f32_e32 v94, v89, v89
	v_fmac_f32_e32 v85, v86, v86
	v_fmac_f32_e32 v94, v88, v88
	v_add_f32_e32 v85, v85, v94
	v_mul_f32_e32 v94, v105, v105
	v_mul_f32_e32 v95, v103, v103
	v_fmac_f32_e32 v94, v104, v104
	v_fmac_f32_e32 v95, v102, v102
	v_add_f32_e32 v94, v94, v95
	v_add_f32_e32 v85, v85, v94
	v_add_f32_e32 v94, v84, v85
	v_mov_b32_e32 v95, v94
	s_nop 1
	v_permlane16_swap_b32_e32 v94, v95
	s_mov_b64 s[0:1], 0x10000
	s_waitcnt lgkmcnt(1)
	v_lshl_add_u64 v[98:99], v[198:199], 0, s[0:1]
	v_cvt_pk_bf16_f32 v83, v96, v97
	v_cvt_pk_bf16_f32 v84, v90, v91
	v_cvt_pk_bf16_f32 v85, v92, v93
	global_store_dwordx4 v[98:99], v[82:85], off
	s_mov_b64 s[0:1], 0x10100
	v_lshl_add_u64 v[100:101], v[198:199], 0, s[0:1]
	s_waitcnt lgkmcnt(0)
	v_add_f32_e32 v82, v94, v95
	v_mov_b32_e32 v83, v82
	s_nop 1
	v_permlane32_swap_b32_e32 v82, v83
	v_cvt_pk_bf16_f32 v84, v86, v87
	v_cvt_pk_bf16_f32 v85, v88, v89
	v_cvt_pk_bf16_f32 v86, v104, v105
	v_cvt_pk_bf16_f32 v87, v102, v103
	global_store_dwordx4 v[100:101], v[84:87], off
	s_and_saveexec_b64 s[22:23], s[4:5]
	s_cbranch_execz .LBB0_2044
	s_waitcnt lgkmcnt(0)
	v_add_f32_e32 v82, v82, v83
	global_store_dword v[200:201], v82, off offset:2048
.LBB0_2044:
	s_or_b64 exec, exec, s[22:23]
	s_waitcnt vmcnt(15)
	v_lshlrev_b32_e32 v86, 16, v166
	v_and_b32_e32 v87, 0xffff0000, v166
	v_lshlrev_b32_e32 v88, 16, v167
	v_and_b32_e32 v89, 0xffff0000, v167
	v_pk_add_f32 v[80:81], v[80:81], 0 op_sel_hi:[1,0]
	v_pk_add_f32 v[78:79], v[78:79], 0 op_sel_hi:[1,0]
	s_waitcnt vmcnt(14)
	v_lshlrev_b32_e32 v100, 16, v165
	v_and_b32_e32 v101, 0xffff0000, v165
	v_pk_add_f32 v[80:81], v[80:81], v[88:89]
	v_pk_add_f32 v[78:79], v[78:79], v[86:87]
	v_pk_add_f32 v[68:69], v[68:69], 0 op_sel_hi:[1,0]
	v_lshlrev_b32_e32 v90, 16, v168
	v_and_b32_e32 v91, 0xffff0000, v168
	v_lshlrev_b32_e32 v92, 16, v169
	v_and_b32_e32 v93, 0xffff0000, v169
	v_pk_add_f32 v[76:77], v[76:77], 0 op_sel_hi:[1,0]
	v_pk_add_f32 v[74:75], v[74:75], 0 op_sel_hi:[1,0]
	v_pk_add_f32 v[86:87], v[68:69], v[100:101]
	v_mul_f32_e32 v68, v79, v79
	v_mul_f32_e32 v69, v81, v81
	v_lshlrev_b32_e32 v98, 16, v164
	v_and_b32_e32 v99, 0xffff0000, v164
	v_pk_add_f32 v[76:77], v[76:77], v[92:93]
	v_pk_add_f32 v[74:75], v[74:75], v[90:91]
	v_pk_add_f32 v[66:67], v[66:67], 0 op_sel_hi:[1,0]
	v_fmac_f32_e32 v68, v78, v78
	v_fmac_f32_e32 v69, v80, v80
	v_pk_add_f32 v[88:89], v[66:67], v[98:99]
	v_cvt_pk_bf16_f32 v66, v78, v79
	v_add_f32_e32 v68, v68, v69
	v_mul_f32_e32 v69, v75, v75
	v_mul_f32_e32 v78, v77, v77
	v_lshlrev_b32_e32 v94, 16, v162
	v_and_b32_e32 v95, 0xffff0000, v162
	v_lshlrev_b32_e32 v96, 16, v163
	v_and_b32_e32 v97, 0xffff0000, v163
	v_pk_add_f32 v[72:73], v[72:73], 0 op_sel_hi:[1,0]
	v_pk_add_f32 v[70:71], v[70:71], 0 op_sel_hi:[1,0]
	v_fmac_f32_e32 v69, v74, v74
	v_fmac_f32_e32 v78, v76, v76
	v_pk_add_f32 v[72:73], v[72:73], v[96:97]
	v_pk_add_f32 v[70:71], v[70:71], v[94:95]
	v_add_f32_e32 v69, v69, v78
	v_add_f32_e32 v68, v68, v69
	v_mul_f32_e32 v69, v71, v71
	v_mul_f32_e32 v78, v73, v73
	v_fmac_f32_e32 v69, v70, v70
	v_fmac_f32_e32 v78, v72, v72
	v_add_f32_e32 v69, v69, v78
	v_mul_f32_e32 v78, v89, v89
	v_mul_f32_e32 v79, v87, v87
	v_fmac_f32_e32 v78, v88, v88
	v_fmac_f32_e32 v79, v86, v86
	v_add_f32_e32 v78, v78, v79
	v_add_f32_e32 v69, v69, v78
	v_add_f32_e32 v78, v68, v69
	v_mov_b32_e32 v79, v78
	s_nop 1
	v_permlane16_swap_b32_e32 v78, v79
	s_mov_b64 s[0:1], 0x18000
	s_waitcnt lgkmcnt(1)
	v_lshl_add_u64 v[82:83], v[198:199], 0, s[0:1]
	v_cvt_pk_bf16_f32 v67, v80, v81
	v_cvt_pk_bf16_f32 v68, v74, v75
	v_cvt_pk_bf16_f32 v69, v76, v77
	global_store_dwordx4 v[82:83], v[66:69], off
	s_mov_b64 s[0:1], 0x18100
	v_lshl_add_u64 v[84:85], v[198:199], 0, s[0:1]
	s_waitcnt lgkmcnt(0)
	v_add_f32_e32 v66, v78, v79
	v_mov_b32_e32 v67, v66
	s_nop 1
	v_permlane32_swap_b32_e32 v66, v67
	v_cvt_pk_bf16_f32 v68, v70, v71
	v_cvt_pk_bf16_f32 v69, v72, v73
	v_cvt_pk_bf16_f32 v70, v88, v89
	v_cvt_pk_bf16_f32 v71, v86, v87
	global_store_dwordx4 v[84:85], v[68:71], off
	s_and_saveexec_b64 s[22:23], s[4:5]
	s_cbranch_execz .LBB0_2046
	s_waitcnt lgkmcnt(0)
	v_add_f32_e32 v66, v66, v67
	global_store_dword v[200:201], v66, off offset:3072
.LBB0_2046:
	s_or_b64 exec, exec, s[22:23]
	s_waitcnt vmcnt(15)
	v_lshlrev_b32_e32 v70, 16, v158
	v_and_b32_e32 v71, 0xffff0000, v158
	v_lshlrev_b32_e32 v74, 16, v160
	v_and_b32_e32 v75, 0xffff0000, v160
	v_lshlrev_b32_e32 v76, 16, v161
	v_and_b32_e32 v77, 0xffff0000, v161
	v_pk_add_f32 v[54:55], v[54:55], 0 op_sel_hi:[1,0]
	v_pk_add_f32 v[52:53], v[52:53], 0 op_sel_hi:[1,0]
	v_pk_add_f32 v[50:51], v[50:51], 0 op_sel_hi:[1,0]
	s_waitcnt vmcnt(14)
	v_lshlrev_b32_e32 v80, 16, v155
	v_and_b32_e32 v81, 0xffff0000, v155
	v_pk_add_f32 v[54:55], v[54:55], v[70:71]
	v_pk_add_f32 v[70:71], v[52:53], v[76:77]
	v_pk_add_f32 v[52:53], v[50:51], v[74:75]
	v_pk_add_f32 v[50:51], v[64:65], 0 op_sel_hi:[1,0]
	v_lshlrev_b32_e32 v72, 16, v159
	v_and_b32_e32 v73, 0xffff0000, v159
	v_lshlrev_b32_e32 v84, 16, v157
	v_and_b32_e32 v85, 0xffff0000, v157
	v_pk_add_f32 v[56:57], v[56:57], 0 op_sel_hi:[1,0]
	v_pk_add_f32 v[64:65], v[50:51], v[80:81]
	v_pk_add_f32 v[50:51], v[60:61], 0 op_sel_hi:[1,0]
	v_pk_add_f32 v[56:57], v[56:57], v[72:73]
	v_pk_add_f32 v[60:61], v[50:51], v[84:85]
	v_cvt_pk_bf16_f32 v50, v54, v55
	v_mul_f32_e32 v55, v55, v55
	v_fmac_f32_e32 v55, v54, v54
	v_mul_f32_e32 v54, v57, v57
	v_fmac_f32_e32 v54, v56, v56
	v_cvt_pk_bf16_f32 v51, v56, v57
	v_add_f32_e32 v54, v55, v54
	v_mul_f32_e32 v55, v53, v53
	v_mul_f32_e32 v56, v71, v71
	v_lshlrev_b32_e32 v78, 16, v154
	v_and_b32_e32 v79, 0xffff0000, v154
	v_pk_add_f32 v[62:63], v[62:63], 0 op_sel_hi:[1,0]
	v_fmac_f32_e32 v55, v52, v52
	v_fmac_f32_e32 v56, v70, v70
	v_pk_add_f32 v[62:63], v[62:63], v[78:79]
	v_add_f32_e32 v55, v55, v56
	v_lshlrev_b32_e32 v82, 16, v156
	v_and_b32_e32 v83, 0xffff0000, v156
	v_pk_add_f32 v[58:59], v[58:59], 0 op_sel_hi:[1,0]
	v_add_f32_e32 v54, v54, v55
	v_mul_f32_e32 v55, v63, v63
	v_mul_f32_e32 v56, v65, v65
	v_pk_add_f32 v[58:59], v[58:59], v[82:83]
	v_fmac_f32_e32 v55, v62, v62
	v_fmac_f32_e32 v56, v64, v64
	v_add_f32_e32 v55, v55, v56
	v_mul_f32_e32 v56, v59, v59
	v_mul_f32_e32 v57, v61, v61
	v_fmac_f32_e32 v56, v58, v58
	v_fmac_f32_e32 v57, v60, v60
	v_add_f32_e32 v56, v56, v57
	v_add_f32_e32 v55, v55, v56
	v_add_f32_e32 v54, v54, v55
	v_mov_b32_e32 v55, v54
	s_nop 1
	v_permlane16_swap_b32_e32 v54, v55
	s_mov_b64 s[0:1], 0x40000
	s_waitcnt lgkmcnt(1)
	v_lshl_add_u64 v[66:67], v[198:199], 0, s[0:1]
	v_cvt_pk_bf16_f32 v52, v52, v53
	v_cvt_pk_bf16_f32 v53, v70, v71
	global_store_dwordx4 v[66:67], v[50:53], off
	s_mov_b64 s[0:1], 0x40100
	v_lshl_add_u64 v[68:69], v[198:199], 0, s[0:1]
	s_waitcnt lgkmcnt(0)
	v_add_f32_e32 v50, v54, v55
	v_mov_b32_e32 v51, v50
	s_nop 1
	v_permlane32_swap_b32_e32 v50, v51
	v_cvt_pk_bf16_f32 v52, v62, v63
	v_cvt_pk_bf16_f32 v53, v64, v65
	v_cvt_pk_bf16_f32 v54, v58, v59
	v_cvt_pk_bf16_f32 v55, v60, v61
	global_store_dwordx4 v[68:69], v[52:55], off
	s_and_saveexec_b64 s[22:23], s[4:5]
	s_cbranch_execz .LBB0_2048
	s_waitcnt lgkmcnt(0)
	v_add_f32_e32 v52, v50, v51
	v_add_co_u32_e32 v50, vcc, 0x2000, v200
	s_nop 1
	v_addc_co_u32_e32 v51, vcc, 0, v201, vcc
	global_store_dword v[50:51], v52, off
.LBB0_2048:
	s_or_b64 exec, exec, s[22:23]
	s_waitcnt vmcnt(15)
	v_lshlrev_b32_e32 v54, 16, v150
	v_and_b32_e32 v55, 0xffff0000, v150
	v_lshlrev_b32_e32 v58, 16, v152
	v_and_b32_e32 v59, 0xffff0000, v152
	v_lshlrev_b32_e32 v60, 16, v153
	v_and_b32_e32 v61, 0xffff0000, v153
	v_pk_add_f32 v[38:39], v[38:39], 0 op_sel_hi:[1,0]
	v_pk_add_f32 v[36:37], v[36:37], 0 op_sel_hi:[1,0]
	v_pk_add_f32 v[34:35], v[34:35], 0 op_sel_hi:[1,0]
	s_waitcnt vmcnt(14)
	v_lshlrev_b32_e32 v64, 16, v147
	v_and_b32_e32 v65, 0xffff0000, v147
	v_pk_add_f32 v[38:39], v[38:39], v[54:55]
	v_pk_add_f32 v[54:55], v[36:37], v[60:61]
	v_pk_add_f32 v[36:37], v[34:35], v[58:59]
	v_pk_add_f32 v[34:35], v[48:49], 0 op_sel_hi:[1,0]
	v_lshlrev_b32_e32 v56, 16, v151
	v_and_b32_e32 v57, 0xffff0000, v151
	v_lshlrev_b32_e32 v68, 16, v149
	v_and_b32_e32 v69, 0xffff0000, v149
	v_pk_add_f32 v[40:41], v[40:41], 0 op_sel_hi:[1,0]
	v_pk_add_f32 v[48:49], v[34:35], v[64:65]
	v_pk_add_f32 v[34:35], v[44:45], 0 op_sel_hi:[1,0]
	v_pk_add_f32 v[40:41], v[40:41], v[56:57]
	v_pk_add_f32 v[44:45], v[34:35], v[68:69]
	v_cvt_pk_bf16_f32 v34, v38, v39
	v_mul_f32_e32 v39, v39, v39
	v_fmac_f32_e32 v39, v38, v38
	v_mul_f32_e32 v38, v41, v41
	v_fmac_f32_e32 v38, v40, v40
	v_cvt_pk_bf16_f32 v35, v40, v41
	v_add_f32_e32 v38, v39, v38
	v_mul_f32_e32 v39, v37, v37
	v_mul_f32_e32 v40, v55, v55
	v_lshlrev_b32_e32 v62, 16, v146
	v_and_b32_e32 v63, 0xffff0000, v146
	v_pk_add_f32 v[46:47], v[46:47], 0 op_sel_hi:[1,0]
	v_fmac_f32_e32 v39, v36, v36
	v_fmac_f32_e32 v40, v54, v54
	v_pk_add_f32 v[46:47], v[46:47], v[62:63]
	v_add_f32_e32 v39, v39, v40
	v_lshlrev_b32_e32 v66, 16, v148
	v_and_b32_e32 v67, 0xffff0000, v148
	v_pk_add_f32 v[42:43], v[42:43], 0 op_sel_hi:[1,0]
	v_add_f32_e32 v38, v38, v39
	v_mul_f32_e32 v39, v47, v47
	v_mul_f32_e32 v40, v49, v49
	v_pk_add_f32 v[42:43], v[42:43], v[66:67]
	v_fmac_f32_e32 v39, v46, v46
	v_fmac_f32_e32 v40, v48, v48
	v_add_f32_e32 v39, v39, v40
	v_mul_f32_e32 v40, v43, v43
	v_mul_f32_e32 v41, v45, v45
	v_fmac_f32_e32 v40, v42, v42
	v_fmac_f32_e32 v41, v44, v44
	v_add_f32_e32 v40, v40, v41
	v_add_f32_e32 v39, v39, v40
	v_add_f32_e32 v38, v38, v39
	v_mov_b32_e32 v39, v38
	s_nop 1
	v_permlane16_swap_b32_e32 v38, v39
	s_mov_b64 s[0:1], 0x48000
	s_waitcnt lgkmcnt(1)
	v_lshl_add_u64 v[50:51], v[198:199], 0, s[0:1]
	v_cvt_pk_bf16_f32 v36, v36, v37
	v_cvt_pk_bf16_f32 v37, v54, v55
	global_store_dwordx4 v[50:51], v[34:37], off
	s_mov_b64 s[0:1], 0x48100
	v_lshl_add_u64 v[52:53], v[198:199], 0, s[0:1]
	s_waitcnt lgkmcnt(0)
	v_add_f32_e32 v34, v38, v39
	v_mov_b32_e32 v35, v34
	s_nop 1
	v_permlane32_swap_b32_e32 v34, v35
	v_cvt_pk_bf16_f32 v36, v46, v47
	v_cvt_pk_bf16_f32 v37, v48, v49
	v_cvt_pk_bf16_f32 v38, v42, v43
	v_cvt_pk_bf16_f32 v39, v44, v45
	global_store_dwordx4 v[52:53], v[36:39], off
	s_and_saveexec_b64 s[22:23], s[4:5]
	s_cbranch_execz .LBB0_2050
	s_waitcnt lgkmcnt(0)
	v_add_f32_e32 v36, v34, v35
	v_add_co_u32_e32 v34, vcc, 0x2000, v200
	s_nop 1
	v_addc_co_u32_e32 v35, vcc, 0, v201, vcc
	global_store_dword v[34:35], v36, off offset:1024
.LBB0_2050:
	s_or_b64 exec, exec, s[22:23]
	s_waitcnt vmcnt(15)
	v_lshlrev_b32_e32 v38, 16, v126
	v_and_b32_e32 v39, 0xffff0000, v126
	v_lshlrev_b32_e32 v42, 16, v128
	v_and_b32_e32 v43, 0xffff0000, v128
	v_lshlrev_b32_e32 v44, 16, v129
	v_and_b32_e32 v45, 0xffff0000, v129
	v_pk_add_f32 v[22:23], v[22:23], 0 op_sel_hi:[1,0]
	v_pk_add_f32 v[20:21], v[20:21], 0 op_sel_hi:[1,0]
	v_pk_add_f32 v[18:19], v[18:19], 0 op_sel_hi:[1,0]
	s_waitcnt vmcnt(14)
	v_lshlrev_b32_e32 v48, 16, v123
	v_and_b32_e32 v49, 0xffff0000, v123
	v_pk_add_f32 v[22:23], v[22:23], v[38:39]
	v_pk_add_f32 v[38:39], v[20:21], v[44:45]
	v_pk_add_f32 v[20:21], v[18:19], v[42:43]
	v_pk_add_f32 v[18:19], v[32:33], 0 op_sel_hi:[1,0]
	v_lshlrev_b32_e32 v40, 16, v127
	v_and_b32_e32 v41, 0xffff0000, v127
	v_lshlrev_b32_e32 v52, 16, v125
	v_and_b32_e32 v53, 0xffff0000, v125
	v_pk_add_f32 v[24:25], v[24:25], 0 op_sel_hi:[1,0]
	v_pk_add_f32 v[32:33], v[18:19], v[48:49]
	v_pk_add_f32 v[18:19], v[28:29], 0 op_sel_hi:[1,0]
	v_pk_add_f32 v[24:25], v[24:25], v[40:41]
	v_pk_add_f32 v[28:29], v[18:19], v[52:53]
	v_cvt_pk_bf16_f32 v18, v22, v23
	v_mul_f32_e32 v23, v23, v23
	v_fmac_f32_e32 v23, v22, v22
	v_mul_f32_e32 v22, v25, v25
	v_fmac_f32_e32 v22, v24, v24
	v_cvt_pk_bf16_f32 v19, v24, v25
	v_add_f32_e32 v22, v23, v22
	v_mul_f32_e32 v23, v21, v21
	v_mul_f32_e32 v24, v39, v39
	v_lshlrev_b32_e32 v46, 16, v122
	v_and_b32_e32 v47, 0xffff0000, v122
	v_pk_add_f32 v[30:31], v[30:31], 0 op_sel_hi:[1,0]
	v_fmac_f32_e32 v23, v20, v20
	v_fmac_f32_e32 v24, v38, v38
	v_pk_add_f32 v[30:31], v[30:31], v[46:47]
	v_add_f32_e32 v23, v23, v24
	v_lshlrev_b32_e32 v50, 16, v124
	v_and_b32_e32 v51, 0xffff0000, v124
	v_pk_add_f32 v[26:27], v[26:27], 0 op_sel_hi:[1,0]
	v_add_f32_e32 v22, v22, v23
	v_mul_f32_e32 v23, v31, v31
	v_mul_f32_e32 v24, v33, v33
	v_pk_add_f32 v[26:27], v[26:27], v[50:51]
	v_fmac_f32_e32 v23, v30, v30
	v_fmac_f32_e32 v24, v32, v32
	v_add_f32_e32 v23, v23, v24
	v_mul_f32_e32 v24, v27, v27
	v_mul_f32_e32 v25, v29, v29
	v_fmac_f32_e32 v24, v26, v26
	v_fmac_f32_e32 v25, v28, v28
	v_add_f32_e32 v24, v24, v25
	v_add_f32_e32 v23, v23, v24
	v_add_f32_e32 v22, v22, v23
	v_mov_b32_e32 v23, v22
	s_nop 1
	v_permlane16_swap_b32_e32 v22, v23
	s_mov_b64 s[0:1], 0x50000
	s_waitcnt lgkmcnt(1)
	v_lshl_add_u64 v[34:35], v[198:199], 0, s[0:1]
	v_cvt_pk_bf16_f32 v20, v20, v21
	v_cvt_pk_bf16_f32 v21, v38, v39
	global_store_dwordx4 v[34:35], v[18:21], off
	s_mov_b64 s[0:1], 0x50100
	v_lshl_add_u64 v[36:37], v[198:199], 0, s[0:1]
	s_waitcnt lgkmcnt(0)
	v_add_f32_e32 v18, v22, v23
	v_mov_b32_e32 v19, v18
	s_nop 1
	v_permlane32_swap_b32_e32 v18, v19
	v_cvt_pk_bf16_f32 v20, v30, v31
	v_cvt_pk_bf16_f32 v21, v32, v33
	v_cvt_pk_bf16_f32 v22, v26, v27
	v_cvt_pk_bf16_f32 v23, v28, v29
	global_store_dwordx4 v[36:37], v[20:23], off
	s_and_saveexec_b64 s[22:23], s[4:5]
	s_cbranch_execz .LBB0_2052
	s_waitcnt lgkmcnt(0)
	v_add_f32_e32 v20, v18, v19
	v_add_co_u32_e32 v18, vcc, 0x2000, v200
	s_nop 1
	v_addc_co_u32_e32 v19, vcc, 0, v201, vcc
	global_store_dword v[18:19], v20, off offset:2048
.LBB0_2052:
	s_or_b64 exec, exec, s[22:23]
	s_waitcnt vmcnt(15)
	v_lshlrev_b32_e32 v22, 16, v110
	v_and_b32_e32 v23, 0xffff0000, v110
	v_lshlrev_b32_e32 v26, 16, v112
	v_and_b32_e32 v27, 0xffff0000, v112
	v_lshlrev_b32_e32 v28, 16, v113
	v_and_b32_e32 v29, 0xffff0000, v113
	v_pk_add_f32 v[6:7], v[6:7], 0 op_sel_hi:[1,0]
	v_pk_add_f32 v[4:5], v[4:5], 0 op_sel_hi:[1,0]
	v_pk_add_f32 v[2:3], v[2:3], 0 op_sel_hi:[1,0]
	s_waitcnt vmcnt(14)
	v_lshlrev_b32_e32 v32, 16, v107
	v_and_b32_e32 v33, 0xffff0000, v107
	v_pk_add_f32 v[6:7], v[6:7], v[22:23]
	v_pk_add_f32 v[22:23], v[4:5], v[28:29]
	v_pk_add_f32 v[4:5], v[2:3], v[26:27]
	v_pk_add_f32 v[2:3], v[16:17], 0 op_sel_hi:[1,0]
	v_lshlrev_b32_e32 v24, 16, v111
	v_and_b32_e32 v25, 0xffff0000, v111
	v_lshlrev_b32_e32 v36, 16, v109
	v_and_b32_e32 v37, 0xffff0000, v109
	v_pk_add_f32 v[8:9], v[8:9], 0 op_sel_hi:[1,0]
	v_pk_add_f32 v[16:17], v[2:3], v[32:33]
	v_pk_add_f32 v[2:3], v[12:13], 0 op_sel_hi:[1,0]
	v_pk_add_f32 v[8:9], v[8:9], v[24:25]
	v_pk_add_f32 v[12:13], v[2:3], v[36:37]
	v_cvt_pk_bf16_f32 v2, v6, v7
	v_mul_f32_e32 v7, v7, v7
	v_fmac_f32_e32 v7, v6, v6
	v_mul_f32_e32 v6, v9, v9
	v_fmac_f32_e32 v6, v8, v8
	v_cvt_pk_bf16_f32 v3, v8, v9
	v_add_f32_e32 v6, v7, v6
	v_mul_f32_e32 v7, v5, v5
	v_mul_f32_e32 v8, v23, v23
	v_lshlrev_b32_e32 v30, 16, v106
	v_and_b32_e32 v31, 0xffff0000, v106
	v_pk_add_f32 v[14:15], v[14:15], 0 op_sel_hi:[1,0]
	v_fmac_f32_e32 v7, v4, v4
	v_fmac_f32_e32 v8, v22, v22
	v_pk_add_f32 v[14:15], v[14:15], v[30:31]
	v_add_f32_e32 v7, v7, v8
	v_lshlrev_b32_e32 v34, 16, v108
	v_and_b32_e32 v35, 0xffff0000, v108
	v_pk_add_f32 v[10:11], v[10:11], 0 op_sel_hi:[1,0]
	v_add_f32_e32 v6, v6, v7
	v_mul_f32_e32 v7, v15, v15
	v_mul_f32_e32 v8, v17, v17
	v_pk_add_f32 v[10:11], v[10:11], v[34:35]
	v_fmac_f32_e32 v7, v14, v14
	v_fmac_f32_e32 v8, v16, v16
	v_add_f32_e32 v7, v7, v8
	v_mul_f32_e32 v8, v11, v11
	v_mul_f32_e32 v9, v13, v13
	v_fmac_f32_e32 v8, v10, v10
	v_fmac_f32_e32 v9, v12, v12
	v_add_f32_e32 v8, v8, v9
	v_add_f32_e32 v7, v7, v8
	v_add_f32_e32 v6, v6, v7
	v_mov_b32_e32 v7, v6
	s_nop 1
	v_permlane16_swap_b32_e32 v6, v7
	s_mov_b64 s[0:1], 0x58000
	s_waitcnt lgkmcnt(1)
	v_lshl_add_u64 v[18:19], v[198:199], 0, s[0:1]
	v_cvt_pk_bf16_f32 v4, v4, v5
	v_cvt_pk_bf16_f32 v5, v22, v23
	global_store_dwordx4 v[18:19], v[2:5], off
	s_mov_b64 s[0:1], 0x58100
	v_lshl_add_u64 v[20:21], v[198:199], 0, s[0:1]
	s_waitcnt lgkmcnt(0)
	v_add_f32_e32 v2, v6, v7
	v_mov_b32_e32 v3, v2
	s_nop 1
	v_permlane32_swap_b32_e32 v2, v3
	v_cvt_pk_bf16_f32 v4, v14, v15
	v_cvt_pk_bf16_f32 v5, v16, v17
	v_cvt_pk_bf16_f32 v6, v10, v11
	v_cvt_pk_bf16_f32 v7, v12, v13
	global_store_dwordx4 v[20:21], v[4:7], off
	s_and_saveexec_b64 s[22:23], s[4:5]
	s_cbranch_execz .LBB0_2054
	s_waitcnt lgkmcnt(0)
	v_add_f32_e32 v4, v2, v3
	v_add_co_u32_e32 v2, vcc, 0x2000, v200
	s_nop 1
	v_addc_co_u32_e32 v3, vcc, 0, v201, vcc
	global_store_dword v[2:3], v4, off offset:3072

.LBB0_2076:
	s_ashr_i32 s5, s4, 31
	s_lshl_b64 s[0:1], s[4:5], 8
	s_add_u32 s0, s0, s49
	s_addc_u32 s1, s1, s58
	s_lshl_b32 s4, s16, 8
	s_ashr_i32 s5, s4, 31
	s_lshl_b64 s[18:19], s[0:1], 11
	v_readlane_b32 s22, v252, 58
	v_readlane_b32 s23, v252, 59
	s_add_u32 s17, s22, s18
	s_addc_u32 s18, s23, s19
	s_lshl_b64 s[4:5], s[4:5], 1
	s_add_u32 s4, s17, s4
	v_mov_b32_e32 v200, v208
	v_mov_b32_e32 v201, v207
	s_addc_u32 s5, s18, s5
	s_add_u32 s22, s4, s60
	v_lshlrev_b32_e32 v130, 11, v200
	s_addc_u32 s23, s5, 0
	v_lshl_add_u32 v202, v201, 4, v130
	global_load_dwordx4 v[190:193], v202, s[22:23]
	global_load_dwordx4 v[186:189], v202, s[22:23] offset:256
	s_lshl_b64 s[0:1], s[0:1], 6
	v_readlane_b32 s4, v250, 7
	v_readlane_b32 s5, v250, 8
	s_add_u32 s4, s4, s0
	s_addc_u32 s5, s5, s1
	s_lshl_b32 s0, s16, 2
	s_ashr_i32 s1, s0, 31
	s_lshl_b64 s[0:1], s[0:1], 2
	s_add_u32 s0, s4, s0
	s_addc_u32 s1, s5, s1
	s_add_u32 s26, s0, s61
	v_lshl_add_u64 v[198:199], s[22:23], 0, v[202:203]
	s_mov_b32 s0, 0x8000
	v_add_co_u32_e32 v130, vcc, s0, v198
	s_mov_b32 s0, 0x10000
	s_nop 0
	v_addc_co_u32_e32 v131, vcc, 0, v199, vcc
	global_load_dwordx4 v[182:185], v[130:131], off
	global_load_dwordx4 v[178:181], v[130:131], off offset:256
	v_add_co_u32_e32 v130, vcc, s0, v198
	s_mov_b32 s0, 0x18000
	s_nop 0
	v_addc_co_u32_e32 v131, vcc, 0, v199, vcc
	global_load_dwordx4 v[174:177], v[130:131], off
	global_load_dwordx4 v[170:173], v[130:131], off offset:256
	v_add_co_u32_e32 v130, vcc, s0, v198
	s_mov_b32 s0, 0x40000
	s_nop 0
	v_addc_co_u32_e32 v131, vcc, 0, v199, vcc
	global_load_dwordx4 v[166:169], v[130:131], off
	global_load_dwordx4 v[162:165], v[130:131], off offset:256
	v_add_co_u32_e32 v130, vcc, s0, v198
	s_mov_b32 s0, 0x48000
	s_nop 0
	v_addc_co_u32_e32 v131, vcc, 0, v199, vcc
	global_load_dwordx4 v[158:161], v[130:131], off
	global_load_dwordx4 v[154:157], v[130:131], off offset:256
	v_add_co_u32_e32 v130, vcc, s0, v198
	s_mov_b32 s0, 0x50000
	s_nop 0
	v_addc_co_u32_e32 v131, vcc, 0, v199, vcc
	global_load_dwordx4 v[150:153], v[130:131], off
	global_load_dwordx4 v[146:149], v[130:131], off offset:256
	v_add_co_u32_e32 v130, vcc, s0, v198
	s_mov_b32 s0, 0x58000
	s_nop 0
	v_addc_co_u32_e32 v131, vcc, 0, v199, vcc
	global_load_dwordx4 v[142:145], v[130:131], off
	global_load_dwordx4 v[138:141], v[130:131], off offset:256
	v_add_co_u32_e32 v130, vcc, s0, v198
	s_mov_b32 s0, 0x3c800000
	s_nop 0
	v_addc_co_u32_e32 v131, vcc, 0, v199, vcc
	global_load_dwordx4 v[134:137], v[130:131], off
	s_nop 0
	global_load_dwordx4 v[130:133], v[130:131], off offset:256
	v_pk_fma_f32 v[116:117], v[116:117], s[0:1], 0 op_sel_hi:[1,0,0]
	v_pk_fma_f32 v[98:99], v[98:99], s[0:1], 0 op_sel_hi:[1,0,0]
	v_pk_fma_f32 v[114:115], v[114:115], s[0:1], 0 op_sel_hi:[1,0,0]
	v_pk_fma_f32 v[100:101], v[100:101], s[0:1], 0 op_sel_hi:[1,0,0]
	v_pk_fma_f32 v[120:121], v[120:121], s[0:1], 0 op_sel_hi:[1,0,0]
	v_pk_fma_f32 v[118:119], v[118:119], s[0:1], 0 op_sel_hi:[1,0,0]
	s_addc_u32 s27, s1, 0
	v_lshlrev_b32_e32 v200, 6, v200
	v_cmp_eq_u32_e64 s[4:5], 0, v201
	v_mov_b32_e32 v201, v203
	v_lshl_add_u64 v[200:201], s[26:27], 0, v[200:201]
	s_waitcnt vmcnt(15)
	v_lshlrev_b32_e32 v210, 16, v190
	v_and_b32_e32 v211, 0xffff0000, v190
	v_lshlrev_b32_e32 v190, 16, v191
	v_and_b32_e32 v191, 0xffff0000, v191
	s_waitcnt vmcnt(14)
	v_lshlrev_b32_e32 v218, 16, v186
	v_and_b32_e32 v219, 0xffff0000, v186
	v_lshlrev_b32_e32 v186, 16, v187
	v_and_b32_e32 v187, 0xffff0000, v187
	v_lshlrev_b32_e32 v220, 16, v188
	v_and_b32_e32 v221, 0xffff0000, v188
	v_lshlrev_b32_e32 v188, 16, v189
	v_and_b32_e32 v189, 0xffff0000, v189
	v_pk_add_f32 v[116:117], v[116:117], v[190:191]
	v_pk_add_f32 v[190:191], v[98:99], v[218:219]
	v_pk_fma_f32 v[98:99], v[104:105], s[0:1], 0 op_sel_hi:[1,0,0]
	v_lshlrev_b32_e32 v212, 16, v192
	v_and_b32_e32 v213, 0xffff0000, v192
	v_lshlrev_b32_e32 v192, 16, v193
	v_and_b32_e32 v193, 0xffff0000, v193
	v_pk_add_f32 v[114:115], v[114:115], v[210:211]
	v_pk_add_f32 v[186:187], v[100:101], v[186:187]
	v_pk_fma_f32 v[100:101], v[102:103], s[0:1], 0 op_sel_hi:[1,0,0]
	v_pk_add_f32 v[102:103], v[98:99], v[188:189]
	v_cvt_pk_bf16_f32 v98, v114, v115
	v_cvt_pk_bf16_f32 v99, v116, v117
	v_pk_add_f32 v[120:121], v[120:121], v[192:193]
	v_pk_add_f32 v[118:119], v[118:119], v[212:213]
	v_pk_add_f32 v[104:105], v[100:101], v[220:221]
	v_cvt_pk_bf16_f32 v100, v118, v119
	v_cvt_pk_bf16_f32 v101, v120, v121
	global_store_dwordx4 v202, v[98:101], s[22:23]
	s_nop 1
	v_cvt_pk_bf16_f32 v98, v190, v191
	v_cvt_pk_bf16_f32 v99, v186, v187
	v_cvt_pk_bf16_f32 v100, v104, v105
	v_cvt_pk_bf16_f32 v101, v102, v103
	global_store_dwordx4 v202, v[98:101], s[22:23] offset:256
	s_nop 1
	v_mul_f32_e32 v98, v115, v115
	v_mul_f32_e32 v99, v117, v117
	v_fmac_f32_e32 v98, v114, v114
	v_fmac_f32_e32 v99, v116, v116
	v_add_f32_e32 v98, v98, v99
	v_mul_f32_e32 v99, v119, v119
	v_mul_f32_e32 v100, v121, v121
	v_fmac_f32_e32 v99, v118, v118
	v_fmac_f32_e32 v100, v120, v120
	v_add_f32_e32 v99, v99, v100
	v_add_f32_e32 v98, v98, v99
	v_mul_f32_e32 v99, v191, v191
	v_mul_f32_e32 v100, v187, v187
	v_fmac_f32_e32 v99, v190, v190
	v_fmac_f32_e32 v100, v186, v186
	v_add_f32_e32 v99, v99, v100
	v_mul_f32_e32 v100, v105, v105
	v_mul_f32_e32 v101, v103, v103
	v_fmac_f32_e32 v100, v104, v104
	v_fmac_f32_e32 v101, v102, v102
	v_add_f32_e32 v100, v100, v101
	v_add_f32_e32 v99, v99, v100
	v_and_b32_e32 v100, 64, v248
	v_add_f32_e32 v99, v98, v99
	v_xor_b32_e32 v98, 16, v248
	v_add_u32_e32 v101, 64, v100
	v_cmp_lt_i32_e32 vcc, v98, v101
	s_nop 1
	v_cndmask_b32_e32 v98, v248, v98, vcc
	v_lshlrev_b32_e32 v98, 2, v98
	v_mov_b32_e32 v100, v99
	s_nop 1
	v_permlane16_swap_b32_e32 v99, v100
	s_waitcnt lgkmcnt(0)
	v_add_f32_e32 v100, v99, v100
	v_xor_b32_e32 v99, 32, v248
	v_cmp_lt_i32_e32 vcc, v99, v101
	s_nop 1
	v_cndmask_b32_e32 v99, v248, v99, vcc
	v_lshlrev_b32_e32 v99, 2, v99
	v_mov_b32_e32 v101, v100
	s_nop 1
	v_permlane32_swap_b32_e32 v100, v101
	s_and_saveexec_b64 s[22:23], s[4:5]
	s_cbranch_execz .LBB0_2078
	s_waitcnt lgkmcnt(0)
	v_add_f32_e32 v100, v100, v101
	global_store_dword v[200:201], v100, off
.LBB0_2078:
	s_or_b64 exec, exec, s[22:23]
	s_mov_b64 s[0:1], 0x8000
	v_lshl_add_u64 v[104:105], v[198:199], 0, s[0:1]
	s_mov_b64 s[0:1], 0x8100
	v_lshl_add_u64 v[114:115], v[198:199], 0, s[0:1]
	s_mov_b32 s0, 0x3c800000
	s_waitcnt vmcnt(15)
	v_lshlrev_b32_e32 v100, 16, v182
	s_waitcnt lgkmcnt(0)
	v_and_b32_e32 v101, 0xffff0000, v182
	v_pk_fma_f32 v[122:123], v[122:123], s[0:1], 0 op_sel_hi:[1,0,0]
	v_lshlrev_b32_e32 v118, 16, v185
	v_and_b32_e32 v119, 0xffff0000, v185
	v_pk_add_f32 v[122:123], v[122:123], v[100:101]
	v_pk_fma_f32 v[100:101], v[128:129], s[0:1], 0 op_sel_hi:[1,0,0]
	v_lshlrev_b32_e32 v102, 16, v183
	v_and_b32_e32 v103, 0xffff0000, v183
	s_waitcnt vmcnt(14)
	v_lshlrev_b32_e32 v120, 16, v178
	v_and_b32_e32 v121, 0xffff0000, v178
	v_lshlrev_b32_e32 v178, 16, v179
	v_and_b32_e32 v179, 0xffff0000, v179
	v_pk_fma_f32 v[124:125], v[124:125], s[0:1], 0 op_sel_hi:[1,0,0]
	v_pk_add_f32 v[118:119], v[100:101], v[118:119]
	v_pk_fma_f32 v[100:101], v[108:109], s[0:1], 0 op_sel_hi:[1,0,0]
	v_lshlrev_b32_e32 v182, 16, v180
	v_and_b32_e32 v183, 0xffff0000, v180
	v_lshlrev_b32_e32 v180, 16, v181
	v_and_b32_e32 v181, 0xffff0000, v181
	v_pk_add_f32 v[102:103], v[124:125], v[102:103]
	v_pk_fma_f32 v[106:107], v[106:107], s[0:1], 0 op_sel_hi:[1,0,0]
	v_pk_add_f32 v[108:109], v[100:101], v[178:179]
	v_pk_fma_f32 v[100:101], v[112:113], s[0:1], 0 op_sel_hi:[1,0,0]
	v_lshlrev_b32_e32 v116, 16, v184
	v_and_b32_e32 v117, 0xffff0000, v184
	v_pk_fma_f32 v[124:125], v[126:127], s[0:1], 0 op_sel_hi:[1,0,0]
	v_pk_add_f32 v[106:107], v[106:107], v[120:121]
	v_pk_add_f32 v[112:113], v[100:101], v[180:181]
	v_cvt_pk_bf16_f32 v100, v122, v123
	v_cvt_pk_bf16_f32 v101, v102, v103
	v_mul_f32_e32 v120, v123, v123
	v_mul_f32_e32 v103, v103, v103
	v_pk_add_f32 v[116:117], v[124:125], v[116:117]
	v_fmac_f32_e32 v120, v122, v122
	v_fmac_f32_e32 v103, v102, v102
	v_add_f32_e32 v102, v120, v103
	v_mul_f32_e32 v103, v117, v117
	v_mul_f32_e32 v120, v119, v119
	v_fmac_f32_e32 v103, v116, v116
	v_fmac_f32_e32 v120, v118, v118
	v_add_f32_e32 v103, v103, v120
	v_pk_fma_f32 v[110:111], v[110:111], s[0:1], 0 op_sel_hi:[1,0,0]
	v_add_f32_e32 v102, v102, v103
	v_mul_f32_e32 v103, v107, v107
	v_mul_f32_e32 v120, v109, v109
	v_pk_add_f32 v[110:111], v[110:111], v[182:183]
	v_fmac_f32_e32 v103, v106, v106
	v_fmac_f32_e32 v120, v108, v108
	v_add_f32_e32 v103, v103, v120
	v_mul_f32_e32 v120, v111, v111
	v_mul_f32_e32 v121, v113, v113
	v_fmac_f32_e32 v120, v110, v110
	v_fmac_f32_e32 v121, v112, v112
	v_add_f32_e32 v120, v120, v121
	v_add_f32_e32 v103, v103, v120
	v_add_f32_e32 v120, v102, v103
	v_mov_b32_e32 v121, v120
	s_nop 1
	v_permlane16_swap_b32_e32 v120, v121
	v_cvt_pk_bf16_f32 v102, v116, v117
	v_cvt_pk_bf16_f32 v103, v118, v119
	global_store_dwordx4 v[104:105], v[100:103], off
	s_waitcnt lgkmcnt(0)
	s_nop 0
	v_add_f32_e32 v100, v120, v121
	v_mov_b32_e32 v101, v100
	s_nop 1
	v_permlane32_swap_b32_e32 v100, v101
	v_cvt_pk_bf16_f32 v102, v106, v107
	v_cvt_pk_bf16_f32 v103, v108, v109
	v_cvt_pk_bf16_f32 v104, v110, v111
	v_cvt_pk_bf16_f32 v105, v112, v113
	global_store_dwordx4 v[114:115], v[102:105], off
	s_and_saveexec_b64 s[22:23], s[4:5]
	s_cbranch_execz .LBB0_2080
	s_waitcnt lgkmcnt(0)
	v_add_f32_e32 v100, v100, v101
	global_store_dword v[200:201], v100, off offset:1024
.LBB0_2080:
	s_or_b64 exec, exec, s[22:23]
	s_mov_b64 s[0:1], 0x10000
	s_waitcnt lgkmcnt(0)
	v_lshl_add_u64 v[100:101], v[198:199], 0, s[0:1]
	s_mov_b64 s[0:1], 0x10100
	v_lshl_add_u64 v[102:103], v[198:199], 0, s[0:1]
	s_mov_b32 s0, 0x3c800000
	s_waitcnt vmcnt(15)
	v_lshlrev_b32_e32 v104, 16, v174
	v_and_b32_e32 v105, 0xffff0000, v174
	v_lshlrev_b32_e32 v106, 16, v175
	v_and_b32_e32 v107, 0xffff0000, v175
	s_waitcnt vmcnt(14)
	v_lshlrev_b32_e32 v114, 16, v171
	v_and_b32_e32 v115, 0xffff0000, v171
	v_pk_fma_f32 v[84:85], v[84:85], s[0:1], 0 op_sel_hi:[1,0,0]
	v_pk_fma_f32 v[82:83], v[82:83], s[0:1], 0 op_sel_hi:[1,0,0]
	v_pk_fma_f32 v[68:69], v[68:69], s[0:1], 0 op_sel_hi:[1,0,0]
	v_lshlrev_b32_e32 v116, 16, v172
	v_and_b32_e32 v117, 0xffff0000, v172
	v_pk_add_f32 v[84:85], v[84:85], v[106:107]
	v_pk_add_f32 v[82:83], v[82:83], v[104:105]
	v_pk_add_f32 v[104:105], v[68:69], v[114:115]
	v_pk_fma_f32 v[68:69], v[70:71], s[0:1], 0 op_sel_hi:[1,0,0]
	v_lshlrev_b32_e32 v108, 16, v176
	v_and_b32_e32 v109, 0xffff0000, v176
	v_lshlrev_b32_e32 v110, 16, v177
	v_and_b32_e32 v111, 0xffff0000, v177
	v_lshlrev_b32_e32 v112, 16, v170
	v_and_b32_e32 v113, 0xffff0000, v170
	v_pk_fma_f32 v[88:89], v[88:89], s[0:1], 0 op_sel_hi:[1,0,0]
	v_pk_fma_f32 v[86:87], v[86:87], s[0:1], 0 op_sel_hi:[1,0,0]
	v_pk_fma_f32 v[66:67], v[66:67], s[0:1], 0 op_sel_hi:[1,0,0]
	v_pk_add_f32 v[70:71], v[68:69], v[116:117]
	v_mul_f32_e32 v68, v83, v83
	v_mul_f32_e32 v69, v85, v85
	v_lshlrev_b32_e32 v118, 16, v173
	v_and_b32_e32 v119, 0xffff0000, v173
	v_pk_add_f32 v[88:89], v[88:89], v[110:111]
	v_pk_add_f32 v[86:87], v[86:87], v[108:109]
	v_pk_add_f32 v[106:107], v[66:67], v[112:113]
	v_pk_fma_f32 v[66:67], v[72:73], s[0:1], 0 op_sel_hi:[1,0,0]
	v_fmac_f32_e32 v68, v82, v82
	v_fmac_f32_e32 v69, v84, v84
	v_pk_add_f32 v[72:73], v[66:67], v[118:119]
	v_cvt_pk_bf16_f32 v66, v82, v83
	v_add_f32_e32 v68, v68, v69
	v_mul_f32_e32 v69, v87, v87
	v_mul_f32_e32 v82, v89, v89
	v_fmac_f32_e32 v69, v86, v86
	v_fmac_f32_e32 v82, v88, v88
	v_add_f32_e32 v69, v69, v82
	v_add_f32_e32 v68, v68, v69
	v_mul_f32_e32 v69, v107, v107
	v_mul_f32_e32 v82, v105, v105
	v_fmac_f32_e32 v69, v106, v106
	v_fmac_f32_e32 v82, v104, v104
	v_add_f32_e32 v69, v69, v82
	v_mul_f32_e32 v82, v71, v71
	v_mul_f32_e32 v83, v73, v73
	v_fmac_f32_e32 v82, v70, v70
	v_fmac_f32_e32 v83, v72, v72
	v_add_f32_e32 v82, v82, v83
	v_add_f32_e32 v69, v69, v82
	v_add_f32_e32 v82, v68, v69
	v_mov_b32_e32 v83, v82
	s_nop 1
	v_permlane16_swap_b32_e32 v82, v83
	v_cvt_pk_bf16_f32 v67, v84, v85
	v_cvt_pk_bf16_f32 v68, v86, v87
	v_cvt_pk_bf16_f32 v69, v88, v89
	global_store_dwordx4 v[100:101], v[66:69], off
	s_waitcnt lgkmcnt(0)
	s_nop 0
	v_add_f32_e32 v66, v82, v83
	v_mov_b32_e32 v67, v66
	s_nop 1
	v_permlane32_swap_b32_e32 v66, v67
	v_cvt_pk_bf16_f32 v68, v106, v107
	v_cvt_pk_bf16_f32 v69, v104, v105
	v_cvt_pk_bf16_f32 v70, v70, v71
	v_cvt_pk_bf16_f32 v71, v72, v73
	global_store_dwordx4 v[102:103], v[68:71], off
	s_and_saveexec_b64 s[22:23], s[4:5]
	s_cbranch_execz .LBB0_2082
	s_waitcnt lgkmcnt(0)
	v_add_f32_e32 v66, v66, v67
	global_store_dword v[200:201], v66, off offset:2048
.LBB0_2082:
	s_or_b64 exec, exec, s[22:23]
	s_mov_b64 s[0:1], 0x18000
	v_lshl_add_u64 v[70:71], v[198:199], 0, s[0:1]
	s_mov_b64 s[0:1], 0x18100
	v_lshl_add_u64 v[72:73], v[198:199], 0, s[0:1]
	s_mov_b32 s0, 0x3c800000
	s_waitcnt vmcnt(15)
	v_lshlrev_b32_e32 v66, 16, v166
	s_waitcnt lgkmcnt(0)
	v_and_b32_e32 v67, 0xffff0000, v166
	v_pk_fma_f32 v[90:91], v[90:91], s[0:1], 0 op_sel_hi:[1,0,0]
	v_lshlrev_b32_e32 v84, 16, v169
	v_and_b32_e32 v85, 0xffff0000, v169
	v_pk_add_f32 v[90:91], v[90:91], v[66:67]
	v_pk_fma_f32 v[66:67], v[96:97], s[0:1], 0 op_sel_hi:[1,0,0]
	v_lshlrev_b32_e32 v68, 16, v167
	v_and_b32_e32 v69, 0xffff0000, v167
	s_waitcnt vmcnt(14)
	v_lshlrev_b32_e32 v88, 16, v163
	v_and_b32_e32 v89, 0xffff0000, v163
	v_pk_fma_f32 v[92:93], v[92:93], s[0:1], 0 op_sel_hi:[1,0,0]
	v_pk_add_f32 v[84:85], v[66:67], v[84:85]
	v_pk_fma_f32 v[66:67], v[76:77], s[0:1], 0 op_sel_hi:[1,0,0]
	v_lshlrev_b32_e32 v86, 16, v162
	v_and_b32_e32 v87, 0xffff0000, v162
	v_lshlrev_b32_e32 v102, 16, v165
	v_and_b32_e32 v103, 0xffff0000, v165
	v_pk_add_f32 v[68:69], v[92:93], v[68:69]
	v_pk_fma_f32 v[74:75], v[74:75], s[0:1], 0 op_sel_hi:[1,0,0]
	v_pk_add_f32 v[76:77], v[66:67], v[88:89]
	v_pk_fma_f32 v[66:67], v[80:81], s[0:1], 0 op_sel_hi:[1,0,0]
	v_lshlrev_b32_e32 v82, 16, v168
	v_and_b32_e32 v83, 0xffff0000, v168
	v_pk_fma_f32 v[92:93], v[94:95], s[0:1], 0 op_sel_hi:[1,0,0]
	v_pk_add_f32 v[74:75], v[74:75], v[86:87]
	v_pk_add_f32 v[80:81], v[66:67], v[102:103]
	v_cvt_pk_bf16_f32 v66, v90, v91
	v_cvt_pk_bf16_f32 v67, v68, v69
	v_mul_f32_e32 v86, v91, v91
	v_mul_f32_e32 v69, v69, v69
	v_pk_add_f32 v[82:83], v[92:93], v[82:83]
	v_fmac_f32_e32 v86, v90, v90
	v_fmac_f32_e32 v69, v68, v68
	v_add_f32_e32 v68, v86, v69
	v_mul_f32_e32 v69, v83, v83
	v_mul_f32_e32 v86, v85, v85
	v_fmac_f32_e32 v69, v82, v82
	v_fmac_f32_e32 v86, v84, v84
	v_add_f32_e32 v69, v69, v86
	v_lshlrev_b32_e32 v100, 16, v164
	v_and_b32_e32 v101, 0xffff0000, v164
	v_pk_fma_f32 v[78:79], v[78:79], s[0:1], 0 op_sel_hi:[1,0,0]
	v_add_f32_e32 v68, v68, v69
	v_mul_f32_e32 v69, v75, v75
	v_mul_f32_e32 v86, v77, v77
	v_pk_add_f32 v[78:79], v[78:79], v[100:101]
	v_fmac_f32_e32 v69, v74, v74
	v_fmac_f32_e32 v86, v76, v76
	v_add_f32_e32 v69, v69, v86
	v_mul_f32_e32 v86, v79, v79
	v_mul_f32_e32 v87, v81, v81
	v_fmac_f32_e32 v86, v78, v78
	v_fmac_f32_e32 v87, v80, v80
	v_add_f32_e32 v86, v86, v87
	v_add_f32_e32 v69, v69, v86
	v_add_f32_e32 v86, v68, v69
	v_mov_b32_e32 v87, v86
	s_nop 1
	v_permlane16_swap_b32_e32 v86, v87
	v_cvt_pk_bf16_f32 v68, v82, v83
	v_cvt_pk_bf16_f32 v69, v84, v85
	global_store_dwordx4 v[70:71], v[66:69], off
	s_waitcnt lgkmcnt(0)
	s_nop 0
	v_add_f32_e32 v66, v86, v87
	v_mov_b32_e32 v67, v66
	s_nop 1
	v_permlane32_swap_b32_e32 v66, v67
	v_cvt_pk_bf16_f32 v68, v74, v75
	v_cvt_pk_bf16_f32 v69, v76, v77
	v_cvt_pk_bf16_f32 v70, v78, v79
	v_cvt_pk_bf16_f32 v71, v80, v81
	global_store_dwordx4 v[72:73], v[68:71], off
	s_and_saveexec_b64 s[22:23], s[4:5]
	s_cbranch_execz .LBB0_2084
	s_waitcnt lgkmcnt(0)
	v_add_f32_e32 v66, v66, v67
	global_store_dword v[200:201], v66, off offset:3072
.LBB0_2084:
	s_or_b64 exec, exec, s[22:23]
	s_mov_b64 s[0:1], 0x40000
	s_waitcnt lgkmcnt(0)
	v_lshl_add_u64 v[66:67], v[198:199], 0, s[0:1]
	s_mov_b64 s[0:1], 0x40100
	v_lshl_add_u64 v[68:69], v[198:199], 0, s[0:1]
	s_mov_b32 s0, 0x3c800000
	s_waitcnt vmcnt(15)
	v_lshlrev_b32_e32 v70, 16, v158
	v_and_b32_e32 v71, 0xffff0000, v158
	v_lshlrev_b32_e32 v72, 16, v159
	v_and_b32_e32 v73, 0xffff0000, v159
	s_waitcnt vmcnt(14)
	v_lshlrev_b32_e32 v80, 16, v155
	v_and_b32_e32 v81, 0xffff0000, v155
	v_pk_fma_f32 v[52:53], v[52:53], s[0:1], 0 op_sel_hi:[1,0,0]
	v_pk_fma_f32 v[50:51], v[50:51], s[0:1], 0 op_sel_hi:[1,0,0]
	v_pk_fma_f32 v[36:37], v[36:37], s[0:1], 0 op_sel_hi:[1,0,0]
	v_lshlrev_b32_e32 v82, 16, v156
	v_and_b32_e32 v83, 0xffff0000, v156
	v_pk_add_f32 v[52:53], v[52:53], v[72:73]
	v_pk_add_f32 v[50:51], v[50:51], v[70:71]
	v_pk_add_f32 v[70:71], v[36:37], v[80:81]
	v_pk_fma_f32 v[36:37], v[38:39], s[0:1], 0 op_sel_hi:[1,0,0]
	v_lshlrev_b32_e32 v74, 16, v160
	v_and_b32_e32 v75, 0xffff0000, v160
	v_lshlrev_b32_e32 v76, 16, v161
	v_and_b32_e32 v77, 0xffff0000, v161
	v_lshlrev_b32_e32 v78, 16, v154
	v_and_b32_e32 v79, 0xffff0000, v154
	v_pk_fma_f32 v[56:57], v[56:57], s[0:1], 0 op_sel_hi:[1,0,0]
	v_pk_fma_f32 v[54:55], v[54:55], s[0:1], 0 op_sel_hi:[1,0,0]
	v_pk_fma_f32 v[34:35], v[34:35], s[0:1], 0 op_sel_hi:[1,0,0]
	v_pk_add_f32 v[38:39], v[36:37], v[82:83]
	v_mul_f32_e32 v36, v51, v51
	v_mul_f32_e32 v37, v53, v53
	v_lshlrev_b32_e32 v84, 16, v157
	v_and_b32_e32 v85, 0xffff0000, v157
	v_pk_add_f32 v[56:57], v[56:57], v[76:77]
	v_pk_add_f32 v[54:55], v[54:55], v[74:75]
	v_pk_add_f32 v[72:73], v[34:35], v[78:79]
	v_pk_fma_f32 v[34:35], v[40:41], s[0:1], 0 op_sel_hi:[1,0,0]
	v_fmac_f32_e32 v36, v50, v50
	v_fmac_f32_e32 v37, v52, v52
	v_pk_add_f32 v[40:41], v[34:35], v[84:85]
	v_cvt_pk_bf16_f32 v34, v50, v51
	v_add_f32_e32 v36, v36, v37
	v_mul_f32_e32 v37, v55, v55
	v_mul_f32_e32 v50, v57, v57
	v_fmac_f32_e32 v37, v54, v54
	v_fmac_f32_e32 v50, v56, v56
	v_add_f32_e32 v37, v37, v50
	v_add_f32_e32 v36, v36, v37
	v_mul_f32_e32 v37, v73, v73
	v_mul_f32_e32 v50, v71, v71
	v_fmac_f32_e32 v37, v72, v72
	v_fmac_f32_e32 v50, v70, v70
	v_add_f32_e32 v37, v37, v50
	v_mul_f32_e32 v50, v39, v39
	v_mul_f32_e32 v51, v41, v41
	v_fmac_f32_e32 v50, v38, v38
	v_fmac_f32_e32 v51, v40, v40
	v_add_f32_e32 v50, v50, v51
	v_add_f32_e32 v37, v37, v50
	v_add_f32_e32 v50, v36, v37
	v_mov_b32_e32 v51, v50
	s_nop 1
	v_permlane16_swap_b32_e32 v50, v51
	v_cvt_pk_bf16_f32 v35, v52, v53
	v_cvt_pk_bf16_f32 v36, v54, v55
	v_cvt_pk_bf16_f32 v37, v56, v57
	global_store_dwordx4 v[66:67], v[34:37], off
	s_waitcnt lgkmcnt(0)
	s_nop 0
	v_add_f32_e32 v34, v50, v51
	v_mov_b32_e32 v35, v34
	s_nop 1
	v_permlane32_swap_b32_e32 v34, v35
	v_cvt_pk_bf16_f32 v36, v72, v73
	v_cvt_pk_bf16_f32 v37, v70, v71
	v_cvt_pk_bf16_f32 v38, v38, v39
	v_cvt_pk_bf16_f32 v39, v40, v41
	global_store_dwordx4 v[68:69], v[36:39], off
	s_and_saveexec_b64 s[22:23], s[4:5]
	s_cbranch_execz .LBB0_2086
	s_waitcnt lgkmcnt(0)
	v_add_f32_e32 v36, v34, v35
	v_add_co_u32_e32 v34, vcc, 0x2000, v200
	s_nop 1
	v_addc_co_u32_e32 v35, vcc, 0, v201, vcc
	global_store_dword v[34:35], v36, off
.LBB0_2086:
	s_or_b64 exec, exec, s[22:23]
	s_mov_b64 s[0:1], 0x48000
	v_lshl_add_u64 v[38:39], v[198:199], 0, s[0:1]
	s_mov_b64 s[0:1], 0x48100
	v_lshl_add_u64 v[40:41], v[198:199], 0, s[0:1]
	s_mov_b32 s0, 0x3c800000
	s_waitcnt vmcnt(15)
	v_lshlrev_b32_e32 v34, 16, v150
	s_waitcnt lgkmcnt(0)
	v_and_b32_e32 v35, 0xffff0000, v150
	v_pk_fma_f32 v[58:59], v[58:59], s[0:1], 0 op_sel_hi:[1,0,0]
	v_lshlrev_b32_e32 v52, 16, v153
	v_and_b32_e32 v53, 0xffff0000, v153
	v_pk_add_f32 v[58:59], v[58:59], v[34:35]
	v_pk_fma_f32 v[34:35], v[64:65], s[0:1], 0 op_sel_hi:[1,0,0]
	v_lshlrev_b32_e32 v36, 16, v151
	v_and_b32_e32 v37, 0xffff0000, v151
	s_waitcnt vmcnt(14)
	v_lshlrev_b32_e32 v56, 16, v147
	v_and_b32_e32 v57, 0xffff0000, v147
	v_pk_fma_f32 v[60:61], v[60:61], s[0:1], 0 op_sel_hi:[1,0,0]
	v_pk_add_f32 v[52:53], v[34:35], v[52:53]
	v_pk_fma_f32 v[34:35], v[44:45], s[0:1], 0 op_sel_hi:[1,0,0]
	v_lshlrev_b32_e32 v54, 16, v146
	v_and_b32_e32 v55, 0xffff0000, v146
	v_lshlrev_b32_e32 v68, 16, v149
	v_and_b32_e32 v69, 0xffff0000, v149
	v_pk_add_f32 v[36:37], v[60:61], v[36:37]
	v_pk_fma_f32 v[42:43], v[42:43], s[0:1], 0 op_sel_hi:[1,0,0]
	v_pk_add_f32 v[44:45], v[34:35], v[56:57]
	v_pk_fma_f32 v[34:35], v[48:49], s[0:1], 0 op_sel_hi:[1,0,0]
	v_lshlrev_b32_e32 v50, 16, v152
	v_and_b32_e32 v51, 0xffff0000, v152
	v_pk_fma_f32 v[60:61], v[62:63], s[0:1], 0 op_sel_hi:[1,0,0]
	v_pk_add_f32 v[42:43], v[42:43], v[54:55]
	v_pk_add_f32 v[48:49], v[34:35], v[68:69]
	v_cvt_pk_bf16_f32 v34, v58, v59
	v_cvt_pk_bf16_f32 v35, v36, v37
	v_mul_f32_e32 v54, v59, v59
	v_mul_f32_e32 v37, v37, v37
	v_pk_add_f32 v[50:51], v[60:61], v[50:51]
	v_fmac_f32_e32 v54, v58, v58
	v_fmac_f32_e32 v37, v36, v36
	v_add_f32_e32 v36, v54, v37
	v_mul_f32_e32 v37, v51, v51
	v_mul_f32_e32 v54, v53, v53
	v_fmac_f32_e32 v37, v50, v50
	v_fmac_f32_e32 v54, v52, v52
	v_add_f32_e32 v37, v37, v54
	v_lshlrev_b32_e32 v66, 16, v148
	v_and_b32_e32 v67, 0xffff0000, v148
	v_pk_fma_f32 v[46:47], v[46:47], s[0:1], 0 op_sel_hi:[1,0,0]
	v_add_f32_e32 v36, v36, v37
	v_mul_f32_e32 v37, v43, v43
	v_mul_f32_e32 v54, v45, v45
	v_pk_add_f32 v[46:47], v[46:47], v[66:67]
	v_fmac_f32_e32 v37, v42, v42
	v_fmac_f32_e32 v54, v44, v44
	v_add_f32_e32 v37, v37, v54
	v_mul_f32_e32 v54, v47, v47
	v_mul_f32_e32 v55, v49, v49
	v_fmac_f32_e32 v54, v46, v46
	v_fmac_f32_e32 v55, v48, v48
	v_add_f32_e32 v54, v54, v55
	v_add_f32_e32 v37, v37, v54
	v_add_f32_e32 v54, v36, v37
	ds_bpermute_b32 v55, v98, v54
	v_cvt_pk_bf16_f32 v36, v50, v51
	v_cvt_pk_bf16_f32 v37, v52, v53
	global_store_dwordx4 v[38:39], v[34:37], off
	s_waitcnt lgkmcnt(0)
	s_nop 0
	v_add_f32_e32 v34, v54, v55
	v_mov_b32_e32 v35, v34
	s_nop 1
	v_permlane32_swap_b32_e32 v34, v35
	v_cvt_pk_bf16_f32 v36, v42, v43
	v_cvt_pk_bf16_f32 v37, v44, v45
	v_cvt_pk_bf16_f32 v38, v46, v47
	v_cvt_pk_bf16_f32 v39, v48, v49
	global_store_dwordx4 v[40:41], v[36:39], off
	s_and_saveexec_b64 s[22:23], s[4:5]
	s_cbranch_execz .LBB0_2088
	s_waitcnt lgkmcnt(0)
	v_add_f32_e32 v36, v34, v35
	v_add_co_u32_e32 v34, vcc, 0x2000, v200
	s_nop 1
	v_addc_co_u32_e32 v35, vcc, 0, v201, vcc
	global_store_dword v[34:35], v36, off offset:1024
.LBB0_2088:
	s_or_b64 exec, exec, s[22:23]
	s_mov_b64 s[0:1], 0x50000
	s_waitcnt lgkmcnt(0)
	v_lshl_add_u64 v[34:35], v[198:199], 0, s[0:1]
	s_mov_b64 s[0:1], 0x50100
	v_lshl_add_u64 v[36:37], v[198:199], 0, s[0:1]
	s_mov_b32 s0, 0x3c800000
	s_waitcnt vmcnt(15)
	v_lshlrev_b32_e32 v38, 16, v142
	v_and_b32_e32 v39, 0xffff0000, v142
	v_lshlrev_b32_e32 v40, 16, v143
	v_and_b32_e32 v41, 0xffff0000, v143
	s_waitcnt vmcnt(14)
	v_lshlrev_b32_e32 v48, 16, v139
	v_and_b32_e32 v49, 0xffff0000, v139
	v_pk_fma_f32 v[20:21], v[20:21], s[0:1], 0 op_sel_hi:[1,0,0]
	v_pk_fma_f32 v[18:19], v[18:19], s[0:1], 0 op_sel_hi:[1,0,0]
	v_pk_fma_f32 v[4:5], v[4:5], s[0:1], 0 op_sel_hi:[1,0,0]
	v_lshlrev_b32_e32 v50, 16, v140
	v_and_b32_e32 v51, 0xffff0000, v140
	v_pk_add_f32 v[20:21], v[20:21], v[40:41]
	v_pk_add_f32 v[18:19], v[18:19], v[38:39]
	v_pk_add_f32 v[38:39], v[4:5], v[48:49]
	v_pk_fma_f32 v[4:5], v[6:7], s[0:1], 0 op_sel_hi:[1,0,0]
	v_lshlrev_b32_e32 v42, 16, v144
	v_and_b32_e32 v43, 0xffff0000, v144
	v_lshlrev_b32_e32 v44, 16, v145
	v_and_b32_e32 v45, 0xffff0000, v145
	v_lshlrev_b32_e32 v46, 16, v138
	v_and_b32_e32 v47, 0xffff0000, v138
	v_pk_fma_f32 v[24:25], v[24:25], s[0:1], 0 op_sel_hi:[1,0,0]
	v_pk_fma_f32 v[22:23], v[22:23], s[0:1], 0 op_sel_hi:[1,0,0]
	v_pk_fma_f32 v[2:3], v[2:3], s[0:1], 0 op_sel_hi:[1,0,0]
	v_pk_add_f32 v[6:7], v[4:5], v[50:51]
	v_mul_f32_e32 v4, v19, v19
	v_mul_f32_e32 v5, v21, v21
	v_lshlrev_b32_e32 v52, 16, v141
	v_and_b32_e32 v53, 0xffff0000, v141
	v_pk_add_f32 v[24:25], v[24:25], v[44:45]
	v_pk_add_f32 v[22:23], v[22:23], v[42:43]
	v_pk_add_f32 v[40:41], v[2:3], v[46:47]
	v_pk_fma_f32 v[2:3], v[8:9], s[0:1], 0 op_sel_hi:[1,0,0]
	v_fmac_f32_e32 v4, v18, v18
	v_fmac_f32_e32 v5, v20, v20
	v_pk_add_f32 v[8:9], v[2:3], v[52:53]
	v_cvt_pk_bf16_f32 v2, v18, v19
	v_add_f32_e32 v4, v4, v5
	v_mul_f32_e32 v5, v23, v23
	v_mul_f32_e32 v18, v25, v25
	v_fmac_f32_e32 v5, v22, v22
	v_fmac_f32_e32 v18, v24, v24
	v_add_f32_e32 v5, v5, v18
	v_add_f32_e32 v4, v4, v5
	v_mul_f32_e32 v5, v41, v41
	v_mul_f32_e32 v18, v39, v39
	v_fmac_f32_e32 v5, v40, v40
	v_fmac_f32_e32 v18, v38, v38
	v_add_f32_e32 v5, v5, v18
	v_mul_f32_e32 v18, v7, v7
	v_mul_f32_e32 v19, v9, v9
	v_fmac_f32_e32 v18, v6, v6
	v_fmac_f32_e32 v19, v8, v8
	v_add_f32_e32 v18, v18, v19
	v_add_f32_e32 v5, v5, v18
	v_add_f32_e32 v18, v4, v5
	v_mov_b32_e32 v19, v18
	s_nop 1
	v_permlane16_swap_b32_e32 v18, v19
	v_cvt_pk_bf16_f32 v3, v20, v21
	v_cvt_pk_bf16_f32 v4, v22, v23
	v_cvt_pk_bf16_f32 v5, v24, v25
	global_store_dwordx4 v[34:35], v[2:5], off
	s_waitcnt lgkmcnt(0)
	s_nop 0
	v_add_f32_e32 v2, v18, v19
	v_mov_b32_e32 v3, v2
	s_nop 1
	v_permlane32_swap_b32_e32 v2, v3
	v_cvt_pk_bf16_f32 v4, v40, v41
	v_cvt_pk_bf16_f32 v5, v38, v39
	v_cvt_pk_bf16_f32 v6, v6, v7
	v_cvt_pk_bf16_f32 v7, v8, v9
	global_store_dwordx4 v[36:37], v[4:7], off
	s_and_saveexec_b64 s[22:23], s[4:5]
	s_cbranch_execz .LBB0_2090
	s_waitcnt lgkmcnt(0)
	v_add_f32_e32 v4, v2, v3
	v_add_co_u32_e32 v2, vcc, 0x2000, v200
	s_nop 1
	v_addc_co_u32_e32 v3, vcc, 0, v201, vcc
	global_store_dword v[2:3], v4, off offset:2048
.LBB0_2090:
	s_or_b64 exec, exec, s[22:23]
	s_mov_b64 s[0:1], 0x58000
	v_lshl_add_u64 v[6:7], v[198:199], 0, s[0:1]
	s_mov_b64 s[0:1], 0x58100
	v_lshl_add_u64 v[8:9], v[198:199], 0, s[0:1]
	s_mov_b32 s0, 0x3c800000
	s_waitcnt vmcnt(15)
	v_lshlrev_b32_e32 v2, 16, v134
	s_waitcnt lgkmcnt(0)
	v_and_b32_e32 v3, 0xffff0000, v134
	v_pk_fma_f32 v[26:27], v[26:27], s[0:1], 0 op_sel_hi:[1,0,0]
	v_lshlrev_b32_e32 v20, 16, v137
	v_and_b32_e32 v21, 0xffff0000, v137
	v_pk_add_f32 v[26:27], v[26:27], v[2:3]
	v_pk_fma_f32 v[2:3], v[32:33], s[0:1], 0 op_sel_hi:[1,0,0]
	v_lshlrev_b32_e32 v4, 16, v135
	v_and_b32_e32 v5, 0xffff0000, v135
	s_waitcnt vmcnt(14)
	v_lshlrev_b32_e32 v24, 16, v131
	v_and_b32_e32 v25, 0xffff0000, v131
	v_pk_fma_f32 v[28:29], v[28:29], s[0:1], 0 op_sel_hi:[1,0,0]
	v_pk_add_f32 v[20:21], v[2:3], v[20:21]
	v_pk_fma_f32 v[2:3], v[12:13], s[0:1], 0 op_sel_hi:[1,0,0]
	v_lshlrev_b32_e32 v22, 16, v130
	v_and_b32_e32 v23, 0xffff0000, v130
	v_lshlrev_b32_e32 v36, 16, v133
	v_and_b32_e32 v37, 0xffff0000, v133
	v_pk_add_f32 v[4:5], v[28:29], v[4:5]
	v_pk_fma_f32 v[10:11], v[10:11], s[0:1], 0 op_sel_hi:[1,0,0]
	v_pk_add_f32 v[12:13], v[2:3], v[24:25]
	v_pk_fma_f32 v[2:3], v[16:17], s[0:1], 0 op_sel_hi:[1,0,0]
	v_lshlrev_b32_e32 v18, 16, v136
	v_and_b32_e32 v19, 0xffff0000, v136
	v_pk_fma_f32 v[28:29], v[30:31], s[0:1], 0 op_sel_hi:[1,0,0]
	v_pk_add_f32 v[10:11], v[10:11], v[22:23]
	v_pk_add_f32 v[16:17], v[2:3], v[36:37]
	v_cvt_pk_bf16_f32 v2, v26, v27
	v_cvt_pk_bf16_f32 v3, v4, v5
	v_mul_f32_e32 v22, v27, v27
	v_mul_f32_e32 v5, v5, v5
	v_pk_add_f32 v[18:19], v[28:29], v[18:19]
	v_fmac_f32_e32 v22, v26, v26
	v_fmac_f32_e32 v5, v4, v4
	v_add_f32_e32 v4, v22, v5
	v_mul_f32_e32 v5, v19, v19
	v_mul_f32_e32 v22, v21, v21
	v_fmac_f32_e32 v5, v18, v18
	v_fmac_f32_e32 v22, v20, v20
	v_add_f32_e32 v5, v5, v22
	v_lshlrev_b32_e32 v34, 16, v132
	v_and_b32_e32 v35, 0xffff0000, v132
	v_pk_fma_f32 v[14:15], v[14:15], s[0:1], 0 op_sel_hi:[1,0,0]
	v_add_f32_e32 v4, v4, v5
	v_mul_f32_e32 v5, v11, v11
	v_mul_f32_e32 v22, v13, v13
	v_pk_add_f32 v[14:15], v[14:15], v[34:35]
	v_fmac_f32_e32 v5, v10, v10
	v_fmac_f32_e32 v22, v12, v12
	v_add_f32_e32 v5, v5, v22
	v_mul_f32_e32 v22, v15, v15
	v_mul_f32_e32 v23, v17, v17
	v_fmac_f32_e32 v22, v14, v14
	v_fmac_f32_e32 v23, v16, v16
	v_add_f32_e32 v22, v22, v23
	v_add_f32_e32 v5, v5, v22
	v_add_f32_e32 v22, v4, v5
	ds_bpermute_b32 v23, v98, v22
	v_cvt_pk_bf16_f32 v4, v18, v19
	v_cvt_pk_bf16_f32 v5, v20, v21
	global_store_dwordx4 v[6:7], v[2:5], off
	s_waitcnt lgkmcnt(0)
	s_nop 0
	v_add_f32_e32 v2, v22, v23
	v_mov_b32_e32 v3, v2
	s_nop 1
	v_permlane32_swap_b32_e32 v2, v3
	v_cvt_pk_bf16_f32 v4, v10, v11
	v_cvt_pk_bf16_f32 v5, v12, v13
	v_cvt_pk_bf16_f32 v6, v14, v15
	v_cvt_pk_bf16_f32 v7, v16, v17
	global_store_dwordx4 v[8:9], v[4:7], off
	s_and_saveexec_b64 s[22:23], s[4:5]
	s_cbranch_execz .LBB0_2092
	s_waitcnt lgkmcnt(0)
	v_add_f32_e32 v4, v2, v3
	v_add_co_u32_e32 v2, vcc, 0x2000, v200
	s_nop 1
	v_addc_co_u32_e32 v3, vcc, 0, v201, vcc
	global_store_dword v[2:3], v4, off offset:3072
